# plus nt on read-once f32 streams: x loads (P0), x1 loads (P7), P11 YB/out loads and final stores
# speedup vs baseline: 1.0298x; 1.0298x over previous
; DI void p0_prologue(Frame& F) {
;     ...
;     { float gvv[32];
; #pragma unroll
;       for (int i = 0; i < 32; ++i) { const int idx = F.tid + NTHR * i; gvv[i] = F.w_in[(size_t)(idx >> 3) * INW + NPROJ + (idx & 7)]; }
; #pragma unroll
;       for (int i = 0; i < 32; ++i) { const int idx = F.tid + NTHR * i; lg[(idx & 7) * DM + (idx >> 3)] = gvv[i]; } }
.LBB0_7:
	s_or_b64 exec, exec, s[0:1]
	s_lshr_b32 s0, s52, 6
	s_cmp_lt_i32 s86, 1
	v_writelane_b32 v254, s0, 23
	s_cselect_b64 s[0:1], -1, 0
	s_cmp_gt_i32 s87, 0
	s_cselect_b64 s[2:3], -1, 0
	s_and_b64 s[20:21], s[0:1], s[2:3]
	s_andn2_b64 vcc, exec, s[20:21]
	v_and_b32_e32 v224, 63, v0
	s_cbranch_vccnz .LBB0_46
	v_lshrrev_b32_e32 v18, 3, v0
	v_readlane_b32 s4, v254, 3
	v_and_b32_e32 v1, 7, v0
	v_mul_u32_u24_e32 v38, 0x6020, v18
	v_mov_b32_e32 v39, 0
	v_readlane_b32 s8, v254, 7
	v_readlane_b32 s9, v254, 8
	v_mov_b32_e32 v7, v39
	v_or_b32_e32 v10, 0x600, v0
	v_lshl_add_u64 v[2:3], s[8:9], 0, v[38:39]
	v_lshlrev_b32_e32 v38, 2, v1
	v_or_b32_e32 v1, 0x200, v0
	v_lshrrev_b32_e32 v1, 3, v1
	v_lshl_add_u64 v[2:3], v[2:3], 0, v[38:39]
	v_mul_u32_u24_e32 v6, 0x6020, v1
	v_add_co_u32_e32 v4, vcc, 0x6000, v2
	v_lshl_add_u64 v[6:7], s[8:9], 0, v[6:7]
	s_nop 0
	v_addc_co_u32_e32 v5, vcc, 0, v3, vcc
	v_lshl_add_u64 v[6:7], v[6:7], 0, v[38:39]
	v_add_co_u32_e32 v6, vcc, 0x6000, v6
	v_lshrrev_b32_e32 v19, 3, v10
	s_nop 0
	v_addc_co_u32_e32 v7, vcc, 0, v7, vcc
	v_mul_u32_u24_e32 v10, 0x6020, v19
	v_mov_b32_e32 v11, v39
	v_add_co_u32_e32 v8, vcc, 0x307000, v2
	v_lshl_add_u64 v[10:11], s[8:9], 0, v[10:11]
	s_movk_i32 s0, 0x6000
	v_addc_co_u32_e32 v9, vcc, 0, v3, vcc
	v_lshl_add_u64 v[10:11], v[10:11], 0, v[38:39]
	v_or_b32_e32 v14, 0xa00, v0
	v_add_co_u32_e32 v10, vcc, s0, v10
	v_lshrrev_b32_e32 v20, 3, v14
	s_nop 0
	v_addc_co_u32_e32 v11, vcc, 0, v11, vcc
	s_mov_b32 s2, 0x608000
	v_mul_u32_u24_e32 v14, 0x6020, v20
	v_mov_b32_e32 v15, v39
	v_add_co_u32_e32 v12, vcc, s2, v2
	v_lshl_add_u64 v[14:15], s[8:9], 0, v[14:15]
	s_nop 0
	v_addc_co_u32_e32 v13, vcc, 0, v3, vcc
	v_lshl_add_u64 v[14:15], v[14:15], 0, v[38:39]
	v_or_b32_e32 v16, 0xe00, v0
	v_add_co_u32_e32 v14, vcc, s0, v14
	v_lshrrev_b32_e32 v21, 3, v16
	s_nop 0
	v_addc_co_u32_e32 v15, vcc, 0, v15, vcc
	s_mov_b32 s2, 0x909000
	v_mul_u32_u24_e32 v16, 0x6020, v21
	v_mov_b32_e32 v17, v39
	v_add_co_u32_e32 v2, vcc, s2, v2
	v_lshl_add_u64 v[16:17], s[8:9], 0, v[16:17]
	s_nop 0
	v_addc_co_u32_e32 v3, vcc, 0, v3, vcc
	v_lshl_add_u64 v[16:17], v[16:17], 0, v[38:39]
	v_add_co_u32_e32 v16, vcc, s0, v16
	s_movk_i32 s1, 0x6020
	s_nop 0
	v_addc_co_u32_e32 v17, vcc, 0, v17, vcc
	global_load_dword v22, v[4:5], off
	global_load_dword v23, v[6:7], off
	global_load_dword v24, v[8:9], off
	global_load_dword v25, v[10:11], off
	global_load_dword v26, v[12:13], off
	global_load_dword v27, v[14:15], off
	global_load_dword v28, v[2:3], off
	global_load_dword v29, v[16:17], off
	v_mov_b32_e32 v2, 0xc04000
	v_mad_u32_u24 v2, v18, s1, v2
	v_mov_b32_e32 v3, v39
	v_or_b32_e32 v4, 0x1200, v0
	v_lshl_add_u64 v[2:3], s[8:9], 0, v[2:3]
	v_lshrrev_b32_e32 v30, 3, v4
	v_lshl_add_u64 v[2:3], v[2:3], 0, v[38:39]
	v_mul_u32_u24_e32 v4, 0x6020, v30
	v_mov_b32_e32 v5, v39
	v_add_co_u32_e32 v2, vcc, s0, v2
	v_lshl_add_u64 v[4:5], s[8:9], 0, v[4:5]
	v_mov_b32_e32 v6, 0xf05000
	v_addc_co_u32_e32 v3, vcc, 0, v3, vcc
	v_lshl_add_u64 v[4:5], v[4:5], 0, v[38:39]
	v_mad_u32_u24 v6, v18, s1, v6
	v_mov_b32_e32 v7, v39
	v_or_b32_e32 v8, 0x1600, v0
	v_add_co_u32_e32 v4, vcc, s0, v4
	v_lshl_add_u64 v[6:7], s[8:9], 0, v[6:7]
	v_lshrrev_b32_e32 v31, 3, v8
	v_addc_co_u32_e32 v5, vcc, 0, v5, vcc
	v_lshl_add_u64 v[6:7], v[6:7], 0, v[38:39]
	v_mul_u32_u24_e32 v8, 0x6020, v31
	v_mov_b32_e32 v9, v39
	v_add_co_u32_e32 v6, vcc, s0, v6
	v_lshl_add_u64 v[8:9], s[8:9], 0, v[8:9]
	v_mov_b32_e32 v10, 0x1206000
	v_addc_co_u32_e32 v7, vcc, 0, v7, vcc
	v_lshl_add_u64 v[8:9], v[8:9], 0, v[38:39]
	v_mad_u32_u24 v10, v18, s1, v10
	v_mov_b32_e32 v11, v39
	v_or_b32_e32 v12, 0x1a00, v0
	v_add_co_u32_e32 v8, vcc, s0, v8
	v_lshl_add_u64 v[10:11], s[8:9], 0, v[10:11]
	v_lshrrev_b32_e32 v32, 3, v12
	v_addc_co_u32_e32 v9, vcc, 0, v9, vcc
	v_lshl_add_u64 v[10:11], v[10:11], 0, v[38:39]
	v_mul_u32_u24_e32 v12, 0x6020, v32
	v_mov_b32_e32 v13, v39
	v_add_co_u32_e32 v10, vcc, s0, v10
	v_lshl_add_u64 v[12:13], s[8:9], 0, v[12:13]
	v_mov_b32_e32 v14, 0x1507000
	v_addc_co_u32_e32 v11, vcc, 0, v11, vcc
	v_lshl_add_u64 v[12:13], v[12:13], 0, v[38:39]
	v_mad_u32_u24 v14, v18, s1, v14
	v_mov_b32_e32 v15, v39
	v_or_b32_e32 v16, 0x1e00, v0
	v_add_co_u32_e32 v12, vcc, s0, v12
	v_lshl_add_u64 v[14:15], s[8:9], 0, v[14:15]
	v_lshrrev_b32_e32 v33, 3, v16
	v_addc_co_u32_e32 v13, vcc, 0, v13, vcc
	v_lshl_add_u64 v[14:15], v[14:15], 0, v[38:39]
	v_mul_u32_u24_e32 v16, 0x6020, v33
	v_mov_b32_e32 v17, v39
	v_add_co_u32_e32 v14, vcc, s0, v14
	v_lshl_add_u64 v[16:17], s[8:9], 0, v[16:17]
	s_nop 0
	v_addc_co_u32_e32 v15, vcc, 0, v15, vcc
	v_lshl_add_u64 v[16:17], v[16:17], 0, v[38:39]
	v_add_co_u32_e32 v16, vcc, s0, v16
	v_readlane_b32 s5, v254, 4
	s_nop 0
	v_addc_co_u32_e32 v17, vcc, 0, v17, vcc
	global_load_dword v34, v[2:3], off
	global_load_dword v35, v[4:5], off
	global_load_dword v36, v[6:7], off
	global_load_dword v37, v[8:9], off
	global_load_dword v40, v[10:11], off
	global_load_dword v41, v[12:13], off
	global_load_dword v42, v[14:15], off
	global_load_dword v43, v[16:17], off
	v_mov_b32_e32 v2, 0x1808000
	v_mad_u32_u24 v2, v18, s1, v2
	v_mov_b32_e32 v3, v39
	v_or_b32_e32 v4, 0x2200, v0
	v_lshl_add_u64 v[2:3], s[8:9], 0, v[2:3]
	v_lshrrev_b32_e32 v44, 3, v4
	v_lshl_add_u64 v[2:3], v[2:3], 0, v[38:39]
	v_mul_u32_u24_e32 v4, 0x6020, v44
	v_mov_b32_e32 v5, v39
	v_add_co_u32_e32 v2, vcc, s0, v2
	v_lshl_add_u64 v[4:5], s[8:9], 0, v[4:5]
	v_mov_b32_e32 v6, 0x1b09000
	v_addc_co_u32_e32 v3, vcc, 0, v3, vcc
	v_lshl_add_u64 v[4:5], v[4:5], 0, v[38:39]
	v_mad_u32_u24 v6, v18, s1, v6
	v_mov_b32_e32 v7, v39
	v_or_b32_e32 v8, 0x2600, v0
	v_add_co_u32_e32 v4, vcc, s0, v4
	v_lshl_add_u64 v[6:7], s[8:9], 0, v[6:7]
; DI void p0_prologue(Frame& F) {
;     ...
;       for (int i = 0; i < 32; ++i) { const int idx = F.tid + NTHR * i; gvv[i] = F.w_in[(size_t)(idx >> 3) * INW + NPROJ + (idx & 7)]; }
; #pragma unroll
;       for (int i = 0; i < 32; ++i) { const int idx = F.tid + NTHR * i; lg[(idx & 7) * DM + (idx >> 3)] = gvv[i]; } }
;     __syncthreads();
	v_lshrrev_b32_e32 v45, 3, v8
	v_addc_co_u32_e32 v5, vcc, 0, v5, vcc
	v_lshl_add_u64 v[6:7], v[6:7], 0, v[38:39]
	v_mul_u32_u24_e32 v8, 0x6020, v45
	v_mov_b32_e32 v9, v39
	v_add_co_u32_e32 v6, vcc, s0, v6
	v_lshl_add_u64 v[8:9], s[8:9], 0, v[8:9]
	v_mov_b32_e32 v10, 0x1e0a000
	v_addc_co_u32_e32 v7, vcc, 0, v7, vcc
	v_lshl_add_u64 v[8:9], v[8:9], 0, v[38:39]
	v_mad_u32_u24 v10, v18, s1, v10
	v_mov_b32_e32 v11, v39
	v_or_b32_e32 v12, 0x2a00, v0
	v_add_co_u32_e32 v8, vcc, s0, v8
	v_lshl_add_u64 v[10:11], s[8:9], 0, v[10:11]
	v_lshrrev_b32_e32 v46, 3, v12
	v_addc_co_u32_e32 v9, vcc, 0, v9, vcc
	v_lshl_add_u64 v[10:11], v[10:11], 0, v[38:39]
	v_mul_u32_u24_e32 v12, 0x6020, v46
	v_mov_b32_e32 v13, v39
	v_add_co_u32_e32 v10, vcc, s0, v10
	v_lshl_add_u64 v[12:13], s[8:9], 0, v[12:13]
	v_mov_b32_e32 v14, 0x210b000
	v_addc_co_u32_e32 v11, vcc, 0, v11, vcc
	v_lshl_add_u64 v[12:13], v[12:13], 0, v[38:39]
	v_mad_u32_u24 v14, v18, s1, v14
	v_mov_b32_e32 v15, v39
	v_or_b32_e32 v16, 0x2e00, v0
	v_add_co_u32_e32 v12, vcc, s0, v12
	v_lshl_add_u64 v[14:15], s[8:9], 0, v[14:15]
	v_lshrrev_b32_e32 v47, 3, v16
	v_addc_co_u32_e32 v13, vcc, 0, v13, vcc
	v_lshl_add_u64 v[14:15], v[14:15], 0, v[38:39]
	v_mul_u32_u24_e32 v16, 0x6020, v47
	v_mov_b32_e32 v17, v39
	v_add_co_u32_e32 v14, vcc, s0, v14
	v_lshl_add_u64 v[16:17], s[8:9], 0, v[16:17]
	s_nop 0
	v_addc_co_u32_e32 v15, vcc, 0, v15, vcc
	v_lshl_add_u64 v[16:17], v[16:17], 0, v[38:39]
	v_add_co_u32_e32 v16, vcc, s0, v16
	v_readlane_b32 s6, v254, 5
	s_nop 0
	v_addc_co_u32_e32 v17, vcc, 0, v17, vcc
	global_load_dword v48, v[2:3], off
	global_load_dword v49, v[4:5], off
	global_load_dword v50, v[6:7], off
	global_load_dword v51, v[8:9], off
	global_load_dword v52, v[10:11], off
	global_load_dword v53, v[12:13], off
	global_load_dword v54, v[14:15], off
	s_nop 0
	global_load_dword v16, v[16:17], off
	v_mov_b32_e32 v2, 0x240c000
	v_mad_u32_u24 v2, v18, s1, v2
	v_mov_b32_e32 v3, v39
	v_or_b32_e32 v4, 0x3200, v0
	v_lshl_add_u64 v[2:3], s[8:9], 0, v[2:3]
	v_lshrrev_b32_e32 v17, 3, v4
	v_lshl_add_u64 v[2:3], v[2:3], 0, v[38:39]
	v_mul_u32_u24_e32 v4, 0x6020, v17
	v_mov_b32_e32 v5, v39
	v_add_co_u32_e32 v2, vcc, s0, v2
	v_lshl_add_u64 v[4:5], s[8:9], 0, v[4:5]
	v_mov_b32_e32 v6, 0x270d000
	v_addc_co_u32_e32 v3, vcc, 0, v3, vcc
	v_lshl_add_u64 v[4:5], v[4:5], 0, v[38:39]
	v_mad_u32_u24 v6, v18, s1, v6
	v_mov_b32_e32 v7, v39
	v_or_b32_e32 v8, 0x3600, v0
	v_add_co_u32_e32 v4, vcc, s0, v4
	v_lshl_add_u64 v[6:7], s[8:9], 0, v[6:7]
	v_lshrrev_b32_e32 v55, 3, v8
	v_addc_co_u32_e32 v5, vcc, 0, v5, vcc
	v_lshl_add_u64 v[6:7], v[6:7], 0, v[38:39]
	v_mul_u32_u24_e32 v8, 0x6020, v55
	v_mov_b32_e32 v9, v39
	v_add_co_u32_e32 v6, vcc, s0, v6
	v_lshl_add_u64 v[8:9], s[8:9], 0, v[8:9]
	v_mov_b32_e32 v10, 0x2a0e000
	v_addc_co_u32_e32 v7, vcc, 0, v7, vcc
	v_lshl_add_u64 v[8:9], v[8:9], 0, v[38:39]
	v_mad_u32_u24 v10, v18, s1, v10
	v_mov_b32_e32 v11, v39
	v_or_b32_e32 v12, 0x3a00, v0
	v_add_co_u32_e32 v8, vcc, s0, v8
	v_lshl_add_u64 v[10:11], s[8:9], 0, v[10:11]
	v_lshrrev_b32_e32 v56, 3, v12
	v_addc_co_u32_e32 v9, vcc, 0, v9, vcc
	v_lshl_add_u64 v[10:11], v[10:11], 0, v[38:39]
	v_mul_u32_u24_e32 v12, 0x6020, v56
	v_mov_b32_e32 v13, v39
	v_add_co_u32_e32 v10, vcc, s0, v10
	v_lshl_add_u64 v[12:13], s[8:9], 0, v[12:13]
	v_mov_b32_e32 v14, 0x2d0f000
	v_addc_co_u32_e32 v11, vcc, 0, v11, vcc
	v_lshl_add_u64 v[12:13], v[12:13], 0, v[38:39]
	v_mad_u32_u24 v14, v18, s1, v14
	v_mov_b32_e32 v15, v39
	v_add_co_u32_e32 v12, vcc, s0, v12
	v_lshl_add_u64 v[14:15], s[8:9], 0, v[14:15]
	s_nop 0
	v_addc_co_u32_e32 v13, vcc, 0, v13, vcc
	v_lshl_add_u64 v[14:15], v[14:15], 0, v[38:39]
	v_add_co_u32_e32 v14, vcc, s0, v14
	v_readlane_b32 s1, v254, 23
	s_nop 0
	v_addc_co_u32_e32 v15, vcc, 0, v15, vcc
	global_load_dword v57, v[2:3], off
	s_nop 0
	global_load_dword v4, v[4:5], off
	s_nop 0
	global_load_dword v5, v[6:7], off
	s_nop 0
	global_load_dword v6, v[8:9], off
	global_load_dword v7, v[10:11], off
	s_nop 0
	global_load_dword v8, v[12:13], off
	global_load_dword v9, v[14:15], off
	v_or_b32_e32 v2, 0x3e00, v0
	v_lshrrev_b32_e32 v10, 3, v2
	v_mul_u32_u24_e32 v2, 0x6020, v10
	v_mov_b32_e32 v3, v39
	v_lshl_add_u64 v[2:3], s[8:9], 0, v[2:3]
	v_lshl_add_u64 v[2:3], v[2:3], 0, v[38:39]
	v_add_co_u32_e32 v2, vcc, s0, v2
	s_lshl_b32 s0, s85, 3
	s_nop 0
	v_addc_co_u32_e32 v3, vcc, 0, v3, vcc
	global_load_dword v2, v[2:3], off
	v_lshlrev_b32_e32 v3, 13, v0
	v_and_b32_e32 v3, 0xe000, v3
	v_add_u32_e32 v3, 0, v3
	v_lshl_add_u32 v11, v18, 2, v3
	v_lshl_add_u32 v1, v1, 2, v3
	s_waitcnt vmcnt(31)
	ds_write_b32 v11, v22
	s_waitcnt vmcnt(30)
	ds_write_b32 v1, v23
	s_waitcnt vmcnt(29)
	ds_write_b32 v11, v24 offset:512
	v_lshl_add_u32 v1, v19, 2, v3
	s_waitcnt vmcnt(28)
	ds_write_b32 v1, v25
	s_waitcnt vmcnt(27)
	ds_write_b32 v11, v26 offset:1024
	v_lshl_add_u32 v1, v20, 2, v3
	s_waitcnt vmcnt(26)
	ds_write_b32 v1, v27
	s_waitcnt vmcnt(25)
	ds_write_b32 v11, v28 offset:1536
	v_lshl_add_u32 v1, v21, 2, v3
	s_waitcnt vmcnt(24)
	ds_write_b32 v1, v29
	s_waitcnt vmcnt(23)
	ds_write_b32 v11, v34 offset:2048
	v_lshl_add_u32 v1, v30, 2, v3
	s_waitcnt vmcnt(22)
	ds_write_b32 v1, v35
	s_waitcnt vmcnt(21)
	ds_write_b32 v11, v36 offset:2560
	v_lshl_add_u32 v1, v31, 2, v3
	s_waitcnt vmcnt(20)
	ds_write_b32 v1, v37
	s_waitcnt vmcnt(19)
	ds_write_b32 v11, v40 offset:3072
	v_lshl_add_u32 v1, v32, 2, v3
	s_waitcnt vmcnt(18)
	ds_write_b32 v1, v41
	s_waitcnt vmcnt(17)
	ds_write_b32 v11, v42 offset:3584
	v_lshl_add_u32 v1, v33, 2, v3
	s_waitcnt vmcnt(16)
	ds_write_b32 v1, v43
	s_waitcnt vmcnt(15)
	ds_write_b32 v11, v48 offset:4096
	v_lshl_add_u32 v1, v44, 2, v3
	s_waitcnt vmcnt(14)
	ds_write_b32 v1, v49
	s_waitcnt vmcnt(13)
	ds_write_b32 v11, v50 offset:4608
	v_lshl_add_u32 v1, v45, 2, v3
	s_waitcnt vmcnt(12)
	ds_write_b32 v1, v51
	s_waitcnt vmcnt(11)
	ds_write_b32 v11, v52 offset:5120
	v_lshl_add_u32 v1, v46, 2, v3
	s_waitcnt vmcnt(10)
	ds_write_b32 v1, v53
	s_waitcnt vmcnt(9)
	ds_write_b32 v11, v54 offset:5632
	v_lshl_add_u32 v1, v47, 2, v3
	s_waitcnt vmcnt(8)
	ds_write_b32 v1, v16
	s_waitcnt vmcnt(7)
	ds_write_b32 v11, v57 offset:6144
	v_lshl_add_u32 v1, v17, 2, v3
	s_waitcnt vmcnt(6)
	ds_write_b32 v1, v4
	s_waitcnt vmcnt(5)
	ds_write_b32 v11, v5 offset:6656
	v_lshl_add_u32 v1, v55, 2, v3
	s_add_i32 s22, s0, s1
	s_waitcnt vmcnt(4)
	ds_write_b32 v1, v6
	s_waitcnt vmcnt(3)
	ds_write_b32 v11, v7 offset:7168
	v_lshl_add_u32 v1, v56, 2, v3
	v_readlane_b32 s0, v254, 2
	s_waitcnt vmcnt(2)
	ds_write_b32 v1, v8
	s_waitcnt vmcnt(1)
	ds_write_b32 v11, v9 offset:7680
	v_lshl_add_u32 v1, v10, 2, v3
	s_lshl_b32 s30, s0, 3
	s_cmpk_gt_i32 s22, 0x7fff
	v_readlane_b32 s7, v254, 6
	v_readlane_b32 s10, v254, 9
	v_readlane_b32 s11, v254, 10
	v_readlane_b32 s12, v254, 11
	v_readlane_b32 s13, v254, 12
	v_readlane_b32 s14, v254, 13
	s_waitcnt vmcnt(0)
	ds_write_b32 v1, v2
	v_and_b32_e32 v1, 3, v0
	v_readlane_b32 s15, v254, 14
	v_readlane_b32 s16, v254, 15
	v_readlane_b32 s17, v254, 16
	v_readlane_b32 s18, v254, 17
	v_readlane_b32 s19, v254, 18
	s_waitcnt lgkmcnt(0)
	s_barrier
; #define P0_XLOAD(dst, row_) do { const f32x4* xr_ = (const f32x4*)(F.x + (size_t)(row_) * DM) + F.lane; _Pragma("unroll") for (int j = 0; j < 8; ++j) dst[j] = xr_[64 * j]; } while (0)
; DI void p0_prologue(Frame& F) {
;     ...
;     { f32x4 va[8], vb[8], gnr[8];
; #pragma unroll
;       for (int j = 0; j < 8; ++j) gnr[j] = ((const f32x4*)F.attn_g)[F.lane + 64 * j];
;       const float gbias = (F.lane < 4) ? F.i_b[F.lane & 3] : F.f_b[(F.lane - 4) & 3];
;       int row = gw;
;       if (row < NTOK) P0_XLOAD(va, row);
	s_cbranch_scc1 .LBB0_17
	v_readlane_b32 s4, v254, 3
	v_lshlrev_b32_e32 v38, 4, v224
	v_readlane_b32 s6, v254, 5
	v_readlane_b32 s7, v254, 6
	v_readlane_b32 s19, v254, 18
	v_readlane_b32 s18, v254, 17
	v_lshl_add_u64 v[18:19], s[6:7], 0, v[38:39]
	v_add_co_u32_e32 v30, vcc, 0x1000, v18
	v_mov_b32_e32 v18, s61
	s_nop 0
	v_addc_co_u32_e32 v31, vcc, 0, v19, vcc
	v_mov_b32_e32 v19, s19
	v_cmp_gt_u32_e32 vcc, 4, v224
	s_ashr_i32 s23, s22, 31
	v_mov_b32_e32 v20, s18
	v_cndmask_b32_e32 v19, v18, v19, vcc
	v_mov_b32_e32 v18, s60
	s_lshl_b64 s[0:1], s[22:23], 13
	v_readlane_b32 s5, v254, 4
	v_cndmask_b32_e32 v18, v18, v20, vcc
	v_lshlrev_b32_e32 v20, 2, v1
	v_mov_b32_e32 v21, v39
	s_add_u32 s0, s4, s0
	v_lshl_add_u64 v[18:19], v[18:19], 0, v[20:21]
	s_addc_u32 s1, s5, s1
	global_load_dwordx4 v[2:5], v38, s[6:7]
	global_load_dwordx4 v[6:9], v38, s[6:7] offset:1024
	global_load_dwordx4 v[10:13], v38, s[6:7] offset:2048
	global_load_dwordx4 v[14:17], v38, s[6:7] offset:3072
	s_movk_i32 s31, 0x1000
	global_load_dword v107, v[18:19], off
	v_lshl_add_u64 v[18:19], s[0:1], 0, v[38:39]
	v_add_co_u32_e32 v34, vcc, s31, v18
	global_load_dwordx4 v[86:89], v38, s[0:1] nt
	global_load_dwordx4 v[78:81], v38, s[0:1] offset:1024 nt
	global_load_dwordx4 v[70:73], v38, s[0:1] offset:2048 nt
	global_load_dwordx4 v[62:65], v38, s[0:1] offset:3072 nt
	v_addc_co_u32_e32 v35, vcc, 0, v19, vcc
	global_load_dwordx4 v[18:21], v[30:31], off nt
	global_load_dwordx4 v[22:25], v[30:31], off offset:1024 nt
	global_load_dwordx4 v[26:29], v[30:31], off offset:2048 nt
	s_nop 0
	global_load_dwordx4 v[30:33], v[30:31], off offset:3072 nt
	s_nop 0
	global_load_dwordx4 v[58:61], v[34:35], off nt
	global_load_dwordx4 v[50:53], v[34:35], off offset:1024 nt
	global_load_dwordx4 v[42:45], v[34:35], off offset:2048 nt
	s_nop 0
	global_load_dwordx4 v[34:37], v[34:35], off offset:3072 nt
	v_mbcnt_lo_u32_b32 v40, -1, 0
	v_mbcnt_hi_u32_b32 v40, -1, v40
	v_and_b32_e32 v41, 64, v40
	v_add_u32_e32 v41, 64, v41
	v_xor_b32_e32 v46, 1, v40
	v_cmp_lt_i32_e32 vcc, v46, v41
	v_lshl_add_u64 v[98:99], s[4:5], 0, v[38:39]
	s_mov_b64 s[0:1], 0x34000000
	v_cndmask_b32_e32 v46, v40, v46, vcc
	v_lshlrev_b32_e32 v108, 2, v46
	v_xor_b32_e32 v46, 2, v40
	v_cmp_lt_i32_e32 vcc, v46, v41
	v_add_u32_e32 v114, 0, v38
	v_lshlrev_b32_e32 v38, 2, v224
	v_cndmask_b32_e32 v46, v40, v46, vcc
	v_lshlrev_b32_e32 v109, 2, v46
	v_xor_b32_e32 v46, 4, v40
	v_cmp_lt_i32_e32 vcc, v46, v41
	v_readlane_b32 s8, v254, 7
	v_readlane_b32 s9, v254, 8
	v_cndmask_b32_e32 v46, v40, v46, vcc
	v_lshlrev_b32_e32 v110, 2, v46
	v_xor_b32_e32 v46, 8, v40
	v_cmp_lt_i32_e32 vcc, v46, v41
	v_readlane_b32 s10, v254, 9
	v_readlane_b32 s11, v254, 10
	v_cndmask_b32_e32 v46, v40, v46, vcc
	v_lshlrev_b32_e32 v111, 2, v46
	v_xor_b32_e32 v46, 16, v40
	v_cmp_lt_i32_e32 vcc, v46, v41
	v_readlane_b32 s12, v254, 11
	v_readlane_b32 s13, v254, 12
	v_cndmask_b32_e32 v46, v40, v46, vcc
	v_lshlrev_b32_e32 v112, 2, v46
	v_xor_b32_e32 v46, 32, v40
	v_cmp_lt_i32_e32 vcc, v46, v41
	v_mov_b32_e32 v41, v39
	v_lshl_add_u64 v[38:39], s[94:95], 0, v[38:39]
	v_cndmask_b32_e32 v40, v40, v46, vcc
	v_lshlrev_b32_e32 v113, 2, v40
	v_lshlrev_b32_e32 v40, 3, v224
	v_lshl_add_u64 v[40:41], s[94:95], 0, v[40:41]
	v_lshl_add_u64 v[100:101], v[40:41], 0, s[0:1]
	s_mov_b64 s[0:1], 0x2300000
	v_readlane_b32 s14, v254, 13
	v_readlane_b32 s15, v254, 14
	v_readlane_b32 s16, v254, 15
	v_readlane_b32 s17, v254, 16
	v_lshl_add_u64 v[102:103], v[38:39], 0, s[0:1]
	v_readlane_b32 s0, v254, 2
	v_cmp_gt_u32_e64 s[2:3], 8, v224
	v_cmp_eq_u32_e64 s[4:5], 1, v224
	v_cmp_eq_u32_e64 s[6:7], 2, v224
	v_cmp_eq_u32_e64 s[8:9], 3, v224
	v_cmp_eq_u32_e64 s[10:11], 4, v224
	v_cmp_eq_u32_e64 s[12:13], 5, v224
	v_cmp_eq_u32_e64 s[14:15], 6, v224
	v_cmp_eq_u32_e64 s[16:17], 7, v224
	s_lshl_b32 s23, s0, 4
	v_mov_b32_e32 v115, 0x358637bd
	s_mov_b32 s34, 0xf800000
	v_mov_b32_e32 v116, 0x260
	s_mov_b32 s26, s22
	s_branch .LBB0_12

; #define P0_XLOAD(dst, row_) do { const f32x4* xr_ = (const f32x4*)(F.x + (size_t)(row_) * DM) + F.lane; _Pragma("unroll") for (int j = 0; j < 8; ++j) dst[j] = xr_[64 * j]; } while (0)
; DI void p0_prologue(Frame& F) {
;     ...
; #pragma unroll 1
;       for (; row < NTOK; row += 2 * NGW) {
;           const int row1 = row + NGW, row2 = row + 2 * NGW;
;           P0_XLOAD(vb, (row1 < NTOK ? row1 : NTOK - 1));
;           __builtin_amdgcn_sched_barrier(0);
;           P0_XROW(va, row);
.LBB0_12:
	s_add_i32 s24, s26, s30
	s_cmp_lt_i32 s24, 0x8000
	s_cselect_b64 s[28:29], -1, 0
	s_and_b64 s[0:1], s[28:29], exec
	s_cselect_b32 s0, s24, 0x7fff
	s_ashr_i32 s1, s0, 31
	s_lshl_b64 s[0:1], s[0:1], 13
	s_waitcnt vmcnt(16)
	v_lshl_add_u64 v[38:39], v[98:99], 0, s[0:1]
	global_load_dwordx4 v[94:97], v[38:39], off nt
	global_load_dwordx4 v[90:93], v[38:39], off offset:1024 nt
	global_load_dwordx4 v[82:85], v[38:39], off offset:2048 nt
	global_load_dwordx4 v[74:77], v[38:39], off offset:3072 nt
	v_add_co_u32_e32 v38, vcc, s31, v38
	s_nop 1
	v_addc_co_u32_e32 v39, vcc, 0, v39, vcc
	s_waitcnt lgkmcnt(0)
	global_load_dwordx4 v[66:69], v[38:39], off nt
	global_load_dwordx4 v[54:57], v[38:39], off offset:1024 nt
	global_load_dwordx4 v[46:49], v[38:39], off offset:2048 nt
	s_nop 0
	global_load_dwordx4 v[38:41], v[38:39], off offset:3072 nt
	s_waitcnt vmcnt(15)
	v_mov_b32_e32 v118, v87
	s_waitcnt vmcnt(14)
	v_mov_b32_e32 v119, v79
	v_mov_b32_e32 v104, v86
	v_mov_b32_e32 v105, v78
	v_pk_mul_f32 v[118:119], v[118:119], v[118:119]
	v_mov_b32_e32 v120, v89
	v_mov_b32_e32 v121, v81
	v_pk_fma_f32 v[104:105], v[104:105], v[104:105], v[118:119]
	v_mov_b32_e32 v118, v88
	v_mov_b32_e32 v119, v80
	v_pk_mul_f32 v[120:121], v[120:121], v[120:121]
	s_waitcnt vmcnt(11)
	v_mul_f32_e32 v106, v58, v58
	v_pk_fma_f32 v[118:119], v[118:119], v[118:119], v[120:121]
	v_pk_mul_f32 v[120:121], v[70:71], v[70:71]
	v_pk_add_f32 v[104:105], v[104:105], v[118:119]
	v_pk_mul_f32 v[118:119], v[72:73], v[72:73]
	v_mul_f32_e32 v117, v59, v59
	v_pk_mov_b32 v[122:123], v[120:121], v[118:119] op_sel:[1,0]
	v_mov_b32_e32 v121, v119
	v_pk_add_f32 v[118:119], v[122:123], v[120:121]
	v_pk_add_f32 v[104:105], v[104:105], v[104:105] op_sel:[0,1] op_sel_hi:[1,0]
	v_pk_add_f32 v[118:119], v[118:119], v[118:119] op_sel:[0,1] op_sel_hi:[1,0]
	v_mov_b32_e32 v105, v106
	v_mov_b32_e32 v119, v117
	v_mul_f32_e32 v106, v63, v63
	v_mul_f32_e32 v120, v60, v60
	v_pk_add_f32 v[104:105], v[104:105], v[118:119]
	v_pk_fma_f32 v[118:119], v[62:63], v[62:63], v[106:107] op_sel_hi:[1,1,0]
	v_mul_f32_e32 v106, v65, v65
	v_mul_f32_e32 v122, v61, v61
	v_mov_b32_e32 v119, v120
	v_pk_fma_f32 v[120:121], v[64:65], v[64:65], v[106:107] op_sel_hi:[1,1,0]
	s_waitcnt vmcnt(8)
	v_mul_f32_e32 v106, v34, v34
	v_mov_b32_e32 v121, v122
	v_pk_add_f32 v[118:119], v[118:119], v[120:121]
	v_pk_mul_f32 v[120:121], v[50:51], v[50:51]
	v_pk_add_f32 v[104:105], v[104:105], v[118:119]
	v_pk_mul_f32 v[118:119], v[52:53], v[52:53]
	v_mul_f32_e32 v117, v35, v35
	v_pk_mov_b32 v[122:123], v[120:121], v[118:119] op_sel:[1,0]
	v_mov_b32_e32 v121, v119
	v_pk_add_f32 v[118:119], v[122:123], v[120:121]
	v_pk_add_f32 v[104:105], v[104:105], v[104:105] op_sel:[0,1] op_sel_hi:[1,0]
	v_pk_add_f32 v[118:119], v[118:119], v[118:119] op_sel:[0,1] op_sel_hi:[1,0]
	v_mov_b32_e32 v105, v106
	v_mov_b32_e32 v119, v117
	v_mul_f32_e32 v106, v43, v43
	v_mul_f32_e32 v120, v36, v36
	v_pk_add_f32 v[104:105], v[104:105], v[118:119]
	v_pk_fma_f32 v[118:119], v[42:43], v[42:43], v[106:107] op_sel_hi:[1,1,0]
	v_mul_f32_e32 v106, v45, v45
	v_mul_f32_e32 v122, v37, v37
	v_mov_b32_e32 v119, v120
	v_pk_fma_f32 v[120:121], v[44:45], v[44:45], v[106:107] op_sel_hi:[1,1,0]
	s_ashr_i32 s27, s26, 31
	v_mov_b32_e32 v121, v122
	v_pk_add_f32 v[118:119], v[118:119], v[120:121]
	s_nop 0
	v_pk_add_f32 v[104:105], v[104:105], v[118:119]
	s_nop 0
	v_add_f32_e32 v104, v104, v105
	ds_bpermute_b32 v105, v108, v104
	s_waitcnt lgkmcnt(0)
	v_add_f32_e32 v104, v104, v105
	ds_bpermute_b32 v105, v109, v104
	s_waitcnt lgkmcnt(0)
	v_add_f32_e32 v104, v104, v105
	ds_bpermute_b32 v105, v110, v104
	s_waitcnt lgkmcnt(0)
	v_add_f32_e32 v104, v104, v105
	ds_bpermute_b32 v105, v111, v104
	s_waitcnt lgkmcnt(0)
	v_add_f32_e32 v104, v104, v105
	ds_bpermute_b32 v105, v112, v104
	s_waitcnt lgkmcnt(0)
	v_add_f32_e32 v104, v104, v105
	ds_bpermute_b32 v105, v113, v104
	s_waitcnt lgkmcnt(0)
	v_add_f32_e32 v104, v104, v105
	v_fmamk_f32 v104, v104, 0x3a000000, v115
	v_mul_f32_e32 v105, 0x4f800000, v104
	v_cmp_gt_f32_e32 vcc, s34, v104
	s_nop 1
	v_cndmask_b32_e32 v104, v104, v105, vcc
	v_sqrt_f32_e32 v105, v104
	s_nop 0
	v_add_u32_e32 v106, -1, v105
	v_fma_f32 v117, -v106, v105, v104
	v_cmp_ge_f32_e64 s[18:19], 0, v117
	v_add_u32_e32 v117, 1, v105
	s_nop 0
	v_cndmask_b32_e64 v106, v105, v106, s[18:19]
	v_fma_f32 v105, -v117, v105, v104
	v_cmp_lt_f32_e64 s[18:19], 0, v105
	s_nop 1
	v_cndmask_b32_e64 v105, v106, v117, s[18:19]
	v_mul_f32_e32 v106, 0x37800000, v105
	v_cndmask_b32_e32 v105, v105, v106, vcc
	v_cmp_class_f32_e32 vcc, v104, v116
	s_nop 1
	v_cndmask_b32_e32 v104, v105, v104, vcc
	v_div_scale_f32 v105, s[0:1], v104, v104, 1.0
	v_rcp_f32_e32 v106, v105
	s_lshl_b64 s[0:1], s[26:27], 12
	v_fma_f32 v117, -v105, v106, 1.0
	v_fmac_f32_e32 v106, v117, v106
	v_div_scale_f32 v117, vcc, 1.0, v104, 1.0
	v_mul_f32_e32 v118, v117, v106
	v_fma_f32 v119, -v105, v118, v117
	v_fmac_f32_e32 v118, v119, v106
	v_fma_f32 v105, -v105, v118, v117
	v_div_fmas_f32 v105, v105, v106, v118
	v_div_fixup_f32 v106, v105, v104, 1.0
	v_pk_mul_f32 v[86:87], v[86:87], v[106:107] op_sel_hi:[1,0]
	v_pk_mul_f32 v[88:89], v[88:89], v[106:107] op_sel_hi:[1,0]
	v_pk_mul_f32 v[124:125], v[2:3], v[86:87]
	v_pk_mul_f32 v[122:123], v[4:5], v[88:89]
	ds_read_b128 v[86:89], v114
	v_lshl_add_u64 v[104:105], v[100:101], 0, s[0:1]
	v_cvt_pk_bf16_f32 v118, v124, v125
	v_cvt_pk_bf16_f32 v119, v122, v123
	global_store_dwordx2 v[104:105], v[118:119], off
	ds_read_b128 v[118:121], v114 offset:8192
	s_waitcnt lgkmcnt(1)
	v_mul_f32_e32 v87, v87, v125
	v_fmac_f32_e32 v87, v86, v124
	v_mul_f32_e32 v86, v89, v123
	v_fmac_f32_e32 v86, v88, v122
	v_add_f32_e32 v86, v87, v86
	v_add_f32_e32 v117, 0, v86
	s_waitcnt lgkmcnt(0)
	v_mul_f32_e32 v119, v119, v125
	ds_read_b128 v[86:89], v114 offset:16384
	v_fmac_f32_e32 v119, v118, v124
	v_mul_f32_e32 v118, v121, v123
	v_fmac_f32_e32 v118, v120, v122
	v_add_f32_e32 v118, v119, v118
	v_add_f32_e32 v126, 0, v118
	ds_read_b128 v[118:121], v114 offset:24576
	s_waitcnt lgkmcnt(1)
	v_mul_f32_e32 v87, v87, v125
	v_fmac_f32_e32 v87, v86, v124
	v_mul_f32_e32 v86, v89, v123
	v_fmac_f32_e32 v86, v88, v122
	v_add_f32_e32 v86, v87, v86
	v_add_f32_e32 v127, 0, v86
	s_waitcnt lgkmcnt(0)
	v_mul_f32_e32 v119, v119, v125
	ds_read_b128 v[86:89], v114 offset:32768
	v_fmac_f32_e32 v119, v118, v124
	v_mul_f32_e32 v118, v121, v123
	v_fmac_f32_e32 v118, v120, v122
	v_add_f32_e32 v118, v119, v118
	v_add_f32_e32 v128, 0, v118
	ds_read_b128 v[118:121], v114 offset:40960
	s_waitcnt lgkmcnt(1)
	v_mul_f32_e32 v87, v87, v125
	v_fmac_f32_e32 v87, v86, v124
	v_mul_f32_e32 v86, v89, v123
	v_fmac_f32_e32 v86, v88, v122
	v_add_f32_e32 v86, v87, v86
	v_add_f32_e32 v129, 0, v86
	s_waitcnt lgkmcnt(0)
	v_mul_f32_e32 v119, v119, v125
	ds_read_b128 v[86:89], v114 offset:49152
	v_fmac_f32_e32 v119, v118, v124
	v_mul_f32_e32 v118, v121, v123
	v_fmac_f32_e32 v118, v120, v122
	v_add_f32_e32 v118, v119, v118
	v_add_f32_e32 v130, 0, v118
	ds_read_b128 v[118:121], v114 offset:57344
	s_waitcnt lgkmcnt(1)
	v_mul_f32_e32 v87, v87, v125
	v_fmac_f32_e32 v87, v86, v124
	v_mul_f32_e32 v86, v89, v123
	v_fmac_f32_e32 v86, v88, v122
	v_add_f32_e32 v86, v87, v86
	v_add_f32_e32 v131, 0, v86
	s_waitcnt lgkmcnt(0)
	v_mul_f32_e32 v86, v119, v125
	v_mul_f32_e32 v87, v121, v123
	v_fmac_f32_e32 v86, v118, v124
	v_fmac_f32_e32 v87, v120, v122
	v_add_f32_e32 v86, v86, v87
	v_add_f32_e32 v118, 0, v86
	v_pk_mul_f32 v[78:79], v[78:79], v[106:107] op_sel_hi:[1,0]
	v_pk_mul_f32 v[80:81], v[80:81], v[106:107] op_sel_hi:[1,0]
	v_pk_mul_f32 v[88:89], v[6:7], v[78:79]
	v_pk_mul_f32 v[86:87], v[8:9], v[80:81]
	v_cvt_pk_bf16_f32 v78, v88, v89
	v_cvt_pk_bf16_f32 v79, v86, v87
	global_store_dwordx2 v[104:105], v[78:79], off offset:512
	ds_read_b128 v[78:81], v114 offset:1024
	s_waitcnt lgkmcnt(0)
	v_mul_f32_e32 v79, v89, v79
	v_fmac_f32_e32 v79, v88, v78
	v_mul_f32_e32 v78, v87, v81
	v_fmac_f32_e32 v78, v86, v80
	v_add_f32_e32 v78, v79, v78
	v_add_f32_e32 v117, v117, v78
	ds_read_b128 v[78:81], v114 offset:9216
	s_waitcnt lgkmcnt(0)
	v_mul_f32_e32 v79, v89, v79
	v_fmac_f32_e32 v79, v88, v78
	v_mul_f32_e32 v78, v87, v81
	v_fmac_f32_e32 v78, v86, v80
	v_add_f32_e32 v78, v79, v78
	v_add_f32_e32 v119, v126, v78
	ds_read_b128 v[78:81], v114 offset:17408
	s_waitcnt lgkmcnt(0)
	v_mul_f32_e32 v79, v89, v79
	v_fmac_f32_e32 v79, v88, v78
	v_mul_f32_e32 v78, v87, v81
	v_fmac_f32_e32 v78, v86, v80
	v_add_f32_e32 v78, v79, v78
	v_add_f32_e32 v120, v127, v78
	ds_read_b128 v[78:81], v114 offset:25600
	s_waitcnt lgkmcnt(0)
	v_mul_f32_e32 v79, v89, v79
	v_fmac_f32_e32 v79, v88, v78
	v_mul_f32_e32 v78, v87, v81
	v_fmac_f32_e32 v78, v86, v80
	v_add_f32_e32 v78, v79, v78
	v_add_f32_e32 v121, v128, v78
	ds_read_b128 v[78:81], v114 offset:33792
	s_waitcnt lgkmcnt(0)
	v_mul_f32_e32 v79, v89, v79
	v_fmac_f32_e32 v79, v88, v78
	v_mul_f32_e32 v78, v87, v81
	v_fmac_f32_e32 v78, v86, v80
	v_add_f32_e32 v78, v79, v78
	v_add_f32_e32 v122, v129, v78
	ds_read_b128 v[78:81], v114 offset:41984
	s_waitcnt lgkmcnt(0)
	v_mul_f32_e32 v79, v89, v79
	v_fmac_f32_e32 v79, v88, v78
	v_mul_f32_e32 v78, v87, v81
	v_fmac_f32_e32 v78, v86, v80
	v_add_f32_e32 v78, v79, v78
	v_add_f32_e32 v123, v130, v78
	ds_read_b128 v[78:81], v114 offset:50176
	s_waitcnt lgkmcnt(0)
	v_mul_f32_e32 v79, v89, v79
	v_fmac_f32_e32 v79, v88, v78
	v_mul_f32_e32 v78, v87, v81
	v_fmac_f32_e32 v78, v86, v80
	v_add_f32_e32 v78, v79, v78
	v_add_f32_e32 v124, v131, v78
	ds_read_b128 v[78:81], v114 offset:58368
	s_waitcnt lgkmcnt(0)
	v_mul_f32_e32 v79, v89, v79
	v_fmac_f32_e32 v79, v88, v78
	v_mul_f32_e32 v78, v87, v81
	v_fmac_f32_e32 v78, v86, v80
	v_add_f32_e32 v78, v79, v78
	v_add_f32_e32 v118, v118, v78
	v_pk_mul_f32 v[70:71], v[70:71], v[106:107] op_sel_hi:[1,0]
	v_pk_mul_f32 v[72:73], v[72:73], v[106:107] op_sel_hi:[1,0]
	v_pk_mul_f32 v[88:89], v[10:11], v[70:71]
	v_pk_mul_f32 v[86:87], v[12:13], v[72:73]
	ds_read_b128 v[70:73], v114 offset:2048
	v_cvt_pk_bf16_f32 v78, v88, v89
	v_cvt_pk_bf16_f32 v79, v86, v87
	global_store_dwordx2 v[104:105], v[78:79], off offset:1024
	ds_read_b128 v[78:81], v114 offset:10240
	s_waitcnt lgkmcnt(1)
	v_mul_f32_e32 v71, v89, v71
	v_fmac_f32_e32 v71, v88, v70
	v_mul_f32_e32 v70, v87, v73
	v_fmac_f32_e32 v70, v86, v72
	v_add_f32_e32 v70, v71, v70
	v_add_f32_e32 v117, v117, v70
	s_waitcnt lgkmcnt(0)
	v_mul_f32_e32 v79, v89, v79
	ds_read_b128 v[70:73], v114 offset:18432
	v_fmac_f32_e32 v79, v88, v78
	v_mul_f32_e32 v78, v87, v81
	v_fmac_f32_e32 v78, v86, v80
	v_add_f32_e32 v78, v79, v78
	v_add_f32_e32 v119, v119, v78
	ds_read_b128 v[78:81], v114 offset:26624
	s_waitcnt lgkmcnt(1)
	v_mul_f32_e32 v71, v89, v71
	v_fmac_f32_e32 v71, v88, v70
	v_mul_f32_e32 v70, v87, v73
	v_fmac_f32_e32 v70, v86, v72
	v_add_f32_e32 v70, v71, v70
	v_add_f32_e32 v120, v120, v70
	s_waitcnt lgkmcnt(0)
	v_mul_f32_e32 v79, v89, v79
	ds_read_b128 v[70:73], v114 offset:34816
	v_fmac_f32_e32 v79, v88, v78
	v_mul_f32_e32 v78, v87, v81
	v_fmac_f32_e32 v78, v86, v80
	v_add_f32_e32 v78, v79, v78
	v_add_f32_e32 v121, v121, v78
	ds_read_b128 v[78:81], v114 offset:43008
	s_waitcnt lgkmcnt(1)
	v_mul_f32_e32 v71, v89, v71
	v_fmac_f32_e32 v71, v88, v70
	v_mul_f32_e32 v70, v87, v73
	v_fmac_f32_e32 v70, v86, v72
	v_add_f32_e32 v70, v71, v70
	v_add_f32_e32 v122, v122, v70
	s_waitcnt lgkmcnt(0)
	v_mul_f32_e32 v79, v89, v79
	ds_read_b128 v[70:73], v114 offset:51200
	v_fmac_f32_e32 v79, v88, v78
	v_mul_f32_e32 v78, v87, v81
	v_fmac_f32_e32 v78, v86, v80
	v_add_f32_e32 v78, v79, v78
	v_add_f32_e32 v123, v123, v78
	ds_read_b128 v[78:81], v114 offset:59392
	s_waitcnt lgkmcnt(1)
	v_mul_f32_e32 v71, v89, v71
	v_fmac_f32_e32 v71, v88, v70
	v_mul_f32_e32 v70, v87, v73
	v_fmac_f32_e32 v70, v86, v72
	v_add_f32_e32 v70, v71, v70
	v_add_f32_e32 v124, v124, v70
	s_waitcnt lgkmcnt(0)
	v_mul_f32_e32 v70, v89, v79
	v_mul_f32_e32 v71, v87, v81
	v_fmac_f32_e32 v70, v88, v78
	v_fmac_f32_e32 v71, v86, v80
	v_add_f32_e32 v70, v70, v71
	v_add_f32_e32 v86, v118, v70
	v_pk_mul_f32 v[62:63], v[62:63], v[106:107] op_sel_hi:[1,0]
	v_pk_mul_f32 v[64:65], v[64:65], v[106:107] op_sel_hi:[1,0]
	v_pk_mul_f32 v[80:81], v[14:15], v[62:63]
	v_pk_mul_f32 v[78:79], v[16:17], v[64:65]
	ds_read_b128 v[62:65], v114 offset:3072
	v_cvt_pk_bf16_f32 v70, v80, v81
	v_cvt_pk_bf16_f32 v71, v78, v79
	global_store_dwordx2 v[104:105], v[70:71], off offset:1536
	ds_read_b128 v[70:73], v114 offset:11264
	s_waitcnt lgkmcnt(1)
	v_mul_f32_e32 v63, v81, v63
	v_fmac_f32_e32 v63, v80, v62
	v_mul_f32_e32 v62, v79, v65
	v_fmac_f32_e32 v62, v78, v64
	v_add_f32_e32 v62, v63, v62
	v_add_f32_e32 v87, v117, v62
	s_waitcnt lgkmcnt(0)
	v_mul_f32_e32 v71, v81, v71
	ds_read_b128 v[62:65], v114 offset:19456
	v_fmac_f32_e32 v71, v80, v70
	v_mul_f32_e32 v70, v79, v73
	v_fmac_f32_e32 v70, v78, v72
	v_add_f32_e32 v70, v71, v70
	v_add_f32_e32 v88, v119, v70
	ds_read_b128 v[70:73], v114 offset:27648
	s_waitcnt lgkmcnt(1)
	v_mul_f32_e32 v63, v81, v63
	v_fmac_f32_e32 v63, v80, v62
	v_mul_f32_e32 v62, v79, v65
	v_fmac_f32_e32 v62, v78, v64
	v_add_f32_e32 v62, v63, v62
	v_add_f32_e32 v89, v120, v62
	s_waitcnt lgkmcnt(0)
	v_mul_f32_e32 v71, v81, v71
	ds_read_b128 v[62:65], v114 offset:35840
	v_fmac_f32_e32 v71, v80, v70
	v_mul_f32_e32 v70, v79, v73
	v_fmac_f32_e32 v70, v78, v72
	v_add_f32_e32 v70, v71, v70
	v_add_f32_e32 v117, v121, v70
	ds_read_b128 v[70:73], v114 offset:44032
	s_waitcnt lgkmcnt(1)
	v_mul_f32_e32 v63, v81, v63
	v_fmac_f32_e32 v63, v80, v62
	v_mul_f32_e32 v62, v79, v65
	v_fmac_f32_e32 v62, v78, v64
	v_add_f32_e32 v62, v63, v62
	v_add_f32_e32 v118, v122, v62
	s_waitcnt lgkmcnt(0)
	v_mul_f32_e32 v71, v81, v71
	ds_read_b128 v[62:65], v114 offset:52224
	v_fmac_f32_e32 v71, v80, v70
	v_mul_f32_e32 v70, v79, v73
	v_fmac_f32_e32 v70, v78, v72
	v_add_f32_e32 v70, v71, v70
	v_add_f32_e32 v119, v123, v70
	ds_read_b128 v[70:73], v114 offset:60416
	s_waitcnt lgkmcnt(1)
	v_mul_f32_e32 v63, v81, v63
	v_fmac_f32_e32 v63, v80, v62
	v_mul_f32_e32 v62, v79, v65
	v_fmac_f32_e32 v62, v78, v64
	v_add_f32_e32 v62, v63, v62
	v_add_f32_e32 v120, v124, v62
	s_waitcnt lgkmcnt(0)
	v_mul_f32_e32 v62, v81, v71
	v_mul_f32_e32 v63, v79, v73
	v_fmac_f32_e32 v62, v80, v70
	v_fmac_f32_e32 v63, v78, v72
	v_add_f32_e32 v62, v62, v63
	v_add_f32_e32 v78, v86, v62
	v_pk_mul_f32 v[58:59], v[58:59], v[106:107] op_sel_hi:[1,0]
	v_pk_mul_f32 v[60:61], v[60:61], v[106:107] op_sel_hi:[1,0]
	v_pk_mul_f32 v[72:73], v[18:19], v[58:59]
	v_pk_mul_f32 v[70:71], v[20:21], v[60:61]
	ds_read_b128 v[58:61], v114 offset:4096
	v_cvt_pk_bf16_f32 v62, v72, v73
	v_cvt_pk_bf16_f32 v63, v70, v71
	global_store_dwordx2 v[104:105], v[62:63], off offset:2048
	ds_read_b128 v[62:65], v114 offset:12288
	s_waitcnt lgkmcnt(1)
	v_mul_f32_e32 v59, v73, v59
	v_fmac_f32_e32 v59, v72, v58
	v_mul_f32_e32 v58, v71, v61
	v_fmac_f32_e32 v58, v70, v60
	v_add_f32_e32 v58, v59, v58
	v_add_f32_e32 v79, v87, v58
	s_waitcnt lgkmcnt(0)
	v_mul_f32_e32 v63, v73, v63
	ds_read_b128 v[58:61], v114 offset:20480
	v_fmac_f32_e32 v63, v72, v62
	v_mul_f32_e32 v62, v71, v65
	v_fmac_f32_e32 v62, v70, v64
	v_add_f32_e32 v62, v63, v62
	v_add_f32_e32 v80, v88, v62
	ds_read_b128 v[62:65], v114 offset:28672
	s_waitcnt lgkmcnt(1)
	v_mul_f32_e32 v59, v73, v59
	v_fmac_f32_e32 v59, v72, v58
	v_mul_f32_e32 v58, v71, v61
	v_fmac_f32_e32 v58, v70, v60
	v_add_f32_e32 v58, v59, v58
	v_add_f32_e32 v81, v89, v58
	s_waitcnt lgkmcnt(0)
	v_mul_f32_e32 v63, v73, v63
	ds_read_b128 v[58:61], v114 offset:36864
	v_fmac_f32_e32 v63, v72, v62
	v_mul_f32_e32 v62, v71, v65
	v_fmac_f32_e32 v62, v70, v64
	v_add_f32_e32 v62, v63, v62
	v_add_f32_e32 v86, v117, v62
	ds_read_b128 v[62:65], v114 offset:45056
	s_waitcnt lgkmcnt(1)
	v_mul_f32_e32 v59, v73, v59
	v_fmac_f32_e32 v59, v72, v58
	v_mul_f32_e32 v58, v71, v61
	v_fmac_f32_e32 v58, v70, v60
	v_add_f32_e32 v58, v59, v58
	v_add_f32_e32 v87, v118, v58
	s_waitcnt lgkmcnt(0)
	v_mul_f32_e32 v63, v73, v63
	ds_read_b128 v[58:61], v114 offset:53248
	v_fmac_f32_e32 v63, v72, v62
	v_mul_f32_e32 v62, v71, v65
	v_fmac_f32_e32 v62, v70, v64
	v_add_f32_e32 v62, v63, v62
	v_add_f32_e32 v88, v119, v62
	ds_read_b128 v[62:65], v114 offset:61440
	s_waitcnt lgkmcnt(1)
	v_mul_f32_e32 v59, v73, v59
	v_fmac_f32_e32 v59, v72, v58
	v_mul_f32_e32 v58, v71, v61
	v_fmac_f32_e32 v58, v70, v60
	v_add_f32_e32 v58, v59, v58
	v_add_f32_e32 v89, v120, v58
	s_waitcnt lgkmcnt(0)
	v_mul_f32_e32 v58, v73, v63
	v_mul_f32_e32 v59, v71, v65
	v_fmac_f32_e32 v58, v72, v62
	v_fmac_f32_e32 v59, v70, v64
	v_add_f32_e32 v58, v58, v59
	v_add_f32_e32 v70, v78, v58
	v_pk_mul_f32 v[50:51], v[50:51], v[106:107] op_sel_hi:[1,0]
	v_pk_mul_f32 v[52:53], v[52:53], v[106:107] op_sel_hi:[1,0]
	v_pk_mul_f32 v[64:65], v[22:23], v[50:51]
	v_pk_mul_f32 v[62:63], v[24:25], v[52:53]
	ds_read_b128 v[50:53], v114 offset:5120
	v_cvt_pk_bf16_f32 v58, v64, v65
	v_cvt_pk_bf16_f32 v59, v62, v63
	global_store_dwordx2 v[104:105], v[58:59], off offset:2560
	ds_read_b128 v[58:61], v114 offset:13312
	s_waitcnt lgkmcnt(1)
	v_mul_f32_e32 v51, v65, v51
	v_fmac_f32_e32 v51, v64, v50
	v_mul_f32_e32 v50, v63, v53
	v_fmac_f32_e32 v50, v62, v52
	v_add_f32_e32 v50, v51, v50
	v_add_f32_e32 v71, v79, v50
	s_waitcnt lgkmcnt(0)
	v_mul_f32_e32 v59, v65, v59
	ds_read_b128 v[50:53], v114 offset:21504
	v_fmac_f32_e32 v59, v64, v58
	v_mul_f32_e32 v58, v63, v61
	v_fmac_f32_e32 v58, v62, v60
	v_add_f32_e32 v58, v59, v58
	v_add_f32_e32 v72, v80, v58
	ds_read_b128 v[58:61], v114 offset:29696
	s_waitcnt lgkmcnt(1)
	v_mul_f32_e32 v51, v65, v51
	v_fmac_f32_e32 v51, v64, v50
	v_mul_f32_e32 v50, v63, v53
	v_fmac_f32_e32 v50, v62, v52
	v_add_f32_e32 v50, v51, v50
	v_add_f32_e32 v73, v81, v50
	s_waitcnt lgkmcnt(0)
	v_mul_f32_e32 v59, v65, v59
	ds_read_b128 v[50:53], v114 offset:37888
	v_fmac_f32_e32 v59, v64, v58
	v_mul_f32_e32 v58, v63, v61
	v_fmac_f32_e32 v58, v62, v60
	v_add_f32_e32 v58, v59, v58
	v_add_f32_e32 v78, v86, v58
	ds_read_b128 v[58:61], v114 offset:46080
	s_waitcnt lgkmcnt(1)
	v_mul_f32_e32 v51, v65, v51
	v_fmac_f32_e32 v51, v64, v50
	v_mul_f32_e32 v50, v63, v53
	v_fmac_f32_e32 v50, v62, v52
	v_add_f32_e32 v50, v51, v50
	v_add_f32_e32 v79, v87, v50
	s_waitcnt lgkmcnt(0)
	v_mul_f32_e32 v59, v65, v59
	ds_read_b128 v[50:53], v114 offset:54272
	v_fmac_f32_e32 v59, v64, v58
	v_mul_f32_e32 v58, v63, v61
	v_fmac_f32_e32 v58, v62, v60
	v_add_f32_e32 v58, v59, v58
	v_add_f32_e32 v80, v88, v58
	ds_read_b128 v[58:61], v114 offset:62464
	s_waitcnt lgkmcnt(1)
	v_mul_f32_e32 v51, v65, v51
	v_fmac_f32_e32 v51, v64, v50
	v_mul_f32_e32 v50, v63, v53
	v_fmac_f32_e32 v50, v62, v52
	v_add_f32_e32 v50, v51, v50
	v_add_f32_e32 v81, v89, v50
	s_waitcnt lgkmcnt(0)
	v_mul_f32_e32 v50, v65, v59
	v_mul_f32_e32 v51, v63, v61
	v_fmac_f32_e32 v50, v64, v58
	v_fmac_f32_e32 v51, v62, v60
	v_add_f32_e32 v50, v50, v51
	v_add_f32_e32 v62, v70, v50
	v_pk_mul_f32 v[42:43], v[42:43], v[106:107] op_sel_hi:[1,0]
	v_pk_mul_f32 v[44:45], v[44:45], v[106:107] op_sel_hi:[1,0]
	v_pk_mul_f32 v[60:61], v[26:27], v[42:43]
	v_pk_mul_f32 v[58:59], v[28:29], v[44:45]
	ds_read_b128 v[42:45], v114 offset:6144
	v_cvt_pk_bf16_f32 v50, v60, v61
	v_cvt_pk_bf16_f32 v51, v58, v59
	global_store_dwordx2 v[104:105], v[50:51], off offset:3072
	ds_read_b128 v[50:53], v114 offset:14336
	s_waitcnt lgkmcnt(1)
	v_mul_f32_e32 v43, v61, v43
	v_fmac_f32_e32 v43, v60, v42
	v_mul_f32_e32 v42, v59, v45
	v_fmac_f32_e32 v42, v58, v44
	v_add_f32_e32 v42, v43, v42
	v_add_f32_e32 v63, v71, v42
	s_waitcnt lgkmcnt(0)
	v_mul_f32_e32 v51, v61, v51
	ds_read_b128 v[42:45], v114 offset:22528
	v_fmac_f32_e32 v51, v60, v50
	v_mul_f32_e32 v50, v59, v53
	v_fmac_f32_e32 v50, v58, v52
	v_add_f32_e32 v50, v51, v50
	v_add_f32_e32 v64, v72, v50
	ds_read_b128 v[50:53], v114 offset:30720
	s_waitcnt lgkmcnt(1)
	v_mul_f32_e32 v43, v61, v43
	v_fmac_f32_e32 v43, v60, v42
	v_mul_f32_e32 v42, v59, v45
	v_fmac_f32_e32 v42, v58, v44
	v_add_f32_e32 v42, v43, v42
	v_add_f32_e32 v65, v73, v42
	s_waitcnt lgkmcnt(0)
	v_mul_f32_e32 v51, v61, v51
	ds_read_b128 v[42:45], v114 offset:38912
	v_fmac_f32_e32 v51, v60, v50
	v_mul_f32_e32 v50, v59, v53
	v_fmac_f32_e32 v50, v58, v52
	v_add_f32_e32 v50, v51, v50
	v_add_f32_e32 v70, v78, v50
	ds_read_b128 v[50:53], v114 offset:47104
	s_waitcnt lgkmcnt(1)
	v_mul_f32_e32 v43, v61, v43
	v_fmac_f32_e32 v43, v60, v42
	v_mul_f32_e32 v42, v59, v45
	v_fmac_f32_e32 v42, v58, v44
	v_add_f32_e32 v42, v43, v42
	v_add_f32_e32 v71, v79, v42
	s_waitcnt lgkmcnt(0)
	v_mul_f32_e32 v51, v61, v51
	ds_read_b128 v[42:45], v114 offset:55296
	v_fmac_f32_e32 v51, v60, v50
	v_mul_f32_e32 v50, v59, v53
	v_fmac_f32_e32 v50, v58, v52
	v_add_f32_e32 v50, v51, v50
	v_add_f32_e32 v72, v80, v50
	ds_read_b128 v[50:53], v114 offset:63488
	s_waitcnt lgkmcnt(1)
	v_mul_f32_e32 v43, v61, v43
	v_fmac_f32_e32 v43, v60, v42
	v_mul_f32_e32 v42, v59, v45
	v_fmac_f32_e32 v42, v58, v44
	v_add_f32_e32 v42, v43, v42
	v_add_f32_e32 v73, v81, v42
	s_waitcnt lgkmcnt(0)
	v_mul_f32_e32 v42, v61, v51
	v_mul_f32_e32 v43, v59, v53
	v_fmac_f32_e32 v42, v60, v50
	v_fmac_f32_e32 v43, v58, v52
	v_add_f32_e32 v42, v42, v43
	v_add_f32_e32 v58, v62, v42
	v_pk_mul_f32 v[34:35], v[34:35], v[106:107] op_sel_hi:[1,0]
	v_pk_mul_f32 v[36:37], v[36:37], v[106:107] op_sel_hi:[1,0]
	v_pk_mul_f32 v[52:53], v[30:31], v[34:35]
	v_pk_mul_f32 v[50:51], v[32:33], v[36:37]
	ds_read_b128 v[34:37], v114 offset:7168
	v_cvt_pk_bf16_f32 v42, v52, v53
	v_cvt_pk_bf16_f32 v43, v50, v51
	global_store_dwordx2 v[104:105], v[42:43], off offset:3584
	ds_read_b128 v[42:45], v114 offset:15360
	s_waitcnt lgkmcnt(1)
	v_mul_f32_e32 v35, v53, v35
	v_fmac_f32_e32 v35, v52, v34
	v_mul_f32_e32 v34, v51, v37
	v_fmac_f32_e32 v34, v50, v36
	v_add_f32_e32 v34, v35, v34
	v_add_f32_e32 v59, v63, v34
	s_waitcnt lgkmcnt(0)
	v_mul_f32_e32 v43, v53, v43
	ds_read_b128 v[34:37], v114 offset:23552
	v_fmac_f32_e32 v43, v52, v42
	v_mul_f32_e32 v42, v51, v45
	v_fmac_f32_e32 v42, v50, v44
	v_add_f32_e32 v42, v43, v42
	v_add_f32_e32 v60, v64, v42
	ds_read_b128 v[42:45], v114 offset:31744
	s_waitcnt lgkmcnt(1)
	v_mul_f32_e32 v35, v53, v35
	v_fmac_f32_e32 v35, v52, v34
	v_mul_f32_e32 v34, v51, v37
	v_fmac_f32_e32 v34, v50, v36
	v_add_f32_e32 v34, v35, v34
	v_add_f32_e32 v61, v65, v34
	s_waitcnt lgkmcnt(0)
	v_mul_f32_e32 v43, v53, v43
	ds_read_b128 v[34:37], v114 offset:39936
	v_fmac_f32_e32 v43, v52, v42
	v_mul_f32_e32 v42, v51, v45
	v_fmac_f32_e32 v42, v50, v44
	v_add_f32_e32 v42, v43, v42
	v_add_f32_e32 v62, v70, v42
	ds_read_b128 v[42:45], v114 offset:48128
	s_waitcnt lgkmcnt(1)
	v_mul_f32_e32 v35, v53, v35
	v_fmac_f32_e32 v35, v52, v34
	v_mul_f32_e32 v34, v51, v37
	v_fmac_f32_e32 v34, v50, v36
	v_add_f32_e32 v34, v35, v34
	v_add_f32_e32 v63, v71, v34
	s_waitcnt lgkmcnt(0)
	v_mul_f32_e32 v43, v53, v43
	ds_read_b128 v[34:37], v114 offset:56320
	v_fmac_f32_e32 v43, v52, v42
	v_mul_f32_e32 v42, v51, v45
	v_fmac_f32_e32 v42, v50, v44
	v_add_f32_e32 v42, v43, v42
	v_add_f32_e32 v64, v72, v42
	ds_read_b128 v[42:45], v114 offset:64512
	s_waitcnt lgkmcnt(1)
	v_mul_f32_e32 v35, v53, v35
	v_fmac_f32_e32 v35, v52, v34
	v_mul_f32_e32 v34, v51, v37
	v_fmac_f32_e32 v34, v50, v36
	v_add_f32_e32 v34, v35, v34
	v_add_f32_e32 v65, v73, v34
	s_waitcnt lgkmcnt(0)
	v_mul_f32_e32 v34, v53, v43
	v_mul_f32_e32 v35, v51, v45
	v_fmac_f32_e32 v34, v52, v42
	v_fmac_f32_e32 v35, v50, v44
	v_add_f32_e32 v34, v34, v35
	v_add_f32_e32 v52, v58, v34
	ds_bpermute_b32 v34, v108, v59
	ds_bpermute_b32 v35, v108, v60
	ds_bpermute_b32 v36, v108, v61
	ds_bpermute_b32 v37, v108, v62
	ds_bpermute_b32 v42, v108, v63
	s_waitcnt lgkmcnt(4)
	v_add_f32_e32 v34, v59, v34
	ds_bpermute_b32 v43, v109, v34
	s_waitcnt lgkmcnt(4)
	v_add_f32_e32 v35, v60, v35
	ds_bpermute_b32 v44, v109, v35
	s_waitcnt lgkmcnt(4)
	v_add_f32_e32 v36, v61, v36
	ds_bpermute_b32 v45, v109, v36
	s_waitcnt lgkmcnt(2)
	v_add_f32_e32 v34, v34, v43
	ds_bpermute_b32 v43, v110, v34
	s_waitcnt lgkmcnt(2)
	v_add_f32_e32 v35, v35, v44
	ds_bpermute_b32 v44, v110, v35
	v_add_f32_e32 v37, v62, v37
	v_add_f32_e32 v42, v63, v42
	s_waitcnt lgkmcnt(1)
	v_add_f32_e32 v34, v34, v43
	ds_bpermute_b32 v43, v111, v34
	v_add_f32_e32 v36, v36, v45
	s_waitcnt lgkmcnt(1)
	v_add_f32_e32 v35, v35, v44
	ds_bpermute_b32 v45, v110, v36
	ds_bpermute_b32 v44, v111, v35
	s_waitcnt lgkmcnt(2)
	v_add_f32_e32 v34, v34, v43
	ds_bpermute_b32 v43, v112, v34
	ds_bpermute_b32 v50, v109, v37
	s_waitcnt lgkmcnt(3)
	v_add_f32_e32 v45, v36, v45
	s_waitcnt lgkmcnt(2)
	v_add_f32_e32 v36, v35, v44
	ds_bpermute_b32 v44, v112, v36
	s_waitcnt lgkmcnt(2)
	v_add_f32_e32 v34, v34, v43
	ds_bpermute_b32 v43, v109, v42
	s_waitcnt lgkmcnt(2)
	v_add_f32_e32 v37, v37, v50
	ds_bpermute_b32 v51, v111, v45
	ds_bpermute_b32 v50, v110, v37
	s_waitcnt lgkmcnt(3)
	v_add_f32_e32 v36, v36, v44
	s_waitcnt lgkmcnt(2)
	v_add_f32_e32 v42, v42, v43
	ds_bpermute_b32 v43, v110, v42
	s_waitcnt lgkmcnt(2)
	v_add_f32_e32 v44, v45, v51
	s_waitcnt lgkmcnt(1)
	v_add_f32_e32 v45, v37, v50
	ds_bpermute_b32 v50, v111, v45
	ds_bpermute_b32 v51, v112, v44
	s_waitcnt lgkmcnt(2)
	v_add_f32_e32 v43, v42, v43
	ds_bpermute_b32 v53, v111, v43
	ds_bpermute_b32 v58, v108, v64
	s_waitcnt lgkmcnt(3)
	v_add_f32_e32 v45, v45, v50
	s_waitcnt lgkmcnt(2)
	v_add_f32_e32 v42, v44, v51
	ds_bpermute_b32 v50, v112, v45
	s_waitcnt lgkmcnt(2)
	v_add_f32_e32 v51, v43, v53
	ds_bpermute_b32 v53, v112, v51
	ds_bpermute_b32 v59, v108, v52
	s_waitcnt lgkmcnt(3)
	v_add_f32_e32 v58, v64, v58
	s_waitcnt lgkmcnt(2)
	v_add_f32_e32 v44, v45, v50
	ds_bpermute_b32 v60, v109, v58
	s_waitcnt lgkmcnt(2)
	v_add_f32_e32 v50, v51, v53
	ds_bpermute_b32 v53, v108, v65
	s_waitcnt lgkmcnt(2)
	v_add_f32_e32 v52, v52, v59
	ds_bpermute_b32 v59, v109, v52
	s_waitcnt lgkmcnt(2)
	v_add_f32_e32 v58, v58, v60
	ds_bpermute_b32 v60, v110, v58
	s_waitcnt lgkmcnt(2)
	v_add_f32_e32 v53, v65, v53
	ds_bpermute_b32 v61, v109, v53
	s_waitcnt lgkmcnt(2)
	v_add_f32_e32 v52, v52, v59
	ds_bpermute_b32 v59, v110, v52
	s_waitcnt lgkmcnt(2)
	v_add_f32_e32 v58, v58, v60
	ds_bpermute_b32 v60, v111, v58
	s_waitcnt lgkmcnt(2)
	v_add_f32_e32 v53, v53, v61
	ds_bpermute_b32 v61, v110, v53
	s_waitcnt lgkmcnt(2)
	v_add_f32_e32 v52, v52, v59
	ds_bpermute_b32 v59, v111, v52
	s_waitcnt lgkmcnt(2)
	v_add_f32_e32 v58, v58, v60
	ds_bpermute_b32 v60, v112, v58
	s_waitcnt lgkmcnt(2)
	v_add_f32_e32 v53, v53, v61
	ds_bpermute_b32 v61, v111, v53
	s_waitcnt lgkmcnt(2)
	v_add_f32_e32 v63, v52, v59
	ds_bpermute_b32 v64, v112, v63
	s_waitcnt lgkmcnt(2)
	v_add_f32_e32 v52, v58, v60
	ds_bpermute_b32 v35, v113, v34
	s_waitcnt lgkmcnt(2)
	v_add_f32_e32 v61, v53, v61
	ds_bpermute_b32 v62, v112, v61
	s_waitcnt lgkmcnt(2)
	v_add_f32_e32 v60, v63, v64
	ds_bpermute_b32 v37, v113, v36
	ds_bpermute_b32 v43, v113, v42
	ds_bpermute_b32 v45, v113, v44
	s_waitcnt lgkmcnt(3)
	v_add_f32_e32 v58, v61, v62
	ds_bpermute_b32 v51, v113, v50
	ds_bpermute_b32 v53, v113, v52
	ds_bpermute_b32 v59, v113, v58
	ds_bpermute_b32 v61, v113, v60
	s_and_saveexec_b64 s[0:1], s[2:3]
	s_cbranch_execz .LBB0_14
	s_waitcnt lgkmcnt(6)
	v_add_f32_e32 v36, v36, v37
	v_add_f32_e32 v34, v34, v35
	s_waitcnt lgkmcnt(5)
	v_add_f32_e32 v42, v42, v43
	v_cndmask_b32_e64 v34, v34, v36, s[4:5]
	s_waitcnt lgkmcnt(4)
	v_add_f32_e32 v44, v44, v45
	v_cndmask_b32_e64 v34, v34, v42, s[6:7]
	s_waitcnt lgkmcnt(3)
	v_add_f32_e32 v50, v50, v51
	v_cndmask_b32_e64 v34, v34, v44, s[8:9]
	s_waitcnt lgkmcnt(2)
	v_add_f32_e32 v52, v52, v53
	v_cndmask_b32_e64 v34, v34, v50, s[10:11]
	s_waitcnt lgkmcnt(1)
	v_add_f32_e32 v58, v58, v59
	v_cndmask_b32_e64 v34, v34, v52, s[12:13]
	s_waitcnt lgkmcnt(0)
	v_add_f32_e32 v60, v60, v61
	v_cndmask_b32_e64 v34, v34, v58, s[14:15]
	v_cndmask_b32_e64 v34, v34, v60, s[16:17]
	s_lshl_b64 s[18:19], s[26:27], 5
	v_add_f32_e32 v36, v107, v34
	v_lshl_add_u64 v[34:35], v[102:103], 0, s[18:19]
	global_store_dword v[34:35], v36, off
; #define P0_XLOAD(dst, row_) do { const f32x4* xr_ = (const f32x4*)(F.x + (size_t)(row_) * DM) + F.lane; _Pragma("unroll") for (int j = 0; j < 8; ++j) dst[j] = xr_[64 * j]; } while (0)
; DI void p0_prologue(Frame& F) {
;     ...
;           P0_XLOAD(va, (row2 < NTOK ? row2 : NTOK - 1));
;           __builtin_amdgcn_sched_barrier(0);
;           if (row1 < NTOK) P0_XROW(vb, row1);
.LBB0_14:
	s_or_b64 exec, exec, s[0:1]
	s_add_i32 s0, s23, s26
	s_min_i32 s0, s0, 0x7fff
	s_ashr_i32 s1, s0, 31
	s_lshl_b64 s[0:1], s[0:1], 13
	v_lshl_add_u64 v[34:35], v[98:99], 0, s[0:1]
	global_load_dwordx4 v[86:89], v[34:35], off nt
	global_load_dwordx4 v[78:81], v[34:35], off offset:1024 nt
	global_load_dwordx4 v[70:73], v[34:35], off offset:2048 nt
	global_load_dwordx4 v[62:65], v[34:35], off offset:3072 nt
	v_add_co_u32_e32 v34, vcc, 0x1000, v34
	s_nop 1
	v_addc_co_u32_e32 v35, vcc, 0, v35, vcc
	s_waitcnt lgkmcnt(0)
	global_load_dwordx4 v[58:61], v[34:35], off nt
	global_load_dwordx4 v[50:53], v[34:35], off offset:1024 nt
	global_load_dwordx4 v[42:45], v[34:35], off offset:2048 nt
	s_nop 0
	global_load_dwordx4 v[34:37], v[34:35], off offset:3072 nt
	s_andn2_b64 vcc, exec, s[28:29]
	s_cbranch_vccnz .LBB0_11
	s_waitcnt vmcnt(23)
	v_mov_b32_e32 v118, v95
	s_waitcnt vmcnt(22)
	v_mov_b32_e32 v119, v91
	v_mov_b32_e32 v104, v94
	v_mov_b32_e32 v105, v90
	v_pk_mul_f32 v[118:119], v[118:119], v[118:119]
	v_mov_b32_e32 v120, v97
	v_mov_b32_e32 v121, v93
	v_pk_fma_f32 v[104:105], v[104:105], v[104:105], v[118:119]
	v_mov_b32_e32 v118, v96
	v_mov_b32_e32 v119, v92
	v_pk_mul_f32 v[120:121], v[120:121], v[120:121]
	s_waitcnt vmcnt(19)
	v_mul_f32_e32 v106, v66, v66
	v_pk_fma_f32 v[118:119], v[118:119], v[118:119], v[120:121]
	v_pk_mul_f32 v[120:121], v[82:83], v[82:83]
	v_pk_add_f32 v[104:105], v[104:105], v[118:119]
	v_pk_mul_f32 v[118:119], v[84:85], v[84:85]
	v_mul_f32_e32 v117, v67, v67
	v_pk_mov_b32 v[122:123], v[120:121], v[118:119] op_sel:[1,0]
	v_mov_b32_e32 v121, v119
	v_pk_add_f32 v[118:119], v[122:123], v[120:121]
	v_pk_add_f32 v[104:105], v[104:105], v[104:105] op_sel:[0,1] op_sel_hi:[1,0]
	v_pk_add_f32 v[118:119], v[118:119], v[118:119] op_sel:[0,1] op_sel_hi:[1,0]
	v_mov_b32_e32 v105, v106
	v_mov_b32_e32 v119, v117
	v_mul_f32_e32 v106, v75, v75
	v_mul_f32_e32 v120, v68, v68
	v_pk_add_f32 v[104:105], v[104:105], v[118:119]
	v_pk_fma_f32 v[118:119], v[74:75], v[74:75], v[106:107] op_sel_hi:[1,1,0]
	v_mul_f32_e32 v106, v77, v77
	v_mul_f32_e32 v122, v69, v69
	v_mov_b32_e32 v119, v120
	v_pk_fma_f32 v[120:121], v[76:77], v[76:77], v[106:107] op_sel_hi:[1,1,0]
	s_waitcnt vmcnt(16)
	v_mul_f32_e32 v106, v38, v38
	v_mov_b32_e32 v121, v122
	v_pk_add_f32 v[118:119], v[118:119], v[120:121]
	v_pk_mul_f32 v[120:121], v[54:55], v[54:55]
	v_pk_add_f32 v[104:105], v[104:105], v[118:119]
	v_pk_mul_f32 v[118:119], v[56:57], v[56:57]
	v_mul_f32_e32 v117, v39, v39
	v_pk_mov_b32 v[122:123], v[120:121], v[118:119] op_sel:[1,0]
	v_mov_b32_e32 v121, v119
	v_pk_add_f32 v[118:119], v[122:123], v[120:121]
	v_pk_add_f32 v[104:105], v[104:105], v[104:105] op_sel:[0,1] op_sel_hi:[1,0]
	v_pk_add_f32 v[118:119], v[118:119], v[118:119] op_sel:[0,1] op_sel_hi:[1,0]
	v_mov_b32_e32 v105, v106
	v_mov_b32_e32 v119, v117
	v_mul_f32_e32 v106, v47, v47
	v_mul_f32_e32 v120, v40, v40
	v_pk_add_f32 v[104:105], v[104:105], v[118:119]
	v_pk_fma_f32 v[118:119], v[46:47], v[46:47], v[106:107] op_sel_hi:[1,1,0]
	v_mul_f32_e32 v106, v49, v49
	v_mul_f32_e32 v122, v41, v41
	v_mov_b32_e32 v119, v120
	v_pk_fma_f32 v[120:121], v[48:49], v[48:49], v[106:107] op_sel_hi:[1,1,0]
	s_ashr_i32 s25, s24, 31
	v_mov_b32_e32 v121, v122
	v_pk_add_f32 v[118:119], v[118:119], v[120:121]
	s_nop 0
	v_pk_add_f32 v[104:105], v[104:105], v[118:119]
	s_nop 0
	v_add_f32_e32 v104, v104, v105
	ds_bpermute_b32 v105, v108, v104
	s_waitcnt lgkmcnt(0)
	v_add_f32_e32 v104, v104, v105
	ds_bpermute_b32 v105, v109, v104
	s_waitcnt lgkmcnt(0)
	v_add_f32_e32 v104, v104, v105
	ds_bpermute_b32 v105, v110, v104
	s_waitcnt lgkmcnt(0)
	v_add_f32_e32 v104, v104, v105
	ds_bpermute_b32 v105, v111, v104
	s_waitcnt lgkmcnt(0)
	v_add_f32_e32 v104, v104, v105
	ds_bpermute_b32 v105, v112, v104
	s_waitcnt lgkmcnt(0)
	v_add_f32_e32 v104, v104, v105
	ds_bpermute_b32 v105, v113, v104
	s_waitcnt lgkmcnt(0)
	v_add_f32_e32 v104, v104, v105
	v_fmamk_f32 v104, v104, 0x3a000000, v115
	v_mul_f32_e32 v105, 0x4f800000, v104
	v_cmp_gt_f32_e32 vcc, s34, v104
	s_nop 1
	v_cndmask_b32_e32 v104, v104, v105, vcc
	v_sqrt_f32_e32 v105, v104
	s_nop 0
	v_add_u32_e32 v106, -1, v105
	v_fma_f32 v117, -v106, v105, v104
	v_cmp_ge_f32_e64 s[18:19], 0, v117
	v_add_u32_e32 v117, 1, v105
	s_nop 0
	v_cndmask_b32_e64 v106, v105, v106, s[18:19]
	v_fma_f32 v105, -v117, v105, v104
	v_cmp_lt_f32_e64 s[18:19], 0, v105
	s_nop 1
	v_cndmask_b32_e64 v105, v106, v117, s[18:19]
	v_mul_f32_e32 v106, 0x37800000, v105
	v_cndmask_b32_e32 v105, v105, v106, vcc
	v_cmp_class_f32_e32 vcc, v104, v116
	s_nop 1
	v_cndmask_b32_e32 v104, v105, v104, vcc
	v_div_scale_f32 v105, s[0:1], v104, v104, 1.0
	v_rcp_f32_e32 v106, v105
	s_lshl_b64 s[0:1], s[24:25], 12
	v_fma_f32 v117, -v105, v106, 1.0
	v_fmac_f32_e32 v106, v117, v106
	v_div_scale_f32 v117, vcc, 1.0, v104, 1.0
	v_mul_f32_e32 v118, v117, v106
	v_fma_f32 v119, -v105, v118, v117
	v_fmac_f32_e32 v118, v119, v106
	v_fma_f32 v105, -v105, v118, v117
	v_div_fmas_f32 v105, v105, v106, v118
	v_div_fixup_f32 v106, v105, v104, 1.0
	v_pk_mul_f32 v[94:95], v[94:95], v[106:107] op_sel_hi:[1,0]
	v_pk_mul_f32 v[96:97], v[96:97], v[106:107] op_sel_hi:[1,0]
	v_pk_mul_f32 v[124:125], v[2:3], v[94:95]
	v_pk_mul_f32 v[122:123], v[4:5], v[96:97]
	ds_read_b128 v[94:97], v114
	v_lshl_add_u64 v[104:105], v[100:101], 0, s[0:1]
	v_cvt_pk_bf16_f32 v118, v124, v125
	v_cvt_pk_bf16_f32 v119, v122, v123
	global_store_dwordx2 v[104:105], v[118:119], off
	ds_read_b128 v[118:121], v114 offset:8192
	s_waitcnt lgkmcnt(1)
	v_mul_f32_e32 v95, v95, v125
	v_fmac_f32_e32 v95, v94, v124
	v_mul_f32_e32 v94, v97, v123
	v_fmac_f32_e32 v94, v96, v122
	v_add_f32_e32 v94, v95, v94
	v_add_f32_e32 v117, 0, v94
	s_waitcnt lgkmcnt(0)
	v_mul_f32_e32 v119, v119, v125
	ds_read_b128 v[94:97], v114 offset:16384
	v_fmac_f32_e32 v119, v118, v124
	v_mul_f32_e32 v118, v121, v123
	v_fmac_f32_e32 v118, v120, v122
	v_add_f32_e32 v118, v119, v118
	v_add_f32_e32 v126, 0, v118
	ds_read_b128 v[118:121], v114 offset:24576
	s_waitcnt lgkmcnt(1)
	v_mul_f32_e32 v95, v95, v125
	v_fmac_f32_e32 v95, v94, v124
	v_mul_f32_e32 v94, v97, v123
	v_fmac_f32_e32 v94, v96, v122
	v_add_f32_e32 v94, v95, v94
	v_add_f32_e32 v127, 0, v94
	s_waitcnt lgkmcnt(0)
	v_mul_f32_e32 v119, v119, v125
	ds_read_b128 v[94:97], v114 offset:32768
	v_fmac_f32_e32 v119, v118, v124
	v_mul_f32_e32 v118, v121, v123
	v_fmac_f32_e32 v118, v120, v122
	v_add_f32_e32 v118, v119, v118
	v_add_f32_e32 v128, 0, v118
	ds_read_b128 v[118:121], v114 offset:40960
	s_waitcnt lgkmcnt(1)
	v_mul_f32_e32 v95, v95, v125
	v_fmac_f32_e32 v95, v94, v124
	v_mul_f32_e32 v94, v97, v123
	v_fmac_f32_e32 v94, v96, v122
	v_add_f32_e32 v94, v95, v94
	v_add_f32_e32 v129, 0, v94
	s_waitcnt lgkmcnt(0)
	v_mul_f32_e32 v119, v119, v125
	ds_read_b128 v[94:97], v114 offset:49152
	v_fmac_f32_e32 v119, v118, v124
	v_mul_f32_e32 v118, v121, v123
	v_fmac_f32_e32 v118, v120, v122
	v_add_f32_e32 v118, v119, v118
	v_add_f32_e32 v130, 0, v118
	ds_read_b128 v[118:121], v114 offset:57344
	s_waitcnt lgkmcnt(1)
	v_mul_f32_e32 v95, v95, v125
	v_fmac_f32_e32 v95, v94, v124
	v_mul_f32_e32 v94, v97, v123
	v_fmac_f32_e32 v94, v96, v122
	v_add_f32_e32 v94, v95, v94
	v_add_f32_e32 v131, 0, v94
	s_waitcnt lgkmcnt(0)
	v_mul_f32_e32 v94, v119, v125
	v_mul_f32_e32 v95, v121, v123
	v_fmac_f32_e32 v94, v118, v124
	v_fmac_f32_e32 v95, v120, v122
	v_add_f32_e32 v94, v94, v95
	v_add_f32_e32 v122, 0, v94
	v_pk_mul_f32 v[90:91], v[90:91], v[106:107] op_sel_hi:[1,0]
	v_pk_mul_f32 v[92:93], v[92:93], v[106:107] op_sel_hi:[1,0]
	v_pk_mul_f32 v[120:121], v[6:7], v[90:91]
	v_pk_mul_f32 v[118:119], v[8:9], v[92:93]
	ds_read_b128 v[90:93], v114 offset:1024
	v_cvt_pk_bf16_f32 v94, v120, v121
	v_cvt_pk_bf16_f32 v95, v118, v119
	global_store_dwordx2 v[104:105], v[94:95], off offset:512
	ds_read_b128 v[94:97], v114 offset:9216
	s_waitcnt lgkmcnt(1)
	v_mul_f32_e32 v91, v121, v91
	v_fmac_f32_e32 v91, v120, v90
	v_mul_f32_e32 v90, v119, v93
	v_fmac_f32_e32 v90, v118, v92
	v_add_f32_e32 v90, v91, v90
	v_add_f32_e32 v117, v117, v90
	s_waitcnt lgkmcnt(0)
	v_mul_f32_e32 v95, v121, v95
	ds_read_b128 v[90:93], v114 offset:17408
	v_fmac_f32_e32 v95, v120, v94
	v_mul_f32_e32 v94, v119, v97
	v_fmac_f32_e32 v94, v118, v96
	v_add_f32_e32 v94, v95, v94
	v_add_f32_e32 v123, v126, v94
	ds_read_b128 v[94:97], v114 offset:25600
	s_waitcnt lgkmcnt(1)
	v_mul_f32_e32 v91, v121, v91
	v_fmac_f32_e32 v91, v120, v90
	v_mul_f32_e32 v90, v119, v93
	v_fmac_f32_e32 v90, v118, v92
	v_add_f32_e32 v90, v91, v90
	v_add_f32_e32 v124, v127, v90
	s_waitcnt lgkmcnt(0)
	v_mul_f32_e32 v95, v121, v95
	ds_read_b128 v[90:93], v114 offset:33792
	v_fmac_f32_e32 v95, v120, v94
	v_mul_f32_e32 v94, v119, v97
	v_fmac_f32_e32 v94, v118, v96
	v_add_f32_e32 v94, v95, v94
	v_add_f32_e32 v125, v128, v94
	ds_read_b128 v[94:97], v114 offset:41984
	s_waitcnt lgkmcnt(1)
	v_mul_f32_e32 v91, v121, v91
	v_fmac_f32_e32 v91, v120, v90
	v_mul_f32_e32 v90, v119, v93
	v_fmac_f32_e32 v90, v118, v92
	v_add_f32_e32 v90, v91, v90
	v_add_f32_e32 v126, v129, v90
	s_waitcnt lgkmcnt(0)
	v_mul_f32_e32 v95, v121, v95
	ds_read_b128 v[90:93], v114 offset:50176
	v_fmac_f32_e32 v95, v120, v94
	v_mul_f32_e32 v94, v119, v97
	v_fmac_f32_e32 v94, v118, v96
	v_add_f32_e32 v94, v95, v94
	v_add_f32_e32 v127, v130, v94
	ds_read_b128 v[94:97], v114 offset:58368
	s_waitcnt lgkmcnt(1)
	v_mul_f32_e32 v91, v121, v91
	v_fmac_f32_e32 v91, v120, v90
	v_mul_f32_e32 v90, v119, v93
	v_fmac_f32_e32 v90, v118, v92
	v_add_f32_e32 v90, v91, v90
	v_add_f32_e32 v128, v131, v90
	s_waitcnt lgkmcnt(0)
	v_mul_f32_e32 v90, v121, v95
	v_mul_f32_e32 v91, v119, v97
	v_fmac_f32_e32 v90, v120, v94
	v_fmac_f32_e32 v91, v118, v96
	v_add_f32_e32 v90, v90, v91
	v_add_f32_e32 v118, v122, v90
	v_pk_mul_f32 v[82:83], v[82:83], v[106:107] op_sel_hi:[1,0]
	v_pk_mul_f32 v[84:85], v[84:85], v[106:107] op_sel_hi:[1,0]
	v_pk_mul_f32 v[96:97], v[10:11], v[82:83]
	v_pk_mul_f32 v[94:95], v[12:13], v[84:85]
	ds_read_b128 v[82:85], v114 offset:2048
	v_cvt_pk_bf16_f32 v90, v96, v97
	v_cvt_pk_bf16_f32 v91, v94, v95
	global_store_dwordx2 v[104:105], v[90:91], off offset:1024
	ds_read_b128 v[90:93], v114 offset:10240
	s_waitcnt lgkmcnt(1)
	v_mul_f32_e32 v83, v97, v83
	v_fmac_f32_e32 v83, v96, v82
	v_mul_f32_e32 v82, v95, v85
	v_fmac_f32_e32 v82, v94, v84
	v_add_f32_e32 v82, v83, v82
	v_add_f32_e32 v117, v117, v82
	s_waitcnt lgkmcnt(0)
	v_mul_f32_e32 v91, v97, v91
	ds_read_b128 v[82:85], v114 offset:18432
	v_fmac_f32_e32 v91, v96, v90
	v_mul_f32_e32 v90, v95, v93
	v_fmac_f32_e32 v90, v94, v92
	v_add_f32_e32 v90, v91, v90
	v_add_f32_e32 v119, v123, v90
	ds_read_b128 v[90:93], v114 offset:26624
	s_waitcnt lgkmcnt(1)
	v_mul_f32_e32 v83, v97, v83
	v_fmac_f32_e32 v83, v96, v82
	v_mul_f32_e32 v82, v95, v85
	v_fmac_f32_e32 v82, v94, v84
	v_add_f32_e32 v82, v83, v82
	v_add_f32_e32 v120, v124, v82
	s_waitcnt lgkmcnt(0)
	v_mul_f32_e32 v91, v97, v91
	ds_read_b128 v[82:85], v114 offset:34816
	v_fmac_f32_e32 v91, v96, v90
	v_mul_f32_e32 v90, v95, v93
	v_fmac_f32_e32 v90, v94, v92
	v_add_f32_e32 v90, v91, v90
	v_add_f32_e32 v121, v125, v90
	ds_read_b128 v[90:93], v114 offset:43008
	s_waitcnt lgkmcnt(1)
	v_mul_f32_e32 v83, v97, v83
	v_fmac_f32_e32 v83, v96, v82
	v_mul_f32_e32 v82, v95, v85
	v_fmac_f32_e32 v82, v94, v84
	v_add_f32_e32 v82, v83, v82
	v_add_f32_e32 v122, v126, v82
	s_waitcnt lgkmcnt(0)
	v_mul_f32_e32 v91, v97, v91
	ds_read_b128 v[82:85], v114 offset:51200
	v_fmac_f32_e32 v91, v96, v90
	v_mul_f32_e32 v90, v95, v93
	v_fmac_f32_e32 v90, v94, v92
	v_add_f32_e32 v90, v91, v90
	v_add_f32_e32 v123, v127, v90
	ds_read_b128 v[90:93], v114 offset:59392
	s_waitcnt lgkmcnt(1)
	v_mul_f32_e32 v83, v97, v83
	v_fmac_f32_e32 v83, v96, v82
	v_mul_f32_e32 v82, v95, v85
	v_fmac_f32_e32 v82, v94, v84
	v_add_f32_e32 v82, v83, v82
	v_add_f32_e32 v124, v128, v82
	s_waitcnt lgkmcnt(0)
	v_mul_f32_e32 v82, v97, v91
	v_mul_f32_e32 v83, v95, v93
	v_fmac_f32_e32 v82, v96, v90
	v_fmac_f32_e32 v83, v94, v92
	v_add_f32_e32 v82, v82, v83
	v_add_f32_e32 v94, v118, v82
	v_pk_mul_f32 v[74:75], v[74:75], v[106:107] op_sel_hi:[1,0]
	v_pk_mul_f32 v[76:77], v[76:77], v[106:107] op_sel_hi:[1,0]
	v_pk_mul_f32 v[92:93], v[14:15], v[74:75]
	v_pk_mul_f32 v[90:91], v[16:17], v[76:77]
	ds_read_b128 v[74:77], v114 offset:3072
	v_cvt_pk_bf16_f32 v82, v92, v93
	v_cvt_pk_bf16_f32 v83, v90, v91
	global_store_dwordx2 v[104:105], v[82:83], off offset:1536
	ds_read_b128 v[82:85], v114 offset:11264
	s_waitcnt lgkmcnt(1)
	v_mul_f32_e32 v75, v93, v75
	v_fmac_f32_e32 v75, v92, v74
	v_mul_f32_e32 v74, v91, v77
	v_fmac_f32_e32 v74, v90, v76
	v_add_f32_e32 v74, v75, v74
	v_add_f32_e32 v95, v117, v74
	s_waitcnt lgkmcnt(0)
	v_mul_f32_e32 v83, v93, v83
	ds_read_b128 v[74:77], v114 offset:19456
	v_fmac_f32_e32 v83, v92, v82
	v_mul_f32_e32 v82, v91, v85
	v_fmac_f32_e32 v82, v90, v84
	v_add_f32_e32 v82, v83, v82
	v_add_f32_e32 v96, v119, v82
	ds_read_b128 v[82:85], v114 offset:27648
	s_waitcnt lgkmcnt(1)
	v_mul_f32_e32 v75, v93, v75
	v_fmac_f32_e32 v75, v92, v74
	v_mul_f32_e32 v74, v91, v77
	v_fmac_f32_e32 v74, v90, v76
	v_add_f32_e32 v74, v75, v74
	v_add_f32_e32 v97, v120, v74
	s_waitcnt lgkmcnt(0)
	v_mul_f32_e32 v83, v93, v83
	ds_read_b128 v[74:77], v114 offset:35840
	v_fmac_f32_e32 v83, v92, v82
	v_mul_f32_e32 v82, v91, v85
	v_fmac_f32_e32 v82, v90, v84
	v_add_f32_e32 v82, v83, v82
	v_add_f32_e32 v117, v121, v82
	ds_read_b128 v[82:85], v114 offset:44032
	s_waitcnt lgkmcnt(1)
	v_mul_f32_e32 v75, v93, v75
	v_fmac_f32_e32 v75, v92, v74
	v_mul_f32_e32 v74, v91, v77
	v_fmac_f32_e32 v74, v90, v76
	v_add_f32_e32 v74, v75, v74
	v_add_f32_e32 v118, v122, v74
	s_waitcnt lgkmcnt(0)
	v_mul_f32_e32 v83, v93, v83
	ds_read_b128 v[74:77], v114 offset:52224
	v_fmac_f32_e32 v83, v92, v82
	v_mul_f32_e32 v82, v91, v85
	v_fmac_f32_e32 v82, v90, v84
	v_add_f32_e32 v82, v83, v82
	v_add_f32_e32 v119, v123, v82
	ds_read_b128 v[82:85], v114 offset:60416
	s_waitcnt lgkmcnt(1)
	v_mul_f32_e32 v75, v93, v75
	v_fmac_f32_e32 v75, v92, v74
	v_mul_f32_e32 v74, v91, v77
	v_fmac_f32_e32 v74, v90, v76
	v_add_f32_e32 v74, v75, v74
	v_add_f32_e32 v120, v124, v74
	s_waitcnt lgkmcnt(0)
	v_mul_f32_e32 v74, v93, v83
	v_mul_f32_e32 v75, v91, v85
	v_fmac_f32_e32 v74, v92, v82
	v_fmac_f32_e32 v75, v90, v84
	v_add_f32_e32 v74, v74, v75
	v_add_f32_e32 v90, v94, v74
	v_pk_mul_f32 v[66:67], v[66:67], v[106:107] op_sel_hi:[1,0]
	v_pk_mul_f32 v[68:69], v[68:69], v[106:107] op_sel_hi:[1,0]
	v_pk_mul_f32 v[84:85], v[18:19], v[66:67]
	v_pk_mul_f32 v[82:83], v[20:21], v[68:69]
	ds_read_b128 v[66:69], v114 offset:4096
	v_cvt_pk_bf16_f32 v74, v84, v85
	v_cvt_pk_bf16_f32 v75, v82, v83
	global_store_dwordx2 v[104:105], v[74:75], off offset:2048
	ds_read_b128 v[74:77], v114 offset:12288
	s_waitcnt lgkmcnt(1)
	v_mul_f32_e32 v67, v85, v67
	v_fmac_f32_e32 v67, v84, v66
	v_mul_f32_e32 v66, v83, v69
	v_fmac_f32_e32 v66, v82, v68
	v_add_f32_e32 v66, v67, v66
	v_add_f32_e32 v91, v95, v66
	s_waitcnt lgkmcnt(0)
	v_mul_f32_e32 v75, v85, v75
	ds_read_b128 v[66:69], v114 offset:20480
	v_fmac_f32_e32 v75, v84, v74
	v_mul_f32_e32 v74, v83, v77
	v_fmac_f32_e32 v74, v82, v76
	v_add_f32_e32 v74, v75, v74
	v_add_f32_e32 v92, v96, v74
	ds_read_b128 v[74:77], v114 offset:28672
	s_waitcnt lgkmcnt(1)
	v_mul_f32_e32 v67, v85, v67
	v_fmac_f32_e32 v67, v84, v66
	v_mul_f32_e32 v66, v83, v69
	v_fmac_f32_e32 v66, v82, v68
	v_add_f32_e32 v66, v67, v66
	v_add_f32_e32 v93, v97, v66
	s_waitcnt lgkmcnt(0)
	v_mul_f32_e32 v75, v85, v75
	ds_read_b128 v[66:69], v114 offset:36864
	v_fmac_f32_e32 v75, v84, v74
	v_mul_f32_e32 v74, v83, v77
	v_fmac_f32_e32 v74, v82, v76
	v_add_f32_e32 v74, v75, v74
	v_add_f32_e32 v94, v117, v74
	ds_read_b128 v[74:77], v114 offset:45056
	s_waitcnt lgkmcnt(1)
	v_mul_f32_e32 v67, v85, v67
	v_fmac_f32_e32 v67, v84, v66
	v_mul_f32_e32 v66, v83, v69
	v_fmac_f32_e32 v66, v82, v68
	v_add_f32_e32 v66, v67, v66
	v_add_f32_e32 v95, v118, v66
	s_waitcnt lgkmcnt(0)
	v_mul_f32_e32 v75, v85, v75
	ds_read_b128 v[66:69], v114 offset:53248
	v_fmac_f32_e32 v75, v84, v74
	v_mul_f32_e32 v74, v83, v77
	v_fmac_f32_e32 v74, v82, v76
	v_add_f32_e32 v74, v75, v74
	v_add_f32_e32 v96, v119, v74
	ds_read_b128 v[74:77], v114 offset:61440
	s_waitcnt lgkmcnt(1)
	v_mul_f32_e32 v67, v85, v67
	v_fmac_f32_e32 v67, v84, v66
	v_mul_f32_e32 v66, v83, v69
	v_fmac_f32_e32 v66, v82, v68
	v_add_f32_e32 v66, v67, v66
	v_add_f32_e32 v97, v120, v66
	s_waitcnt lgkmcnt(0)
	v_mul_f32_e32 v66, v85, v75
	v_mul_f32_e32 v67, v83, v77
	v_fmac_f32_e32 v66, v84, v74
	v_fmac_f32_e32 v67, v82, v76
	v_add_f32_e32 v66, v66, v67
	v_add_f32_e32 v82, v90, v66
	v_pk_mul_f32 v[54:55], v[54:55], v[106:107] op_sel_hi:[1,0]
	v_pk_mul_f32 v[56:57], v[56:57], v[106:107] op_sel_hi:[1,0]
	v_pk_mul_f32 v[76:77], v[22:23], v[54:55]
	v_pk_mul_f32 v[74:75], v[24:25], v[56:57]
	ds_read_b128 v[54:57], v114 offset:5120
	v_cvt_pk_bf16_f32 v66, v76, v77
	v_cvt_pk_bf16_f32 v67, v74, v75
	global_store_dwordx2 v[104:105], v[66:67], off offset:2560
	ds_read_b128 v[66:69], v114 offset:13312
	s_waitcnt lgkmcnt(1)
	v_mul_f32_e32 v55, v77, v55
	v_fmac_f32_e32 v55, v76, v54
	v_mul_f32_e32 v54, v75, v57
	v_fmac_f32_e32 v54, v74, v56
	v_add_f32_e32 v54, v55, v54
	v_add_f32_e32 v83, v91, v54
	s_waitcnt lgkmcnt(0)
	v_mul_f32_e32 v67, v77, v67
	ds_read_b128 v[54:57], v114 offset:21504
	v_fmac_f32_e32 v67, v76, v66
	v_mul_f32_e32 v66, v75, v69
	v_fmac_f32_e32 v66, v74, v68
	v_add_f32_e32 v66, v67, v66
	v_add_f32_e32 v84, v92, v66
	ds_read_b128 v[66:69], v114 offset:29696
	s_waitcnt lgkmcnt(1)
	v_mul_f32_e32 v55, v77, v55
	v_fmac_f32_e32 v55, v76, v54
	v_mul_f32_e32 v54, v75, v57
	v_fmac_f32_e32 v54, v74, v56
	v_add_f32_e32 v54, v55, v54
	v_add_f32_e32 v85, v93, v54
	s_waitcnt lgkmcnt(0)
	v_mul_f32_e32 v67, v77, v67
	ds_read_b128 v[54:57], v114 offset:37888
	v_fmac_f32_e32 v67, v76, v66
	v_mul_f32_e32 v66, v75, v69
	v_fmac_f32_e32 v66, v74, v68
	v_add_f32_e32 v66, v67, v66
	v_add_f32_e32 v90, v94, v66
	ds_read_b128 v[66:69], v114 offset:46080
	s_waitcnt lgkmcnt(1)
	v_mul_f32_e32 v55, v77, v55
	v_fmac_f32_e32 v55, v76, v54
	v_mul_f32_e32 v54, v75, v57
	v_fmac_f32_e32 v54, v74, v56
	v_add_f32_e32 v54, v55, v54
	v_add_f32_e32 v91, v95, v54
	s_waitcnt lgkmcnt(0)
	v_mul_f32_e32 v67, v77, v67
	ds_read_b128 v[54:57], v114 offset:54272
	v_fmac_f32_e32 v67, v76, v66
	v_mul_f32_e32 v66, v75, v69
	v_fmac_f32_e32 v66, v74, v68
	v_add_f32_e32 v66, v67, v66
	v_add_f32_e32 v92, v96, v66
	ds_read_b128 v[66:69], v114 offset:62464
	s_waitcnt lgkmcnt(1)
	v_mul_f32_e32 v55, v77, v55
	v_fmac_f32_e32 v55, v76, v54
	v_mul_f32_e32 v54, v75, v57
	v_fmac_f32_e32 v54, v74, v56
	v_add_f32_e32 v54, v55, v54
	v_add_f32_e32 v93, v97, v54
	s_waitcnt lgkmcnt(0)
	v_mul_f32_e32 v54, v77, v67
	v_mul_f32_e32 v55, v75, v69
	v_fmac_f32_e32 v54, v76, v66
	v_fmac_f32_e32 v55, v74, v68
	v_add_f32_e32 v54, v54, v55
	v_add_f32_e32 v74, v82, v54
	v_pk_mul_f32 v[46:47], v[46:47], v[106:107] op_sel_hi:[1,0]
	v_pk_mul_f32 v[48:49], v[48:49], v[106:107] op_sel_hi:[1,0]
	v_pk_mul_f32 v[68:69], v[26:27], v[46:47]
	v_pk_mul_f32 v[66:67], v[28:29], v[48:49]
	ds_read_b128 v[46:49], v114 offset:6144
	v_cvt_pk_bf16_f32 v54, v68, v69
	v_cvt_pk_bf16_f32 v55, v66, v67
	global_store_dwordx2 v[104:105], v[54:55], off offset:3072
	ds_read_b128 v[54:57], v114 offset:14336
	s_waitcnt lgkmcnt(1)
	v_mul_f32_e32 v47, v69, v47
	v_fmac_f32_e32 v47, v68, v46
	v_mul_f32_e32 v46, v67, v49
	v_fmac_f32_e32 v46, v66, v48
	v_add_f32_e32 v46, v47, v46
	v_add_f32_e32 v75, v83, v46
	s_waitcnt lgkmcnt(0)
	v_mul_f32_e32 v55, v69, v55
	ds_read_b128 v[46:49], v114 offset:22528
	v_fmac_f32_e32 v55, v68, v54
	v_mul_f32_e32 v54, v67, v57
	v_fmac_f32_e32 v54, v66, v56
	v_add_f32_e32 v54, v55, v54
	v_add_f32_e32 v76, v84, v54
	ds_read_b128 v[54:57], v114 offset:30720
	s_waitcnt lgkmcnt(1)
	v_mul_f32_e32 v47, v69, v47
	v_fmac_f32_e32 v47, v68, v46
	v_mul_f32_e32 v46, v67, v49
	v_fmac_f32_e32 v46, v66, v48
	v_add_f32_e32 v46, v47, v46
	v_add_f32_e32 v77, v85, v46
	s_waitcnt lgkmcnt(0)
	v_mul_f32_e32 v55, v69, v55
	ds_read_b128 v[46:49], v114 offset:38912
	v_fmac_f32_e32 v55, v68, v54
	v_mul_f32_e32 v54, v67, v57
	v_fmac_f32_e32 v54, v66, v56
	v_add_f32_e32 v54, v55, v54
	v_add_f32_e32 v82, v90, v54
	ds_read_b128 v[54:57], v114 offset:47104
	s_waitcnt lgkmcnt(1)
	v_mul_f32_e32 v47, v69, v47
	v_fmac_f32_e32 v47, v68, v46
	v_mul_f32_e32 v46, v67, v49
	v_fmac_f32_e32 v46, v66, v48
	v_add_f32_e32 v46, v47, v46
	v_add_f32_e32 v83, v91, v46
	s_waitcnt lgkmcnt(0)
	v_mul_f32_e32 v55, v69, v55
	ds_read_b128 v[46:49], v114 offset:55296
	v_fmac_f32_e32 v55, v68, v54
	v_mul_f32_e32 v54, v67, v57
	v_fmac_f32_e32 v54, v66, v56
	v_add_f32_e32 v54, v55, v54
	v_add_f32_e32 v84, v92, v54
	ds_read_b128 v[54:57], v114 offset:63488
	s_waitcnt lgkmcnt(1)
	v_mul_f32_e32 v47, v69, v47
	v_fmac_f32_e32 v47, v68, v46
	v_mul_f32_e32 v46, v67, v49
	v_fmac_f32_e32 v46, v66, v48
	v_add_f32_e32 v46, v47, v46
	v_add_f32_e32 v85, v93, v46
	s_waitcnt lgkmcnt(0)
	v_mul_f32_e32 v46, v69, v55
	v_mul_f32_e32 v47, v67, v57
	v_fmac_f32_e32 v46, v68, v54
	v_fmac_f32_e32 v47, v66, v56
	v_add_f32_e32 v46, v46, v47
	v_add_f32_e32 v66, v74, v46
	v_pk_mul_f32 v[38:39], v[38:39], v[106:107] op_sel_hi:[1,0]
	v_pk_mul_f32 v[40:41], v[40:41], v[106:107] op_sel_hi:[1,0]
	v_pk_mul_f32 v[56:57], v[30:31], v[38:39]
	v_pk_mul_f32 v[54:55], v[32:33], v[40:41]
	ds_read_b128 v[38:41], v114 offset:7168
	v_cvt_pk_bf16_f32 v46, v56, v57
	v_cvt_pk_bf16_f32 v47, v54, v55
	global_store_dwordx2 v[104:105], v[46:47], off offset:3584
	ds_read_b128 v[46:49], v114 offset:15360
	s_waitcnt lgkmcnt(1)
	v_mul_f32_e32 v39, v57, v39
	v_fmac_f32_e32 v39, v56, v38
	v_mul_f32_e32 v38, v55, v41
	v_fmac_f32_e32 v38, v54, v40
	v_add_f32_e32 v38, v39, v38
	v_add_f32_e32 v67, v75, v38
	s_waitcnt lgkmcnt(0)
	v_mul_f32_e32 v47, v57, v47
	ds_read_b128 v[38:41], v114 offset:23552
	v_fmac_f32_e32 v47, v56, v46
	v_mul_f32_e32 v46, v55, v49
	v_fmac_f32_e32 v46, v54, v48
	v_add_f32_e32 v46, v47, v46
	v_add_f32_e32 v68, v76, v46
	ds_read_b128 v[46:49], v114 offset:31744
	s_waitcnt lgkmcnt(1)
	v_mul_f32_e32 v39, v57, v39
	v_fmac_f32_e32 v39, v56, v38
	v_mul_f32_e32 v38, v55, v41
	v_fmac_f32_e32 v38, v54, v40
	v_add_f32_e32 v38, v39, v38
	v_add_f32_e32 v69, v77, v38
	s_waitcnt lgkmcnt(0)
	v_mul_f32_e32 v47, v57, v47
	ds_read_b128 v[38:41], v114 offset:39936
	v_fmac_f32_e32 v47, v56, v46
	v_mul_f32_e32 v46, v55, v49
	v_fmac_f32_e32 v46, v54, v48
	v_add_f32_e32 v46, v47, v46
	v_add_f32_e32 v74, v82, v46
	ds_read_b128 v[46:49], v114 offset:48128
	s_waitcnt lgkmcnt(1)
	v_mul_f32_e32 v39, v57, v39
	v_fmac_f32_e32 v39, v56, v38
	v_mul_f32_e32 v38, v55, v41
	v_fmac_f32_e32 v38, v54, v40
	v_add_f32_e32 v38, v39, v38
	v_add_f32_e32 v75, v83, v38
	s_waitcnt lgkmcnt(0)
	v_mul_f32_e32 v47, v57, v47
	ds_read_b128 v[38:41], v114 offset:56320
	v_fmac_f32_e32 v47, v56, v46
	v_mul_f32_e32 v46, v55, v49
	v_fmac_f32_e32 v46, v54, v48
	v_add_f32_e32 v46, v47, v46
	v_add_f32_e32 v76, v84, v46
	ds_read_b128 v[46:49], v114 offset:64512
	s_waitcnt lgkmcnt(1)
	v_mul_f32_e32 v39, v57, v39
	v_fmac_f32_e32 v39, v56, v38
	v_mul_f32_e32 v38, v55, v41
	v_fmac_f32_e32 v38, v54, v40
	v_add_f32_e32 v38, v39, v38
	v_add_f32_e32 v77, v85, v38
	s_waitcnt lgkmcnt(0)
	v_mul_f32_e32 v38, v57, v47
	v_mul_f32_e32 v39, v55, v49
	v_fmac_f32_e32 v38, v56, v46
	v_fmac_f32_e32 v39, v54, v48
	v_add_f32_e32 v38, v38, v39
	v_add_f32_e32 v56, v66, v38
	ds_bpermute_b32 v38, v108, v67
	ds_bpermute_b32 v39, v108, v68
	ds_bpermute_b32 v40, v108, v69
	ds_bpermute_b32 v41, v108, v74
	ds_bpermute_b32 v46, v108, v75
	s_waitcnt lgkmcnt(4)
	v_add_f32_e32 v38, v67, v38
	ds_bpermute_b32 v47, v109, v38
	s_waitcnt lgkmcnt(4)
	v_add_f32_e32 v39, v68, v39
	ds_bpermute_b32 v48, v109, v39
	s_waitcnt lgkmcnt(4)
	v_add_f32_e32 v40, v69, v40
	ds_bpermute_b32 v49, v109, v40
	s_waitcnt lgkmcnt(2)
	v_add_f32_e32 v38, v38, v47
	ds_bpermute_b32 v47, v110, v38
	s_waitcnt lgkmcnt(2)
	v_add_f32_e32 v39, v39, v48
	ds_bpermute_b32 v48, v110, v39
	v_add_f32_e32 v41, v74, v41
	v_add_f32_e32 v46, v75, v46
	s_waitcnt lgkmcnt(1)
	v_add_f32_e32 v38, v38, v47
	ds_bpermute_b32 v47, v111, v38
	v_add_f32_e32 v40, v40, v49
	s_waitcnt lgkmcnt(1)
	v_add_f32_e32 v39, v39, v48
	ds_bpermute_b32 v49, v110, v40
	ds_bpermute_b32 v48, v111, v39
	s_waitcnt lgkmcnt(2)
	v_add_f32_e32 v38, v38, v47
	ds_bpermute_b32 v47, v112, v38
	ds_bpermute_b32 v54, v109, v41
	s_waitcnt lgkmcnt(3)
	v_add_f32_e32 v49, v40, v49
	s_waitcnt lgkmcnt(2)
	v_add_f32_e32 v40, v39, v48
	ds_bpermute_b32 v48, v112, v40
	s_waitcnt lgkmcnt(2)
	v_add_f32_e32 v38, v38, v47
	ds_bpermute_b32 v47, v109, v46
	s_waitcnt lgkmcnt(2)
	v_add_f32_e32 v41, v41, v54
	ds_bpermute_b32 v55, v111, v49
	ds_bpermute_b32 v54, v110, v41
	s_waitcnt lgkmcnt(3)
	v_add_f32_e32 v40, v40, v48
	s_waitcnt lgkmcnt(2)
	v_add_f32_e32 v46, v46, v47
	ds_bpermute_b32 v47, v110, v46
	s_waitcnt lgkmcnt(2)
	v_add_f32_e32 v48, v49, v55
	s_waitcnt lgkmcnt(1)
	v_add_f32_e32 v49, v41, v54
	ds_bpermute_b32 v54, v111, v49
	ds_bpermute_b32 v55, v112, v48
	s_waitcnt lgkmcnt(2)
	v_add_f32_e32 v47, v46, v47
	ds_bpermute_b32 v57, v111, v47
	ds_bpermute_b32 v66, v108, v76
	s_waitcnt lgkmcnt(3)
	v_add_f32_e32 v49, v49, v54
	s_waitcnt lgkmcnt(2)
	v_add_f32_e32 v46, v48, v55
	ds_bpermute_b32 v54, v112, v49
	s_waitcnt lgkmcnt(2)
	v_add_f32_e32 v55, v47, v57
	ds_bpermute_b32 v57, v112, v55
	ds_bpermute_b32 v67, v108, v56
	s_waitcnt lgkmcnt(3)
	v_add_f32_e32 v66, v76, v66
	s_waitcnt lgkmcnt(2)
	v_add_f32_e32 v48, v49, v54
	ds_bpermute_b32 v68, v109, v66
	s_waitcnt lgkmcnt(2)
	v_add_f32_e32 v54, v55, v57
	ds_bpermute_b32 v57, v108, v77
	s_waitcnt lgkmcnt(2)
	v_add_f32_e32 v56, v56, v67
	ds_bpermute_b32 v67, v109, v56
	s_waitcnt lgkmcnt(2)
	v_add_f32_e32 v66, v66, v68
	ds_bpermute_b32 v68, v110, v66
	s_waitcnt lgkmcnt(2)
	v_add_f32_e32 v57, v77, v57
	ds_bpermute_b32 v69, v109, v57
	s_waitcnt lgkmcnt(2)
	v_add_f32_e32 v56, v56, v67
	ds_bpermute_b32 v67, v110, v56
	s_waitcnt lgkmcnt(2)
	v_add_f32_e32 v66, v66, v68
	ds_bpermute_b32 v68, v111, v66
	s_waitcnt lgkmcnt(2)
	v_add_f32_e32 v57, v57, v69
	ds_bpermute_b32 v69, v110, v57
	s_waitcnt lgkmcnt(2)
	v_add_f32_e32 v56, v56, v67
	ds_bpermute_b32 v67, v111, v56
	s_waitcnt lgkmcnt(2)
	v_add_f32_e32 v66, v66, v68
	ds_bpermute_b32 v68, v112, v66
	s_waitcnt lgkmcnt(2)
	v_add_f32_e32 v57, v57, v69
	ds_bpermute_b32 v69, v111, v57
	s_waitcnt lgkmcnt(2)
	v_add_f32_e32 v75, v56, v67
	ds_bpermute_b32 v76, v112, v75
	s_waitcnt lgkmcnt(2)
	v_add_f32_e32 v56, v66, v68
	ds_bpermute_b32 v39, v113, v38
	s_waitcnt lgkmcnt(2)
	v_add_f32_e32 v69, v57, v69
	ds_bpermute_b32 v74, v112, v69
	s_waitcnt lgkmcnt(2)
	v_add_f32_e32 v68, v75, v76
	ds_bpermute_b32 v41, v113, v40
	ds_bpermute_b32 v47, v113, v46
	ds_bpermute_b32 v49, v113, v48
	s_waitcnt lgkmcnt(3)
	v_add_f32_e32 v66, v69, v74
	ds_bpermute_b32 v55, v113, v54
	ds_bpermute_b32 v57, v113, v56
	ds_bpermute_b32 v67, v113, v66
	ds_bpermute_b32 v69, v113, v68
	s_and_saveexec_b64 s[0:1], s[2:3]
	s_cbranch_execz .LBB0_10
	s_waitcnt lgkmcnt(6)
	v_add_f32_e32 v40, v40, v41
	v_add_f32_e32 v38, v38, v39
	s_waitcnt lgkmcnt(5)
	v_add_f32_e32 v46, v46, v47
	v_cndmask_b32_e64 v38, v38, v40, s[4:5]
	s_waitcnt lgkmcnt(4)
	v_add_f32_e32 v48, v48, v49
	v_cndmask_b32_e64 v38, v38, v46, s[6:7]
	s_waitcnt lgkmcnt(3)
	v_add_f32_e32 v54, v54, v55
	v_cndmask_b32_e64 v38, v38, v48, s[8:9]
	s_waitcnt lgkmcnt(2)
	v_add_f32_e32 v56, v56, v57
	v_cndmask_b32_e64 v38, v38, v54, s[10:11]
	s_waitcnt lgkmcnt(1)
	v_add_f32_e32 v66, v66, v67
	v_cndmask_b32_e64 v38, v38, v56, s[12:13]
	s_waitcnt lgkmcnt(0)
	v_add_f32_e32 v68, v68, v69
	v_cndmask_b32_e64 v38, v38, v66, s[14:15]
	v_cndmask_b32_e64 v38, v38, v68, s[16:17]
	s_lshl_b64 s[18:19], s[24:25], 5
	v_add_f32_e32 v40, v107, v38
	v_lshl_add_u64 v[38:39], v[102:103], 0, s[18:19]
	global_store_dword v[38:39], v40, off
	s_branch .LBB0_10

; #define LAS __attribute__((address_space(3)))
; #define P7_DMA(s_) do { const unsigned d_ = __builtin_amdgcn_readfirstlane((unsigned)(unsigned long long)(wbuf + ((s_) & 1) * 32768 + F.wave * 1024)); const size_t so_ = (size_t)(s_) * 16384; \
;         P7_G16(rhb + so_, d_); P7_G16(rhb + so_ + 8192, d_ + 8192u); P7_G16(rlb + so_, d_ + 16384u); P7_G16(rlb + so_ + 8192, d_ + 24576u); } while (0)
; #define P7_LOADX(slot, ch_) do { xv[slot][0] = *(const f32x4*)(xp + 64 * (ch_)); xv[slot][1] = *(const f32x4*)(xp + 64 * (ch_) + 4 * DM); xv[slot][2] = *(const f32x4*)(xp + 64 * (ch_) + 8 * DM); xv[slot][3] = *(const f32x4*)(xp + 64 * (ch_) + 12 * DM); } while (0)
; DI void p7_router(Frame& F) {
;     ...
;     for (int t0 = F.vcu * NWAVES; t0 < NTOK / 16; t0 += F.G * NWAVES) {
;         const int tile = t0 + F.wave;
;         const int tok0 = 16 * tile;
;         f32x4 acc0 = {0.f, 0.f, 0.f, 0.f}, acc1 = {0.f, 0.f, 0.f, 0.f};
;         float ss0 = 0.f, ss1 = 0.f, ss2 = 0.f, ss3 = 0.f;
;         const float* xp = X1 + (size_t)(tok0 + g4) * DM + 4 * c;
;         unsigned char* hp = H2 + (size_t)(tok0 + (lane >> 2)) * DM + 16 * (lane & 3);
;         f32x4 xv[4][4];
;         P7_DMA(0);
;         P7_LOADX(0, 0); P7_LOADX(1, 1); P7_LOADX(2, 2);
; #pragma unroll 2
;         for (int sl = 0; sl < 8; ++sl) {
;             asm volatile("s_waitcnt vmcnt(12) lgkmcnt(0)" ::: "memory");
;             __builtin_amdgcn_s_barrier(); asm volatile("" ::: "memory");
;             if (sl + 1 < 8) P7_DMA(sl + 1);
;             const LAS unsigned char* wsl = wbuf + (sl & 1) * 32768 + lane * 16;
; #pragma unroll
;             for (int u = 0; u < 4; ++u) {
;                 const int ch = 4 * sl + u;
;                 { const int cn = (ch + 3 < 32) ? ch + 3 : 31; P7_LOADX((u + 3) & 3, cn); }
;                 __builtin_amdgcn_sched_barrier(0);
;                 const f32x4 gv = *(const LAS f32x4*)(gl + 64 * ch + 4 * c);
;     ...
;                 P7_ROW(xv[u][0], 0, ss0); P7_ROW(xv[u][1], 1, ss1); P7_ROW(xv[u][2], 2, ss2); P7_ROW(xv[u][3], 3, ss3);
.LBB0_858:
	v_readlane_b32 s0, v254, 23
	s_add_i32 s0, s44, s0
	s_lshl_b32 s56, s0, 4
	v_or_b32_e32 v162, s56, v147
	v_ashrrev_i32_e32 v163, 31, v162
	v_lshlrev_b64 v[2:3], 13, v[162:163]
	v_lshl_add_u64 v[164:165], v[144:145], 0, v[2:3]
	v_add_co_u32_e32 v6, vcc, s50, v164
	s_mov_b32 m0, s46
	global_load_lds_dwordx4 v[140:141], off
	s_add_i32 s0, s46, 0x2000
	s_nop 0
	v_addc_co_u32_e32 v7, vcc, 0, v165, vcc
	s_mov_b32 m0, s0
	global_load_lds_dwordx4 v[148:149], off
	v_add_co_u32_e32 v22, vcc, s51, v164
	s_add_i32 s1, s46, 0x4000
	s_mov_b32 m0, s1
	global_load_lds_dwordx4 v[142:143], off
	s_nop 0
	v_addc_co_u32_e32 v23, vcc, 0, v165, vcc
	s_add_i32 s42, s46, 0x6000
	s_mov_b32 m0, s42
	global_load_lds_dwordx4 v[150:151], off
	v_add_co_u32_e32 v34, vcc, 0x18000, v164
	v_ashrrev_i32_e32 v159, 31, v158
	s_nop 0
	v_addc_co_u32_e32 v35, vcc, 0, v165, vcc
	s_waitcnt lgkmcnt(0)
	global_load_dwordx4 v[10:13], v[164:165], off nt
	global_load_dwordx4 v[26:29], v[164:165], off offset:256 nt
	global_load_dwordx4 v[2:5], v[22:23], off nt
	global_load_dwordx4 v[18:21], v[22:23], off offset:256 nt
	global_load_dwordx4 v[14:17], v[6:7], off nt
	global_load_dwordx4 v[66:69], v[164:165], off offset:512 nt
	global_load_dwordx4 v[30:33], v[6:7], off offset:256 nt
	global_load_dwordx4 v[70:73], v[6:7], off offset:512 nt
	s_nop 0
	global_load_dwordx4 v[6:9], v[34:35], off nt
	global_load_dwordx4 v[58:61], v[22:23], off offset:512 nt
	s_nop 0
	global_load_dwordx4 v[22:25], v[34:35], off offset:256 nt
	global_load_dwordx4 v[62:65], v[34:35], off offset:512 nt
	v_ashrrev_i32_e32 v161, 31, v160
	v_lshlrev_b64 v[166:167], 11, v[158:159]
	v_lshlrev_b64 v[34:35], 13, v[160:161]
	v_or_b32_e32 v166, v146, v166
	v_lshl_add_u64 v[168:169], v[144:145], 0, v[34:35]
	s_mov_b64 s[8:9], 0
	s_mov_b32 s43, 7
	v_mov_b32_e32 v159, v192
	v_mov_b64_e32 v[170:171], v[138:139]
	v_mov_b32_e32 v34, 0
	v_mov_b32_e32 v35, v139
	v_mov_b32_e32 v36, v139
	v_mov_b32_e32 v37, v139
	v_mov_b32_e32 v38, 0
	v_mov_b32_e32 v39, v139
	v_mov_b32_e32 v40, v139
	v_mov_b32_e32 v41, v139
	v_mov_b32_e32 v98, 0
	v_mov_b32_e32 v99, v139
	v_mov_b32_e32 v174, 0
	v_mov_b32_e32 v175, v139
	s_branch .LBB0_860
.LBB0_859:
	v_mov_b32_e32 v123, v14
	v_mov_b32_e32 v14, v11
	v_mov_b32_e32 v122, v10
	v_pk_mul_f32 v[10:11], v[14:15], v[14:15]
	v_mov_b32_e32 v15, v16
	v_mov_b32_e32 v16, v13
	v_mov_b32_e32 v14, v12
	v_pk_mul_f32 v[12:13], v[16:17], v[16:17]
	v_pk_fma_f32 v[10:11], v[122:123], v[122:123], v[10:11]
	v_pk_fma_f32 v[12:13], v[14:15], v[14:15], v[12:13]
	s_nop 0
	v_pk_add_f32 v[10:11], v[10:11], v[12:13]
	v_mov_b32_e32 v13, v30
	v_pk_add_f32 v[10:11], v[10:11], v[98:99]
	global_load_dwordx4 v[126:129], v[100:101], off offset:1792 nt
	global_load_dwordx4 v[122:125], v[102:103], off offset:1792 nt
	s_nop 0
	global_load_dwordx4 v[98:101], v[104:105], off offset:1792 nt
	s_nop 0
	global_load_dwordx4 v[102:105], v[176:177], off offset:1792 nt
	v_mov_b32_e32 v30, v27
	v_mov_b32_e32 v12, v26
	v_pk_mul_f32 v[14:15], v[30:31], v[30:31]
	s_nop 0
	v_pk_fma_f32 v[12:13], v[12:13], v[12:13], v[14:15]
	v_mov_b32_e32 v15, v32
	v_mov_b32_e32 v32, v29
	v_mov_b32_e32 v14, v28
	v_pk_mul_f32 v[16:17], v[32:33], v[32:33]
	s_nop 0
	v_pk_fma_f32 v[14:15], v[14:15], v[14:15], v[16:17]
	s_nop 0
	v_pk_add_f32 v[12:13], v[12:13], v[14:15]
	s_nop 0
	v_pk_add_f32 v[10:11], v[12:13], v[10:11]
	v_mov_b32_e32 v13, v70
	v_mov_b32_e32 v70, v67
	v_mov_b32_e32 v12, v66
	v_pk_mul_f32 v[14:15], v[70:71], v[70:71]
	s_nop 0
	v_pk_fma_f32 v[12:13], v[12:13], v[12:13], v[14:15]
	v_mov_b32_e32 v15, v72
	v_mov_b32_e32 v72, v69
	v_mov_b32_e32 v14, v68
	v_pk_mul_f32 v[16:17], v[72:73], v[72:73]
	s_nop 0
	v_pk_fma_f32 v[14:15], v[14:15], v[14:15], v[16:17]
	s_nop 0
	v_pk_add_f32 v[12:13], v[12:13], v[14:15]
	s_nop 0
	v_pk_add_f32 v[10:11], v[12:13], v[10:11]
	v_mov_b32_e32 v13, v118
	v_mov_b32_e32 v118, v115
	v_mov_b32_e32 v12, v114
	v_pk_mul_f32 v[14:15], v[118:119], v[118:119]
	s_nop 0
	v_pk_fma_f32 v[12:13], v[12:13], v[12:13], v[14:15]
	v_mov_b32_e32 v15, v120
	v_mov_b32_e32 v120, v117
	v_mov_b32_e32 v14, v116
	v_pk_mul_f32 v[16:17], v[120:121], v[120:121]
	s_nop 0
	v_pk_fma_f32 v[14:15], v[14:15], v[14:15], v[16:17]
	s_nop 0
	v_pk_add_f32 v[12:13], v[12:13], v[14:15]
	v_mov_b32_e32 v15, v6
	v_mov_b32_e32 v6, v3
	v_mov_b32_e32 v14, v2
	v_pk_mul_f32 v[2:3], v[6:7], v[6:7]
	v_mov_b32_e32 v7, v8
	v_mov_b32_e32 v8, v5
	v_mov_b32_e32 v6, v4
	v_pk_mul_f32 v[4:5], v[8:9], v[8:9]
	v_pk_fma_f32 v[2:3], v[14:15], v[14:15], v[2:3]
	v_pk_fma_f32 v[4:5], v[6:7], v[6:7], v[4:5]
	v_pk_add_f32 v[120:121], v[10:11], v[12:13]
	v_pk_add_f32 v[2:3], v[2:3], v[4:5]
	v_mov_b32_e32 v5, v22
	v_mov_b32_e32 v22, v19
	v_mov_b32_e32 v4, v18
	v_pk_mul_f32 v[6:7], v[22:23], v[22:23]
	v_pk_add_f32 v[2:3], v[2:3], v[174:175]
	v_pk_fma_f32 v[4:5], v[4:5], v[4:5], v[6:7]
	v_mov_b32_e32 v7, v24
	v_mov_b32_e32 v24, v21
	v_mov_b32_e32 v6, v20
	v_pk_mul_f32 v[8:9], v[24:25], v[24:25]
	s_nop 0
	v_pk_fma_f32 v[6:7], v[6:7], v[6:7], v[8:9]
	s_nop 0
	v_pk_add_f32 v[4:5], v[4:5], v[6:7]
	s_nop 0
	v_pk_add_f32 v[2:3], v[4:5], v[2:3]
	v_mov_b32_e32 v5, v62
	v_mov_b32_e32 v62, v59
	v_mov_b32_e32 v4, v58
	v_pk_mul_f32 v[6:7], v[62:63], v[62:63]
	s_nop 0
	v_pk_fma_f32 v[4:5], v[4:5], v[4:5], v[6:7]
	v_mov_b32_e32 v7, v64
	v_mov_b32_e32 v64, v61
	v_mov_b32_e32 v6, v60
	v_pk_mul_f32 v[8:9], v[64:65], v[64:65]
	s_nop 0
	v_pk_fma_f32 v[6:7], v[6:7], v[6:7], v[8:9]
	s_nop 0
	v_pk_add_f32 v[4:5], v[4:5], v[6:7]
	s_nop 0
	v_pk_add_f32 v[2:3], v[4:5], v[2:3]
	v_mov_b32_e32 v5, v110
	v_mov_b32_e32 v110, v107
	v_mov_b32_e32 v4, v106
	v_pk_mul_f32 v[6:7], v[110:111], v[110:111]
	s_nop 0
	v_pk_fma_f32 v[4:5], v[4:5], v[4:5], v[6:7]
	v_mov_b32_e32 v7, v112
	v_mov_b32_e32 v112, v109
	v_mov_b32_e32 v6, v108
	v_pk_mul_f32 v[8:9], v[112:113], v[112:113]
	s_nop 0
	v_pk_fma_f32 v[6:7], v[6:7], v[6:7], v[8:9]
	s_nop 0
	v_pk_add_f32 v[4:5], v[4:5], v[6:7]
	s_nop 0
	v_pk_add_f32 v[118:119], v[2:3], v[4:5]
	ds_read_b128 v[2:5], v159 offset:1024
	v_mov_b32_e32 v10, 0
	s_waitcnt vmcnt(18)
; #define LAS __attribute__((address_space(3)))
; #define P7_LOADX(slot, ch_) do { xv[slot][0] = *(const f32x4*)(xp + 64 * (ch_)); xv[slot][1] = *(const f32x4*)(xp + 64 * (ch_) + 4 * DM); xv[slot][2] = *(const f32x4*)(xp + 64 * (ch_) + 8 * DM); xv[slot][3] = *(const f32x4*)(xp + 64 * (ch_) + 12 * DM); } while (0)
; DI void p7_router(Frame& F) {
;     ...
;                 { const int cn = (ch + 3 < 32) ? ch + 3 : 31; P7_LOADX((u + 3) & 3, cn); }
;                 __builtin_amdgcn_sched_barrier(0);
;                 const f32x4 gv = *(const LAS f32x4*)(gl + 64 * ch + 4 * c);
;     ...
;                 P7_ROW(xv[u][0], 0, ss0); P7_ROW(xv[u][1], 1, ss1); P7_ROW(xv[u][2], 2, ss2); P7_ROW(xv[u][3], 3, ss3);
;     ...
;                 *(u32x4*)(hp + 64 * ch) = *(const LAS u32x4*)(fimg + 16 * lane);
; #pragma unroll
;                 for (int kk = 0; kk < 2; ++kk) {
;                     const bf16x8 bh_ = *(const LAS bf16x8*)(himg + c * 144 + (32 * kk + 8 * g4) * 2), bl_ = *(const LAS bf16x8*)(limg + c * 144 + (32 * kk + 8 * g4) * 2);
;                     const bf16x8 ah0 = *(const LAS bf16x8*)(wsl + u * 4096 + (kk * 2) * 1024), ah1 = *(const LAS bf16x8*)(wsl + u * 4096 + (kk * 2 + 1) * 1024);
;                     const bf16x8 al0 = *(const LAS bf16x8*)(wsl + 16384 + u * 4096 + (kk * 2) * 1024), al1 = *(const LAS bf16x8*)(wsl + 16384 + u * 4096 + (kk * 2 + 1) * 1024);
;                     acc0 = __builtin_amdgcn_mfma_f32_16x16x32_bf16(ah0, bh_, acc0, 0, 0, 0); acc0 = __builtin_amdgcn_mfma_f32_16x16x32_bf16(ah0, bl_, acc0, 0, 0, 0); acc0 = __builtin_amdgcn_mfma_f32_16x16x32_bf16(al0, bh_, acc0, 0, 0, 0);
;                     acc1 = __builtin_amdgcn_mfma_f32_16x16x32_bf16(ah1, bh_, acc1, 0, 0, 0); acc1 = __builtin_amdgcn_mfma_f32_16x16x32_bf16(ah1, bl_, acc1, 0, 0, 0); acc1 = __builtin_amdgcn_mfma_f32_16x16x32_bf16(al1, bh_, acc1, 0, 0, 0);
;                 }
	v_cvt_pk_bf16_f32 v6, v54, v55
	v_mov_b32_e32 v14, 0
	v_cvt_pk_bf16_f32 v7, v56, v57
	s_waitcnt lgkmcnt(0)
	v_pk_mul_f32 v[8:9], v[54:55], v[2:3]
	s_waitcnt vmcnt(17)
	v_pk_mul_f32 v[12:13], v[50:51], v[2:3]
	v_med3_f32 v8, v8, s53, v197
	v_med3_f32 v9, v9, s53, v197
	v_cvt_pk_fp8_f32 v10, v8, v9
	v_pk_mul_f32 v[8:9], v[56:57], v[4:5]
	v_and_b32_e32 v11, 0xffff0000, v7
	v_med3_f32 v8, v8, s53, v197
	v_med3_f32 v9, v9, s53, v197
	v_cvt_pk_fp8_f32 v10, v8, v9 op_sel:[0,0,1]
	v_lshlrev_b32_e32 v8, 16, v6
	v_and_b32_e32 v9, 0xffff0000, v6
	v_pk_add_f32 v[8:9], v[54:55], v[8:9] neg_lo:[0,1] neg_hi:[0,1]
	ds_write_b32 v198, v10 offset:5120
	v_cvt_pk_bf16_f32 v8, v8, v9
	v_med3_f32 v9, v12, s53, v197
	v_med3_f32 v12, v13, s53, v197
	v_cvt_pk_fp8_f32 v14, v9, v12
	v_pk_mul_f32 v[12:13], v[52:53], v[4:5]
	v_lshlrev_b32_e32 v10, 16, v7
	v_med3_f32 v9, v12, s53, v197
	v_med3_f32 v12, v13, s53, v197
	v_cvt_pk_fp8_f32 v14, v9, v12 op_sel:[0,0,1]
	v_pk_add_f32 v[10:11], v[56:57], v[10:11] neg_lo:[0,1] neg_hi:[0,1]
	s_waitcnt vmcnt(16)
	v_pk_mul_f32 v[12:13], v[38:39], v[2:3]
	v_cvt_pk_bf16_f32 v9, v10, v11
	ds_write_b64 v207, v[6:7]
	ds_write_b64 v207, v[8:9] offset:2304
	ds_write_b32 v199, v14 offset:5120
	v_cvt_pk_bf16_f32 v6, v50, v51
	v_lshlrev_b32_e32 v8, 16, v6
	v_and_b32_e32 v9, 0xffff0000, v6
	v_pk_add_f32 v[8:9], v[50:51], v[8:9] neg_lo:[0,1] neg_hi:[0,1]
	v_mov_b32_e32 v14, 0
	v_cvt_pk_bf16_f32 v8, v8, v9
	v_med3_f32 v9, v12, s53, v197
	v_med3_f32 v12, v13, s53, v197
	v_cvt_pk_fp8_f32 v14, v9, v12
	v_pk_mul_f32 v[12:13], v[40:41], v[4:5]
	s_waitcnt vmcnt(15)
	v_pk_mul_f32 v[2:3], v[34:35], v[2:3]
	v_med3_f32 v9, v12, s53, v197
	v_med3_f32 v12, v13, s53, v197
	v_cvt_pk_fp8_f32 v14, v9, v12 op_sel:[0,0,1]
	v_med3_f32 v2, v2, s53, v197
	v_med3_f32 v3, v3, s53, v197
	v_mov_b32_e32 v12, 0
	v_cvt_pk_bf16_f32 v7, v52, v53
	v_cvt_pk_fp8_f32 v12, v2, v3
	v_lshlrev_b32_e32 v10, 16, v7
	v_and_b32_e32 v11, 0xffff0000, v7
	v_pk_add_f32 v[10:11], v[52:53], v[10:11] neg_lo:[0,1] neg_hi:[0,1]
	v_pk_mul_f32 v[2:3], v[36:37], v[4:5]
	v_cvt_pk_bf16_f32 v9, v10, v11
	ds_write_b64 v200, v[6:7]
	ds_write_b64 v200, v[8:9] offset:2304
	ds_write_b32 v201, v14 offset:5120
	v_cvt_pk_bf16_f32 v6, v38, v39
	v_cvt_pk_bf16_f32 v7, v40, v41
	v_med3_f32 v2, v2, s53, v197
	v_med3_f32 v3, v3, s53, v197
	v_lshlrev_b32_e32 v8, 16, v6
	v_and_b32_e32 v9, 0xffff0000, v6
	v_lshlrev_b32_e32 v10, 16, v7
	v_and_b32_e32 v11, 0xffff0000, v7
	v_cvt_pk_fp8_f32 v12, v2, v3 op_sel:[0,0,1]
	v_pk_add_f32 v[8:9], v[38:39], v[8:9] neg_lo:[0,1] neg_hi:[0,1]
	v_pk_add_f32 v[10:11], v[40:41], v[10:11] neg_lo:[0,1] neg_hi:[0,1]
	v_cvt_pk_bf16_f32 v2, v34, v35
	v_cvt_pk_bf16_f32 v3, v36, v37
	v_cvt_pk_bf16_f32 v8, v8, v9
	v_cvt_pk_bf16_f32 v9, v10, v11
	ds_write_b64 v202, v[6:7]
	ds_write_b64 v202, v[8:9] offset:2304
	ds_write_b32 v203, v12 offset:5120
	v_lshlrev_b32_e32 v4, 16, v2
	v_and_b32_e32 v5, 0xffff0000, v2
	v_lshlrev_b32_e32 v6, 16, v3
	v_and_b32_e32 v7, 0xffff0000, v3
	v_pk_add_f32 v[4:5], v[34:35], v[4:5] neg_lo:[0,1] neg_hi:[0,1]
	v_pk_add_f32 v[6:7], v[36:37], v[6:7] neg_lo:[0,1] neg_hi:[0,1]
	v_cvt_pk_bf16_f32 v4, v4, v5
	v_cvt_pk_bf16_f32 v5, v6, v7
	ds_write_b64 v204, v[2:3]
	ds_write_b64 v204, v[4:5] offset:2304
	ds_read_b128 v[2:5], v179 offset:32768
	ds_read_b128 v[6:9], v205
	ds_read_b128 v[10:13], v179 offset:33792
	s_waitcnt lgkmcnt(1)
	v_mfma_f32_16x16x32_bf16 v[14:17], v[2:5], v[6:9], v[134:137]
	ds_read_b128 v[18:21], v205 offset:2304
	ds_read_b128 v[22:25], v205 offset:64
	s_waitcnt lgkmcnt(1)
	v_mfma_f32_16x16x32_bf16 v[2:5], v[2:5], v[18:21], v[14:17]
	s_nop 3
	ds_read_b128 v[14:17], v179 offset:49152
	ds_read_b128 v[26:29], v179 offset:50176
	s_waitcnt lgkmcnt(1)
	v_mfma_f32_16x16x32_bf16 v[2:5], v[14:17], v[6:9], v[2:5]
	v_mfma_f32_16x16x32_bf16 v[14:17], v[10:13], v[6:9], v[130:133]
	v_mfma_f32_16x16x32_bf16 v[10:13], v[10:13], v[18:21], v[14:17]
	s_waitcnt lgkmcnt(0)
	v_mfma_f32_16x16x32_bf16 v[6:9], v[26:29], v[6:9], v[10:13]
	s_nop 5
	ds_read_b128 v[10:13], v179 offset:34816
	ds_read_b128 v[14:17], v179 offset:35840
	ds_read_b128 v[18:21], v205 offset:2368
	s_waitcnt lgkmcnt(2)
	v_mfma_f32_16x16x32_bf16 v[2:5], v[10:13], v[22:25], v[2:5]
	s_waitcnt lgkmcnt(0)
	v_mfma_f32_16x16x32_bf16 v[2:5], v[10:13], v[18:21], v[2:5]
	ds_read_b128 v[10:13], v179 offset:51200
	ds_read_b128 v[26:29], v179 offset:52224
	s_waitcnt lgkmcnt(1)
	v_mfma_f32_16x16x32_bf16 v[30:33], v[10:13], v[22:25], v[2:5]
	v_mfma_f32_16x16x32_bf16 v[2:5], v[14:17], v[22:25], v[6:9]
	v_mfma_f32_16x16x32_bf16 v[2:5], v[14:17], v[18:21], v[2:5]
	s_nop 1
	ds_read_b128 v[6:9], v161 offset:5120
	s_waitcnt lgkmcnt(0)
	global_store_dwordx4 v[172:173], v[6:9], off offset:256
	v_mfma_f32_16x16x32_bf16 v[18:21], v[26:29], v[22:25], v[2:5]
	s_add_i32 s12, s43, -2
	s_min_u32 s12, s12, 28
	s_lshl_b32 s12, s12, 8
	v_lshl_add_u64 v[2:3], v[164:165], 0, s[12:13]
	v_add_co_u32_e32 v4, vcc, s50, v2
	s_nop 1
	v_addc_co_u32_e32 v5, vcc, 0, v3, vcc
	global_load_dwordx4 v[10:13], v[2:3], off offset:768 nt
	global_load_dwordx4 v[14:17], v[4:5], off offset:768 nt
	v_add_co_u32_e32 v4, vcc, s51, v2
	s_nop 1
	v_addc_co_u32_e32 v5, vcc, 0, v3, vcc
	v_add_co_u32_e32 v6, vcc, s52, v2
	s_nop 1
	v_addc_co_u32_e32 v7, vcc, 0, v3, vcc
	global_load_dwordx4 v[2:5], v[4:5], off offset:768 nt
	s_nop 0
	global_load_dwordx4 v[6:9], v[6:7], off offset:768 nt
	ds_read_b128 v[22:25], v159 offset:1280
	v_mov_b32_e32 v58, 0
	s_waitcnt vmcnt(18)
	v_cvt_pk_bf16_f32 v26, v86, v87
	v_mov_b32_e32 v62, 0
	v_cvt_pk_bf16_f32 v27, v88, v89
	s_waitcnt lgkmcnt(0)
	v_pk_mul_f32 v[28:29], v[86:87], v[22:23]
	s_waitcnt vmcnt(17)
; #define LAS __attribute__((address_space(3)))
; #define P7_LOADX(slot, ch_) do { xv[slot][0] = *(const f32x4*)(xp + 64 * (ch_)); xv[slot][1] = *(const f32x4*)(xp + 64 * (ch_) + 4 * DM); xv[slot][2] = *(const f32x4*)(xp + 64 * (ch_) + 8 * DM); xv[slot][3] = *(const f32x4*)(xp + 64 * (ch_) + 12 * DM); } while (0)
; DI void p7_router(Frame& F) {
;     ...
;                 { const int cn = (ch + 3 < 32) ? ch + 3 : 31; P7_LOADX((u + 3) & 3, cn); }
;                 __builtin_amdgcn_sched_barrier(0);
;                 const f32x4 gv = *(const LAS f32x4*)(gl + 64 * ch + 4 * c);
;     ...
;                 P7_ROW(xv[u][0], 0, ss0); P7_ROW(xv[u][1], 1, ss1); P7_ROW(xv[u][2], 2, ss2); P7_ROW(xv[u][3], 3, ss3);
;     ...
;                 *(u32x4*)(hp + 64 * ch) = *(const LAS u32x4*)(fimg + 16 * lane);
; #pragma unroll
;                 for (int kk = 0; kk < 2; ++kk) {
;                     const bf16x8 bh_ = *(const LAS bf16x8*)(himg + c * 144 + (32 * kk + 8 * g4) * 2), bl_ = *(const LAS bf16x8*)(limg + c * 144 + (32 * kk + 8 * g4) * 2);
;                     const bf16x8 ah0 = *(const LAS bf16x8*)(wsl + u * 4096 + (kk * 2) * 1024), ah1 = *(const LAS bf16x8*)(wsl + u * 4096 + (kk * 2 + 1) * 1024);
;                     const bf16x8 al0 = *(const LAS bf16x8*)(wsl + 16384 + u * 4096 + (kk * 2) * 1024), al1 = *(const LAS bf16x8*)(wsl + 16384 + u * 4096 + (kk * 2 + 1) * 1024);
;                     acc0 = __builtin_amdgcn_mfma_f32_16x16x32_bf16(ah0, bh_, acc0, 0, 0, 0); acc0 = __builtin_amdgcn_mfma_f32_16x16x32_bf16(ah0, bl_, acc0, 0, 0, 0); acc0 = __builtin_amdgcn_mfma_f32_16x16x32_bf16(al0, bh_, acc0, 0, 0, 0);
;                     acc1 = __builtin_amdgcn_mfma_f32_16x16x32_bf16(ah1, bh_, acc1, 0, 0, 0); acc1 = __builtin_amdgcn_mfma_f32_16x16x32_bf16(ah1, bl_, acc1, 0, 0, 0); acc1 = __builtin_amdgcn_mfma_f32_16x16x32_bf16(al1, bh_, acc1, 0, 0, 0);
;                 }
	v_pk_mul_f32 v[60:61], v[82:83], v[22:23]
	v_med3_f32 v28, v28, s53, v197
	v_med3_f32 v29, v29, s53, v197
	v_cvt_pk_fp8_f32 v58, v28, v29
	v_pk_mul_f32 v[28:29], v[88:89], v[24:25]
	v_and_b32_e32 v59, 0xffff0000, v27
	v_med3_f32 v28, v28, s53, v197
	v_med3_f32 v29, v29, s53, v197
	v_cvt_pk_fp8_f32 v58, v28, v29 op_sel:[0,0,1]
	v_lshlrev_b32_e32 v28, 16, v26
	v_and_b32_e32 v29, 0xffff0000, v26
	v_pk_add_f32 v[28:29], v[86:87], v[28:29] neg_lo:[0,1] neg_hi:[0,1]
	ds_write_b32 v198, v58 offset:5120
	v_cvt_pk_bf16_f32 v28, v28, v29
	v_med3_f32 v29, v60, s53, v197
	v_med3_f32 v60, v61, s53, v197
	v_cvt_pk_fp8_f32 v62, v29, v60
	v_pk_mul_f32 v[60:61], v[84:85], v[24:25]
	v_lshlrev_b32_e32 v58, 16, v27
	v_med3_f32 v29, v60, s53, v197
	v_med3_f32 v60, v61, s53, v197
	v_cvt_pk_fp8_f32 v62, v29, v60 op_sel:[0,0,1]
	v_pk_add_f32 v[58:59], v[88:89], v[58:59] neg_lo:[0,1] neg_hi:[0,1]
	s_waitcnt vmcnt(16)
	v_pk_mul_f32 v[60:61], v[42:43], v[22:23]
	v_cvt_pk_bf16_f32 v29, v58, v59
	ds_write_b64 v207, v[26:27]
	ds_write_b64 v207, v[28:29] offset:2304
	ds_write_b32 v199, v62 offset:5120
	v_cvt_pk_bf16_f32 v26, v82, v83
	v_lshlrev_b32_e32 v28, 16, v26
	v_and_b32_e32 v29, 0xffff0000, v26
	v_pk_add_f32 v[28:29], v[82:83], v[28:29] neg_lo:[0,1] neg_hi:[0,1]
	v_mov_b32_e32 v62, 0
	v_cvt_pk_bf16_f32 v28, v28, v29
	v_med3_f32 v29, v60, s53, v197
	v_med3_f32 v60, v61, s53, v197
	v_cvt_pk_fp8_f32 v62, v29, v60
	v_pk_mul_f32 v[60:61], v[44:45], v[24:25]
	s_waitcnt vmcnt(15)
	v_pk_mul_f32 v[22:23], v[46:47], v[22:23]
	v_med3_f32 v29, v60, s53, v197
	v_med3_f32 v60, v61, s53, v197
	v_cvt_pk_fp8_f32 v62, v29, v60 op_sel:[0,0,1]
	v_med3_f32 v22, v22, s53, v197
	v_med3_f32 v23, v23, s53, v197
	v_mov_b32_e32 v60, 0
	v_cvt_pk_bf16_f32 v27, v84, v85
	v_cvt_pk_fp8_f32 v60, v22, v23
	v_lshlrev_b32_e32 v58, 16, v27
	v_and_b32_e32 v59, 0xffff0000, v27
	v_pk_add_f32 v[58:59], v[84:85], v[58:59] neg_lo:[0,1] neg_hi:[0,1]
	v_pk_mul_f32 v[22:23], v[48:49], v[24:25]
	v_cvt_pk_bf16_f32 v29, v58, v59
	ds_write_b64 v200, v[26:27]
	ds_write_b64 v200, v[28:29] offset:2304
	ds_write_b32 v201, v62 offset:5120
	v_cvt_pk_bf16_f32 v26, v42, v43
	v_cvt_pk_bf16_f32 v27, v44, v45
	v_med3_f32 v22, v22, s53, v197
	v_med3_f32 v23, v23, s53, v197
	v_lshlrev_b32_e32 v28, 16, v26
	v_and_b32_e32 v29, 0xffff0000, v26
	v_lshlrev_b32_e32 v58, 16, v27
	v_and_b32_e32 v59, 0xffff0000, v27
	v_cvt_pk_fp8_f32 v60, v22, v23 op_sel:[0,0,1]
	v_pk_add_f32 v[28:29], v[42:43], v[28:29] neg_lo:[0,1] neg_hi:[0,1]
	v_pk_add_f32 v[58:59], v[44:45], v[58:59] neg_lo:[0,1] neg_hi:[0,1]
	v_cvt_pk_bf16_f32 v22, v46, v47
	v_cvt_pk_bf16_f32 v23, v48, v49
	v_cvt_pk_bf16_f32 v28, v28, v29
	v_cvt_pk_bf16_f32 v29, v58, v59
	ds_write_b64 v202, v[26:27]
	ds_write_b64 v202, v[28:29] offset:2304
	ds_write_b32 v203, v60 offset:5120
	v_lshlrev_b32_e32 v24, 16, v22
	v_and_b32_e32 v25, 0xffff0000, v22
	v_lshlrev_b32_e32 v26, 16, v23
	v_and_b32_e32 v27, 0xffff0000, v23
	v_pk_add_f32 v[24:25], v[46:47], v[24:25] neg_lo:[0,1] neg_hi:[0,1]
	v_pk_add_f32 v[26:27], v[48:49], v[26:27] neg_lo:[0,1] neg_hi:[0,1]
	v_cvt_pk_bf16_f32 v24, v24, v25
	v_cvt_pk_bf16_f32 v25, v26, v27
	ds_write_b64 v204, v[22:23]
	ds_write_b64 v204, v[24:25] offset:2304
	ds_read_b128 v[22:25], v179 offset:36864
	ds_read_b128 v[26:29], v205
	ds_read_b128 v[58:61], v179 offset:37888
	s_waitcnt lgkmcnt(1)
	v_mfma_f32_16x16x32_bf16 v[30:33], v[22:25], v[26:29], v[30:33]
	ds_read_b128 v[62:65], v205 offset:2304
	ds_read_b128 v[66:69], v205 offset:64
	s_waitcnt lgkmcnt(2)
	v_mfma_f32_16x16x32_bf16 v[18:21], v[58:61], v[26:29], v[18:21]
	s_waitcnt lgkmcnt(1)
	v_mfma_f32_16x16x32_bf16 v[22:25], v[22:25], v[62:65], v[30:33]
	s_nop 2
	ds_read_b128 v[30:33], v179 offset:53248
	ds_read_b128 v[70:73], v179 offset:54272
	v_mfma_f32_16x16x32_bf16 v[18:21], v[58:61], v[62:65], v[18:21]
	s_waitcnt lgkmcnt(1)
	v_mfma_f32_16x16x32_bf16 v[22:25], v[30:33], v[26:29], v[22:25]
	s_waitcnt lgkmcnt(0)
	v_mfma_f32_16x16x32_bf16 v[18:21], v[70:73], v[26:29], v[18:21]
	ds_read_b128 v[26:29], v179 offset:38912
	ds_read_b128 v[30:33], v179 offset:39936
	ds_read_b128 v[58:61], v205 offset:2368
	s_waitcnt lgkmcnt(2)
	v_mfma_f32_16x16x32_bf16 v[22:25], v[26:29], v[66:69], v[22:25]
	s_waitcnt lgkmcnt(1)
	v_mfma_f32_16x16x32_bf16 v[18:21], v[30:33], v[66:69], v[18:21]
	s_waitcnt lgkmcnt(0)
	v_mfma_f32_16x16x32_bf16 v[22:25], v[26:29], v[58:61], v[22:25]
	ds_read_b128 v[26:29], v179 offset:55296
	ds_read_b128 v[62:65], v179 offset:56320
	v_mfma_f32_16x16x32_bf16 v[18:21], v[30:33], v[58:61], v[18:21]
	s_waitcnt lgkmcnt(1)
	v_mfma_f32_16x16x32_bf16 v[70:73], v[26:29], v[66:69], v[22:25]
	s_nop 2
	ds_read_b128 v[22:25], v161 offset:5120
	s_waitcnt lgkmcnt(1)
	v_mfma_f32_16x16x32_bf16 v[58:61], v[62:65], v[66:69], v[18:21]
	s_waitcnt lgkmcnt(0)
	global_store_dwordx4 v[172:173], v[22:25], off offset:320
	s_add_i32 s12, s43, -1
	s_min_u32 s12, s12, 28
	s_lshl_b32 s12, s12, 8
	v_lshl_add_u64 v[18:19], v[164:165], 0, s[12:13]
	v_add_co_u32_e32 v20, vcc, s50, v18
	s_nop 1
	v_addc_co_u32_e32 v21, vcc, 0, v19, vcc
	global_load_dwordx4 v[26:29], v[18:19], off offset:768 nt
	global_load_dwordx4 v[30:33], v[20:21], off offset:768 nt
	v_add_co_u32_e32 v20, vcc, s51, v18
	s_nop 1
	v_addc_co_u32_e32 v21, vcc, 0, v19, vcc
	v_add_co_u32_e32 v22, vcc, s52, v18
	s_nop 1
	v_addc_co_u32_e32 v23, vcc, 0, v19, vcc
	global_load_dwordx4 v[18:21], v[20:21], off offset:768 nt
	s_nop 0
	global_load_dwordx4 v[22:25], v[22:23], off offset:768 nt
	ds_read_b128 v[62:65], v159 offset:1536
	v_mov_b32_e32 v106, 0
	s_waitcnt vmcnt(18)
	v_cvt_pk_bf16_f32 v66, v94, v95
	v_mov_b32_e32 v110, 0
	v_cvt_pk_bf16_f32 v67, v96, v97
	s_waitcnt lgkmcnt(0)
; #define LAS __attribute__((address_space(3)))
; #define P7_LOADX(slot, ch_) do { xv[slot][0] = *(const f32x4*)(xp + 64 * (ch_)); xv[slot][1] = *(const f32x4*)(xp + 64 * (ch_) + 4 * DM); xv[slot][2] = *(const f32x4*)(xp + 64 * (ch_) + 8 * DM); xv[slot][3] = *(const f32x4*)(xp + 64 * (ch_) + 12 * DM); } while (0)
; DI void p7_router(Frame& F) {
;     ...
;                 { const int cn = (ch + 3 < 32) ? ch + 3 : 31; P7_LOADX((u + 3) & 3, cn); }
;                 __builtin_amdgcn_sched_barrier(0);
;                 const f32x4 gv = *(const LAS f32x4*)(gl + 64 * ch + 4 * c);
;     ...
;                 P7_ROW(xv[u][0], 0, ss0); P7_ROW(xv[u][1], 1, ss1); P7_ROW(xv[u][2], 2, ss2); P7_ROW(xv[u][3], 3, ss3);
;     ...
;                 *(u32x4*)(hp + 64 * ch) = *(const LAS u32x4*)(fimg + 16 * lane);
; #pragma unroll
;                 for (int kk = 0; kk < 2; ++kk) {
;                     const bf16x8 bh_ = *(const LAS bf16x8*)(himg + c * 144 + (32 * kk + 8 * g4) * 2), bl_ = *(const LAS bf16x8*)(limg + c * 144 + (32 * kk + 8 * g4) * 2);
;                     const bf16x8 ah0 = *(const LAS bf16x8*)(wsl + u * 4096 + (kk * 2) * 1024), ah1 = *(const LAS bf16x8*)(wsl + u * 4096 + (kk * 2 + 1) * 1024);
;                     const bf16x8 al0 = *(const LAS bf16x8*)(wsl + 16384 + u * 4096 + (kk * 2) * 1024), al1 = *(const LAS bf16x8*)(wsl + 16384 + u * 4096 + (kk * 2 + 1) * 1024);
;                     acc0 = __builtin_amdgcn_mfma_f32_16x16x32_bf16(ah0, bh_, acc0, 0, 0, 0); acc0 = __builtin_amdgcn_mfma_f32_16x16x32_bf16(ah0, bl_, acc0, 0, 0, 0); acc0 = __builtin_amdgcn_mfma_f32_16x16x32_bf16(al0, bh_, acc0, 0, 0, 0);
;                     acc1 = __builtin_amdgcn_mfma_f32_16x16x32_bf16(ah1, bh_, acc1, 0, 0, 0); acc1 = __builtin_amdgcn_mfma_f32_16x16x32_bf16(ah1, bl_, acc1, 0, 0, 0); acc1 = __builtin_amdgcn_mfma_f32_16x16x32_bf16(al1, bh_, acc1, 0, 0, 0);
;                 }
	v_pk_mul_f32 v[68:69], v[94:95], v[62:63]
	s_waitcnt vmcnt(17)
	v_pk_mul_f32 v[108:109], v[90:91], v[62:63]
	v_med3_f32 v68, v68, s53, v197
	v_med3_f32 v69, v69, s53, v197
	v_cvt_pk_fp8_f32 v106, v68, v69
	v_pk_mul_f32 v[68:69], v[96:97], v[64:65]
	v_and_b32_e32 v107, 0xffff0000, v67
	v_med3_f32 v68, v68, s53, v197
	v_med3_f32 v69, v69, s53, v197
	v_cvt_pk_fp8_f32 v106, v68, v69 op_sel:[0,0,1]
	v_lshlrev_b32_e32 v68, 16, v66
	v_and_b32_e32 v69, 0xffff0000, v66
	v_pk_add_f32 v[68:69], v[94:95], v[68:69] neg_lo:[0,1] neg_hi:[0,1]
	ds_write_b32 v198, v106 offset:5120
	v_cvt_pk_bf16_f32 v68, v68, v69
	v_med3_f32 v69, v108, s53, v197
	v_med3_f32 v108, v109, s53, v197
	v_cvt_pk_fp8_f32 v110, v69, v108
	v_pk_mul_f32 v[108:109], v[92:93], v[64:65]
	v_lshlrev_b32_e32 v106, 16, v67
	v_med3_f32 v69, v108, s53, v197
	v_med3_f32 v108, v109, s53, v197
	v_cvt_pk_fp8_f32 v110, v69, v108 op_sel:[0,0,1]
	v_pk_add_f32 v[106:107], v[96:97], v[106:107] neg_lo:[0,1] neg_hi:[0,1]
	s_waitcnt vmcnt(16)
	v_pk_mul_f32 v[108:109], v[74:75], v[62:63]
	v_cvt_pk_bf16_f32 v69, v106, v107
	ds_write_b64 v207, v[66:67]
	ds_write_b64 v207, v[68:69] offset:2304
	ds_write_b32 v199, v110 offset:5120
	v_cvt_pk_bf16_f32 v66, v90, v91
	v_lshlrev_b32_e32 v68, 16, v66
	v_and_b32_e32 v69, 0xffff0000, v66
	v_pk_add_f32 v[68:69], v[90:91], v[68:69] neg_lo:[0,1] neg_hi:[0,1]
	v_mov_b32_e32 v110, 0
	v_cvt_pk_bf16_f32 v68, v68, v69
	v_med3_f32 v69, v108, s53, v197
	v_med3_f32 v108, v109, s53, v197
	v_cvt_pk_fp8_f32 v110, v69, v108
	v_pk_mul_f32 v[108:109], v[76:77], v[64:65]
	s_waitcnt vmcnt(15)
	v_pk_mul_f32 v[62:63], v[78:79], v[62:63]
	v_med3_f32 v69, v108, s53, v197
	v_med3_f32 v108, v109, s53, v197
	v_cvt_pk_fp8_f32 v110, v69, v108 op_sel:[0,0,1]
	v_med3_f32 v62, v62, s53, v197
	v_med3_f32 v63, v63, s53, v197
	v_mov_b32_e32 v108, 0
	v_cvt_pk_bf16_f32 v67, v92, v93
	v_cvt_pk_fp8_f32 v108, v62, v63
	v_lshlrev_b32_e32 v106, 16, v67
	v_and_b32_e32 v107, 0xffff0000, v67
	v_pk_add_f32 v[106:107], v[92:93], v[106:107] neg_lo:[0,1] neg_hi:[0,1]
	v_pk_mul_f32 v[62:63], v[80:81], v[64:65]
	v_cvt_pk_bf16_f32 v69, v106, v107
	ds_write_b64 v200, v[66:67]
	ds_write_b64 v200, v[68:69] offset:2304
	ds_write_b32 v201, v110 offset:5120
	v_cvt_pk_bf16_f32 v66, v74, v75
	v_cvt_pk_bf16_f32 v67, v76, v77
	v_med3_f32 v62, v62, s53, v197
	v_med3_f32 v63, v63, s53, v197
	v_lshlrev_b32_e32 v68, 16, v66
	v_and_b32_e32 v69, 0xffff0000, v66
	v_lshlrev_b32_e32 v106, 16, v67
	v_and_b32_e32 v107, 0xffff0000, v67
	v_cvt_pk_fp8_f32 v108, v62, v63 op_sel:[0,0,1]
	v_pk_add_f32 v[68:69], v[74:75], v[68:69] neg_lo:[0,1] neg_hi:[0,1]
	v_pk_add_f32 v[106:107], v[76:77], v[106:107] neg_lo:[0,1] neg_hi:[0,1]
	v_cvt_pk_bf16_f32 v62, v78, v79
	v_cvt_pk_bf16_f32 v63, v80, v81
	v_cvt_pk_bf16_f32 v68, v68, v69
	v_cvt_pk_bf16_f32 v69, v106, v107
	ds_write_b64 v202, v[66:67]
	ds_write_b64 v202, v[68:69] offset:2304
	ds_write_b32 v203, v108 offset:5120
	v_lshlrev_b32_e32 v64, 16, v62
	v_and_b32_e32 v65, 0xffff0000, v62
	v_lshlrev_b32_e32 v66, 16, v63
	v_and_b32_e32 v67, 0xffff0000, v63
	v_pk_add_f32 v[64:65], v[78:79], v[64:65] neg_lo:[0,1] neg_hi:[0,1]
	v_pk_add_f32 v[66:67], v[80:81], v[66:67] neg_lo:[0,1] neg_hi:[0,1]
	v_cvt_pk_bf16_f32 v64, v64, v65
	v_cvt_pk_bf16_f32 v65, v66, v67
	ds_write_b64 v204, v[62:63]
	ds_write_b64 v204, v[64:65] offset:2304
	ds_read_b128 v[62:65], v179 offset:40960
	ds_read_b128 v[66:69], v205
	ds_read_b128 v[106:109], v179 offset:41984
	s_waitcnt lgkmcnt(1)
	v_mfma_f32_16x16x32_bf16 v[70:73], v[62:65], v[66:69], v[70:73]
	ds_read_b128 v[110:113], v205 offset:2304
	ds_read_b128 v[114:117], v205 offset:64
	s_waitcnt lgkmcnt(2)
	v_mfma_f32_16x16x32_bf16 v[58:61], v[106:109], v[66:69], v[58:61]
	s_waitcnt lgkmcnt(1)
	v_mfma_f32_16x16x32_bf16 v[62:65], v[62:65], v[110:113], v[70:73]
	s_nop 2
	ds_read_b128 v[70:73], v179 offset:57344
	ds_read_b128 v[130:133], v179 offset:58368
	v_mfma_f32_16x16x32_bf16 v[58:61], v[106:109], v[110:113], v[58:61]
	s_waitcnt lgkmcnt(1)
	v_mfma_f32_16x16x32_bf16 v[62:65], v[70:73], v[66:69], v[62:65]
	s_waitcnt lgkmcnt(0)
	v_mfma_f32_16x16x32_bf16 v[58:61], v[130:133], v[66:69], v[58:61]
	ds_read_b128 v[66:69], v179 offset:43008
	ds_read_b128 v[70:73], v179 offset:44032
	ds_read_b128 v[106:109], v205 offset:2368
	s_waitcnt lgkmcnt(2)
	v_mfma_f32_16x16x32_bf16 v[62:65], v[66:69], v[114:117], v[62:65]
	s_waitcnt lgkmcnt(0)
	v_mfma_f32_16x16x32_bf16 v[62:65], v[66:69], v[106:109], v[62:65]
	ds_read_b128 v[66:69], v179 offset:59392
	ds_read_b128 v[130:133], v179 offset:60416
	v_mfma_f32_16x16x32_bf16 v[58:61], v[70:73], v[114:117], v[58:61]
	s_waitcnt lgkmcnt(1)
	v_mfma_f32_16x16x32_bf16 v[110:113], v[66:69], v[114:117], v[62:65]
	s_nop 2
	ds_read_b128 v[62:65], v161 offset:5120
	v_mfma_f32_16x16x32_bf16 v[58:61], v[70:73], v[106:109], v[58:61]
	s_waitcnt lgkmcnt(0)
	global_store_dwordx4 v[172:173], v[62:65], off offset:384
	v_mfma_f32_16x16x32_bf16 v[106:109], v[130:133], v[114:117], v[58:61]
	s_min_u32 s12, s43, 28
	s_lshl_b32 s12, s12, 8
	s_nop 2
	v_lshl_add_u64 v[58:59], v[164:165], 0, s[12:13]
	v_add_co_u32_e32 v60, vcc, s50, v58
	s_nop 1
	v_addc_co_u32_e32 v61, vcc, 0, v59, vcc
	global_load_dwordx4 v[66:69], v[58:59], off offset:768 nt
	global_load_dwordx4 v[70:73], v[60:61], off offset:768 nt
	v_add_co_u32_e32 v60, vcc, s51, v58
	s_nop 1
	v_addc_co_u32_e32 v61, vcc, 0, v59, vcc
	v_add_co_u32_e32 v62, vcc, s52, v58
	s_nop 1
	v_addc_co_u32_e32 v63, vcc, 0, v59, vcc
	global_load_dwordx4 v[58:61], v[60:61], off offset:768 nt
	s_nop 0
	global_load_dwordx4 v[62:65], v[62:63], off offset:768 nt
	ds_read_b128 v[114:117], v159 offset:1792
	v_mov_b32_e32 v134, 0
	s_waitcnt vmcnt(18)
; #define LAS __attribute__((address_space(3)))
; #define P7_LOADX(slot, ch_) do { xv[slot][0] = *(const f32x4*)(xp + 64 * (ch_)); xv[slot][1] = *(const f32x4*)(xp + 64 * (ch_) + 4 * DM); xv[slot][2] = *(const f32x4*)(xp + 64 * (ch_) + 8 * DM); xv[slot][3] = *(const f32x4*)(xp + 64 * (ch_) + 12 * DM); } while (0)
; DI void p7_router(Frame& F) {
;     ...
;             for (int u = 0; u < 4; ++u) {
;                 const int ch = 4 * sl + u;
;                 { const int cn = (ch + 3 < 32) ? ch + 3 : 31; P7_LOADX((u + 3) & 3, cn); }
;                 __builtin_amdgcn_sched_barrier(0);
;                 const f32x4 gv = *(const LAS f32x4*)(gl + 64 * ch + 4 * c);
;     ...
;                 P7_ROW(xv[u][0], 0, ss0); P7_ROW(xv[u][1], 1, ss1); P7_ROW(xv[u][2], 2, ss2); P7_ROW(xv[u][3], 3, ss3);
;     ...
;                 *(u32x4*)(hp + 64 * ch) = *(const LAS u32x4*)(fimg + 16 * lane);
	v_cvt_pk_bf16_f32 v130, v126, v127
	v_cvt_pk_bf16_f32 v131, v128, v129
	v_and_b32_e32 v135, 0xffff0000, v131
	s_waitcnt lgkmcnt(0)
	v_pk_mul_f32 v[132:133], v[126:127], v[114:115]
	s_nop 0
	v_med3_f32 v132, v132, s53, v197
	v_med3_f32 v133, v133, s53, v197
	v_cvt_pk_fp8_f32 v134, v132, v133
	v_pk_mul_f32 v[132:133], v[128:129], v[116:117]
	s_nop 0
	v_med3_f32 v132, v132, s53, v197
	v_med3_f32 v133, v133, s53, v197
	v_cvt_pk_fp8_f32 v134, v132, v133 op_sel:[0,0,1]
	v_lshlrev_b32_e32 v132, 16, v130
	v_and_b32_e32 v133, 0xffff0000, v130
	v_pk_add_f32 v[132:133], v[126:127], v[132:133] neg_lo:[0,1] neg_hi:[0,1]
	ds_write_b32 v198, v134 offset:5120
	v_lshlrev_b32_e32 v134, 16, v131
	v_pk_add_f32 v[134:135], v[128:129], v[134:135] neg_lo:[0,1] neg_hi:[0,1]
	v_cvt_pk_bf16_f32 v132, v132, v133
	v_cvt_pk_bf16_f32 v133, v134, v135
	ds_write_b64 v207, v[130:131]
	ds_write_b64 v207, v[132:133] offset:2304
	v_mov_b32_e32 v131, v50
	v_mov_b32_e32 v50, v55
	v_mov_b32_e32 v55, v52
	v_mov_b32_e32 v52, v57
	v_mov_b32_e32 v130, v54
	v_pk_mul_f32 v[50:51], v[50:51], v[50:51]
	v_mov_b32_e32 v54, v56
	v_pk_mul_f32 v[52:53], v[52:53], v[52:53]
	v_pk_fma_f32 v[50:51], v[130:131], v[130:131], v[50:51]
	v_pk_fma_f32 v[52:53], v[54:55], v[54:55], v[52:53]
	s_nop 0
	v_pk_add_f32 v[50:51], v[50:51], v[52:53]
	v_mov_b32_e32 v53, v82
	v_mov_b32_e32 v82, v87
	v_mov_b32_e32 v52, v86
	v_pk_mul_f32 v[54:55], v[82:83], v[82:83]
	v_pk_add_f32 v[50:51], v[50:51], v[120:121]
	v_pk_fma_f32 v[52:53], v[52:53], v[52:53], v[54:55]
	v_mov_b32_e32 v55, v84
	v_mov_b32_e32 v84, v89
	v_mov_b32_e32 v54, v88
	v_pk_mul_f32 v[56:57], v[84:85], v[84:85]
	s_waitcnt vmcnt(17)
	v_pk_mul_f32 v[82:83], v[122:123], v[114:115]
	v_pk_fma_f32 v[54:55], v[54:55], v[54:55], v[56:57]
	v_med3_f32 v82, v82, s53, v197
	v_pk_add_f32 v[52:53], v[52:53], v[54:55]
	v_med3_f32 v83, v83, s53, v197
	v_pk_add_f32 v[50:51], v[52:53], v[50:51]
	v_mov_b32_e32 v53, v90
	v_mov_b32_e32 v90, v95
	v_mov_b32_e32 v52, v94
	v_pk_mul_f32 v[54:55], v[90:91], v[90:91]
	v_mov_b32_e32 v84, 0
	v_pk_fma_f32 v[52:53], v[52:53], v[52:53], v[54:55]
	v_mov_b32_e32 v55, v92
	v_mov_b32_e32 v92, v97
	v_mov_b32_e32 v54, v96
	v_pk_mul_f32 v[56:57], v[92:93], v[92:93]
	v_cvt_pk_fp8_f32 v84, v82, v83
	v_pk_fma_f32 v[54:55], v[54:55], v[54:55], v[56:57]
	v_pk_mul_f32 v[82:83], v[124:125], v[116:117]
	v_pk_add_f32 v[52:53], v[52:53], v[54:55]
	v_mov_b32_e32 v54, v127
	v_mov_b32_e32 v55, v123
	v_pk_add_f32 v[50:51], v[52:53], v[50:51]
	v_mov_b32_e32 v52, v126
	v_mov_b32_e32 v53, v122
	v_pk_mul_f32 v[54:55], v[54:55], v[54:55]
	v_mov_b32_e32 v56, v129
	v_mov_b32_e32 v57, v125
	v_med3_f32 v82, v82, s53, v197
	v_med3_f32 v83, v83, s53, v197
	v_pk_fma_f32 v[52:53], v[52:53], v[52:53], v[54:55]
	v_mov_b32_e32 v54, v128
	v_mov_b32_e32 v55, v124
	v_cvt_pk_fp8_f32 v84, v82, v83 op_sel:[0,0,1]
	v_pk_mul_f32 v[56:57], v[56:57], v[56:57]
	v_mov_b32_e32 v86, 0
	v_pk_fma_f32 v[54:55], v[54:55], v[54:55], v[56:57]
	ds_write_b32 v199, v84 offset:5120
	v_pk_add_f32 v[56:57], v[52:53], v[54:55]
	v_cvt_pk_bf16_f32 v52, v122, v123
	v_lshlrev_b32_e32 v54, 16, v52
	v_and_b32_e32 v55, 0xffff0000, v52
	v_pk_add_f32 v[54:55], v[122:123], v[54:55] neg_lo:[0,1] neg_hi:[0,1]
	s_waitcnt vmcnt(16)
	v_pk_mul_f32 v[84:85], v[98:99], v[114:115]
	v_cvt_pk_bf16_f32 v54, v54, v55
	v_med3_f32 v55, v84, s53, v197
	v_med3_f32 v84, v85, s53, v197
	v_cvt_pk_fp8_f32 v86, v55, v84
	v_pk_mul_f32 v[84:85], v[100:101], v[116:117]
	v_cvt_pk_bf16_f32 v53, v124, v125
	v_med3_f32 v55, v84, s53, v197
	v_med3_f32 v84, v85, s53, v197
	v_lshlrev_b32_e32 v82, 16, v53
	v_and_b32_e32 v83, 0xffff0000, v53
	v_cvt_pk_fp8_f32 v86, v55, v84 op_sel:[0,0,1]
	v_pk_add_f32 v[82:83], v[124:125], v[82:83] neg_lo:[0,1] neg_hi:[0,1]
	v_mov_b32_e32 v97, v78
	v_cvt_pk_bf16_f32 v55, v82, v83
	ds_write_b64 v200, v[52:53]
	ds_write_b64 v200, v[54:55] offset:2304
	ds_write_b32 v201, v86 offset:5120
	v_cvt_pk_bf16_f32 v52, v98, v99
	v_cvt_pk_bf16_f32 v53, v100, v101
	v_lshlrev_b32_e32 v54, 16, v52
	v_and_b32_e32 v55, 0xffff0000, v52
	v_lshlrev_b32_e32 v82, 16, v53
	v_and_b32_e32 v83, 0xffff0000, v53
	v_pk_add_f32 v[54:55], v[98:99], v[54:55] neg_lo:[0,1] neg_hi:[0,1]
	v_pk_add_f32 v[82:83], v[100:101], v[82:83] neg_lo:[0,1] neg_hi:[0,1]
	v_cvt_pk_bf16_f32 v54, v54, v55
	v_cvt_pk_bf16_f32 v55, v82, v83
	ds_write_b64 v202, v[52:53]
	ds_write_b64 v202, v[54:55] offset:2304
	v_mov_b32_e32 v53, v34
	v_mov_b32_e32 v34, v39
	v_mov_b32_e32 v39, v36
	v_mov_b32_e32 v36, v41
	v_mov_b32_e32 v52, v38
	v_pk_mul_f32 v[34:35], v[34:35], v[34:35]
	v_mov_b32_e32 v38, v40
	v_pk_mul_f32 v[36:37], v[36:37], v[36:37]
	v_pk_fma_f32 v[34:35], v[52:53], v[52:53], v[34:35]
	v_pk_fma_f32 v[36:37], v[38:39], v[38:39], v[36:37]
	v_mov_b32_e32 v40, v44
	v_pk_add_f32 v[34:35], v[34:35], v[36:37]
	v_mov_b32_e32 v41, v48
	v_pk_add_f32 v[52:53], v[34:35], v[118:119]
	v_mov_b32_e32 v35, v46
	v_mov_b32_e32 v46, v43
	v_mov_b32_e32 v34, v42
	v_pk_mul_f32 v[36:37], v[46:47], v[46:47]
	v_mov_b32_e32 v48, v45
	v_pk_fma_f32 v[38:39], v[34:35], v[34:35], v[36:37]
	s_waitcnt vmcnt(15)
	v_pk_mul_f32 v[34:35], v[102:103], v[114:115]
	v_mov_b32_e32 v36, 0
	v_med3_f32 v34, v34, s53, v197
	v_med3_f32 v35, v35, s53, v197
	v_cvt_pk_fp8_f32 v36, v34, v35
	v_pk_mul_f32 v[34:35], v[104:105], v[116:117]
	v_pk_mul_f32 v[42:43], v[48:49], v[48:49]
	v_med3_f32 v34, v34, s53, v197
	v_med3_f32 v35, v35, s53, v197
	v_cvt_pk_fp8_f32 v36, v34, v35 op_sel:[0,0,1]
	v_cvt_pk_bf16_f32 v34, v102, v103
	v_cvt_pk_bf16_f32 v35, v104, v105
	v_and_b32_e32 v37, 0xffff0000, v34
	ds_write_b32 v203, v36 offset:5120
	v_lshlrev_b32_e32 v36, 16, v34
	v_lshlrev_b32_e32 v44, 16, v35
	v_and_b32_e32 v45, 0xffff0000, v35
	v_pk_add_f32 v[36:37], v[102:103], v[36:37] neg_lo:[0,1] neg_hi:[0,1]
	v_pk_add_f32 v[44:45], v[104:105], v[44:45] neg_lo:[0,1] neg_hi:[0,1]
	v_cvt_pk_bf16_f32 v36, v36, v37
	v_cvt_pk_bf16_f32 v37, v44, v45
	ds_write_b64 v204, v[34:35]
	ds_write_b64 v204, v[36:37] offset:2304
	ds_read_b128 v[34:37], v179 offset:45056
	v_pk_fma_f32 v[40:41], v[40:41], v[40:41], v[42:43]
	v_mov_b32_e32 v78, v75
	v_pk_add_f32 v[46:47], v[38:39], v[40:41]
	ds_read_b128 v[38:41], v161 offset:5120
	ds_read_b128 v[42:45], v205
	s_waitcnt lgkmcnt(0)
; #define LAS __attribute__((address_space(3)))
; #define P7_DMA(s_) do { const unsigned d_ = __builtin_amdgcn_readfirstlane((unsigned)(unsigned long long)(wbuf + ((s_) & 1) * 32768 + F.wave * 1024)); const size_t so_ = (size_t)(s_) * 16384; \
;         P7_G16(rhb + so_, d_); P7_G16(rhb + so_ + 8192, d_ + 8192u); P7_G16(rlb + so_, d_ + 16384u); P7_G16(rlb + so_ + 8192, d_ + 24576u); } while (0)
; DI void p7_router(Frame& F) {
;     ...
; #pragma unroll 2
;         for (int sl = 0; sl < 8; ++sl) {
;             asm volatile("s_waitcnt vmcnt(12) lgkmcnt(0)" ::: "memory");
;             __builtin_amdgcn_s_barrier(); asm volatile("" ::: "memory");
;             if (sl + 1 < 8) P7_DMA(sl + 1);
;             const LAS unsigned char* wsl = wbuf + (sl & 1) * 32768 + lane * 16;
; #pragma unroll
;             for (int u = 0; u < 4; ++u) {
;                 const int ch = 4 * sl + u;
;                 { const int cn = (ch + 3 < 32) ? ch + 3 : 31; P7_LOADX((u + 3) & 3, cn); }
;                 __builtin_amdgcn_sched_barrier(0);
;                 const f32x4 gv = *(const LAS f32x4*)(gl + 64 * ch + 4 * c);
;     ...
;                 P7_ROW(xv[u][0], 0, ss0); P7_ROW(xv[u][1], 1, ss1); P7_ROW(xv[u][2], 2, ss2); P7_ROW(xv[u][3], 3, ss3);
;     ...
;                 *(u32x4*)(hp + 64 * ch) = *(const LAS u32x4*)(fimg + 16 * lane);
; #pragma unroll
;                 for (int kk = 0; kk < 2; ++kk) {
;                     const bf16x8 bh_ = *(const LAS bf16x8*)(himg + c * 144 + (32 * kk + 8 * g4) * 2), bl_ = *(const LAS bf16x8*)(limg + c * 144 + (32 * kk + 8 * g4) * 2);
;                     const bf16x8 ah0 = *(const LAS bf16x8*)(wsl + u * 4096 + (kk * 2) * 1024), ah1 = *(const LAS bf16x8*)(wsl + u * 4096 + (kk * 2 + 1) * 1024);
;                     const bf16x8 al0 = *(const LAS bf16x8*)(wsl + 16384 + u * 4096 + (kk * 2) * 1024), al1 = *(const LAS bf16x8*)(wsl + 16384 + u * 4096 + (kk * 2 + 1) * 1024);
;                     acc0 = __builtin_amdgcn_mfma_f32_16x16x32_bf16(ah0, bh_, acc0, 0, 0, 0); acc0 = __builtin_amdgcn_mfma_f32_16x16x32_bf16(ah0, bl_, acc0, 0, 0, 0); acc0 = __builtin_amdgcn_mfma_f32_16x16x32_bf16(al0, bh_, acc0, 0, 0, 0);
;                     acc1 = __builtin_amdgcn_mfma_f32_16x16x32_bf16(ah1, bh_, acc1, 0, 0, 0); acc1 = __builtin_amdgcn_mfma_f32_16x16x32_bf16(ah1, bl_, acc1, 0, 0, 0); acc1 = __builtin_amdgcn_mfma_f32_16x16x32_bf16(al1, bh_, acc1, 0, 0, 0);
;                 }
	v_mfma_f32_16x16x32_bf16 v[86:89], v[34:37], v[42:45], v[110:113]
	v_add_f32_e64 v94, v46, v52
	v_add_f32_e64 v95, v47, v53
	ds_read_b128 v[46:49], v205 offset:2304
	ds_read_b128 v[52:55], v179 offset:46080
	ds_read_b128 v[82:85], v179 offset:61440
	v_mov_b32_e32 v96, v74
	s_waitcnt lgkmcnt(2)
	v_mfma_f32_16x16x32_bf16 v[34:37], v[34:37], v[46:49], v[86:89]
	v_mul_f32_e64 v74, v78, v78
	v_mul_f32_e64 v75, v79, v79
	ds_read_b128 v[90:93], v205 offset:64
	ds_read_b128 v[86:89], v179 offset:62464
	v_pk_fma_f32 v[78:79], v[96:97], v[96:97], v[74:75]
	v_mov_b32_e32 v96, v76
	v_mov_b32_e32 v97, v80
	v_mov_b32_e32 v80, v77
	ds_read_b128 v[74:77], v179 offset:47104
	s_waitcnt lgkmcnt(3)
	v_mfma_f32_16x16x32_bf16 v[34:37], v[82:85], v[42:45], v[34:37]
	v_mul_f32_e64 v80, v80, v80
	v_mul_f32_e64 v81, v81, v81
	v_mfma_f32_16x16x32_bf16 v[82:85], v[52:55], v[42:45], v[106:109]
	v_mfma_f32_16x16x32_bf16 v[46:49], v[52:55], v[46:49], v[82:85]
	v_fma_f32 v52, v96, v96, v80
	v_fma_f32 v53, v97, v97, v81
	v_pk_add_f32 v[52:53], v[78:79], v[52:53]
	s_waitcnt lgkmcnt(0)
	v_mfma_f32_16x16x32_bf16 v[34:37], v[74:77], v[90:93], v[34:37]
	s_nop 1
	v_add_f32_e64 v82, v52, v94
	v_add_f32_e64 v83, v53, v95
	v_mov_b32_e32 v84, v98
	v_mov_b32_e32 v85, v102
	v_mfma_f32_16x16x32_bf16 v[42:45], v[86:89], v[42:45], v[46:49]
	s_nop 2
	ds_read_b128 v[46:49], v205 offset:2368
	ds_read_b128 v[52:55], v179 offset:48128
	ds_read_b128 v[78:81], v179 offset:63488
	v_mov_b32_e32 v86, v99
	v_mov_b32_e32 v87, v103
	s_waitcnt lgkmcnt(2)
	v_mfma_f32_16x16x32_bf16 v[34:37], v[74:77], v[46:49], v[34:37]
	ds_read_b128 v[74:77], v179 offset:64512
	v_pk_mul_f32 v[86:87], v[86:87], v[86:87]
	global_store_dwordx4 v[172:173], v[38:41], off offset:448
	s_waitcnt lgkmcnt(2)
	v_mfma_f32_16x16x32_bf16 v[42:45], v[52:55], v[90:93], v[42:45]
	v_add_f32_e64 v98, v50, v56
	v_add_f32_e64 v99, v51, v57
	v_mfma_f32_16x16x32_bf16 v[42:45], v[52:55], v[46:49], v[42:45]
	s_waitcnt lgkmcnt(1)
	v_mfma_f32_16x16x32_bf16 v[34:37], v[78:81], v[90:93], v[34:37]
	v_fma_f32 v78, v84, v84, v86
	v_fma_f32 v79, v85, v85, v87
	v_mov_b32_e32 v84, v101
	v_mov_b32_e32 v85, v105
	v_mov_b32_e32 v80, v100
	v_mov_b32_e32 v81, v104
	v_pk_mul_f32 v[84:85], v[84:85], v[84:85]
	s_waitcnt lgkmcnt(0)
	v_mfma_f32_16x16x32_bf16 v[38:41], v[74:77], v[90:93], v[42:45]
	v_fma_f32 v46, v80, v80, v84
	v_fma_f32 v47, v81, v81, v85
	v_pk_add_f32 v[46:47], v[78:79], v[46:47]
	s_nop 0
	v_pk_add_f32 v[174:175], v[82:83], v[46:47]
	s_add_u32 s8, s8, 0x800
	s_addc_u32 s9, s9, 0
	s_add_i32 s43, s43, 8
	v_lshl_add_u64 v[170:171], v[170:171], 0, s[38:39]
	v_add_u32_e32 v159, 0x800, v159
	s_cmpk_eq_i32 s8, 0x2000
	v_lshl_add_u64 v[166:167], v[166:167], 0, s[40:41]
	s_cbranch_scc1 .LBB0_862
.LBB0_860:
	v_lshl_add_u64 v[100:101], v[168:169], 0, s[8:9]
	s_waitcnt vmcnt(12) lgkmcnt(0)
	s_barrier
	v_lshl_add_u64 v[122:123], s[94:95], 0, v[170:171]
	v_add_co_u32_e32 v102, vcc, s50, v100
	v_lshl_add_u64 v[42:43], v[122:123], 0, s[20:21]
	s_mov_b32 m0, s48
	global_load_lds_dwordx4 v[42:43], off
	s_nop 0
	v_addc_co_u32_e32 v103, vcc, 0, v101, vcc
	v_lshl_add_u64 v[42:43], v[122:123], 0, s[22:23]
	s_add_i32 s12, s48, 0x2000
	s_mov_b32 m0, s12
	global_load_lds_dwordx4 v[42:43], off
	v_add_co_u32_e32 v104, vcc, s51, v100
	v_lshl_add_u64 v[42:43], v[122:123], 0, s[24:25]
	s_add_i32 s12, s48, 0x4000
	s_mov_b32 m0, s12
	global_load_lds_dwordx4 v[42:43], off
	v_addc_co_u32_e32 v105, vcc, 0, v101, vcc
	v_lshl_add_u64 v[42:43], v[122:123], 0, s[26:27]
	s_add_i32 s12, s48, 0x6000
	s_mov_b32 m0, s12
	global_load_lds_dwordx4 v[42:43], off
	v_add_co_u32_e32 v176, vcc, s52, v100
	global_load_dwordx4 v[114:117], v[100:101], off offset:768 nt
	global_load_dwordx4 v[118:121], v[102:103], off offset:768 nt
	v_addc_co_u32_e32 v177, vcc, 0, v101, vcc
	global_load_dwordx4 v[106:109], v[104:105], off offset:768 nt
	global_load_dwordx4 v[110:113], v[176:177], off offset:768 nt
	ds_read_b128 v[42:45], v159
	v_mov_b32_e32 v50, 0
	s_waitcnt vmcnt(15)
	v_cvt_pk_bf16_f32 v46, v10, v11
	v_cvt_pk_bf16_f32 v47, v12, v13
	v_and_b32_e32 v51, 0xffff0000, v47
	s_waitcnt lgkmcnt(0)
	v_pk_mul_f32 v[48:49], v[10:11], v[42:43]
	v_mov_b32_e32 v52, 0
	v_med3_f32 v48, v48, s53, v197
	v_med3_f32 v49, v49, s53, v197
	v_cvt_pk_fp8_f32 v50, v48, v49
	v_pk_mul_f32 v[48:49], v[12:13], v[44:45]
	v_add_u32_e32 v207, v180, v181
	v_med3_f32 v48, v48, s53, v197
	v_med3_f32 v49, v49, s53, v197
	v_cvt_pk_fp8_f32 v50, v48, v49 op_sel:[0,0,1]
	v_lshlrev_b32_e32 v48, 16, v46
	v_and_b32_e32 v49, 0xffff0000, v46
	v_pk_add_f32 v[48:49], v[10:11], v[48:49] neg_lo:[0,1] neg_hi:[0,1]
	ds_write_b32 v198, v50 offset:5120
	v_lshlrev_b32_e32 v50, 16, v47
	v_pk_add_f32 v[50:51], v[12:13], v[50:51] neg_lo:[0,1] neg_hi:[0,1]
	v_cvt_pk_bf16_f32 v48, v48, v49
	v_cvt_pk_bf16_f32 v49, v50, v51
	s_waitcnt vmcnt(11)
	v_pk_mul_f32 v[50:51], v[14:15], v[42:43]
	v_mov_b32_e32 v54, 0
	v_med3_f32 v50, v50, s53, v197
	v_med3_f32 v51, v51, s53, v197
	v_cvt_pk_fp8_f32 v52, v50, v51
	v_pk_mul_f32 v[50:51], v[16:17], v[44:45]
	v_add_u32_e32 v161, s45, v153
	v_med3_f32 v50, v50, s53, v197
	v_med3_f32 v51, v51, s53, v197
	v_cvt_pk_fp8_f32 v52, v50, v51 op_sel:[0,0,1]
	ds_write_b64 v207, v[46:47]
	ds_write_b64 v207, v[48:49] offset:2304
	ds_write_b32 v199, v52 offset:5120
	v_cvt_pk_bf16_f32 v46, v14, v15
	v_lshlrev_b32_e32 v48, 16, v46
	v_and_b32_e32 v49, 0xffff0000, v46
	v_pk_add_f32 v[48:49], v[14:15], v[48:49] neg_lo:[0,1] neg_hi:[0,1]
	v_pk_mul_f32 v[52:53], v[2:3], v[42:43]
	v_cvt_pk_bf16_f32 v48, v48, v49
	v_med3_f32 v49, v52, s53, v197
	v_med3_f32 v52, v53, s53, v197
	v_cvt_pk_fp8_f32 v54, v49, v52
	v_pk_mul_f32 v[52:53], v[4:5], v[44:45]
	s_waitcnt vmcnt(7)
; #define LAS __attribute__((address_space(3)))
; #define P7_LOADX(slot, ch_) do { xv[slot][0] = *(const f32x4*)(xp + 64 * (ch_)); xv[slot][1] = *(const f32x4*)(xp + 64 * (ch_) + 4 * DM); xv[slot][2] = *(const f32x4*)(xp + 64 * (ch_) + 8 * DM); xv[slot][3] = *(const f32x4*)(xp + 64 * (ch_) + 12 * DM); } while (0)
; DI void p7_router(Frame& F) {
;     ...
;             for (int u = 0; u < 4; ++u) {
;                 const int ch = 4 * sl + u;
;                 { const int cn = (ch + 3 < 32) ? ch + 3 : 31; P7_LOADX((u + 3) & 3, cn); }
;                 __builtin_amdgcn_sched_barrier(0);
;                 const f32x4 gv = *(const LAS f32x4*)(gl + 64 * ch + 4 * c);
;     ...
;                 P7_ROW(xv[u][0], 0, ss0); P7_ROW(xv[u][1], 1, ss1); P7_ROW(xv[u][2], 2, ss2); P7_ROW(xv[u][3], 3, ss3);
;     ...
;                 *(u32x4*)(hp + 64 * ch) = *(const LAS u32x4*)(fimg + 16 * lane);
; #pragma unroll
;                 for (int kk = 0; kk < 2; ++kk) {
;                     const bf16x8 bh_ = *(const LAS bf16x8*)(himg + c * 144 + (32 * kk + 8 * g4) * 2), bl_ = *(const LAS bf16x8*)(limg + c * 144 + (32 * kk + 8 * g4) * 2);
;                     const bf16x8 ah0 = *(const LAS bf16x8*)(wsl + u * 4096 + (kk * 2) * 1024), ah1 = *(const LAS bf16x8*)(wsl + u * 4096 + (kk * 2 + 1) * 1024);
;                     const bf16x8 al0 = *(const LAS bf16x8*)(wsl + 16384 + u * 4096 + (kk * 2) * 1024), al1 = *(const LAS bf16x8*)(wsl + 16384 + u * 4096 + (kk * 2 + 1) * 1024);
;                     acc0 = __builtin_amdgcn_mfma_f32_16x16x32_bf16(ah0, bh_, acc0, 0, 0, 0); acc0 = __builtin_amdgcn_mfma_f32_16x16x32_bf16(ah0, bl_, acc0, 0, 0, 0); acc0 = __builtin_amdgcn_mfma_f32_16x16x32_bf16(al0, bh_, acc0, 0, 0, 0);
;                     acc1 = __builtin_amdgcn_mfma_f32_16x16x32_bf16(ah1, bh_, acc1, 0, 0, 0); acc1 = __builtin_amdgcn_mfma_f32_16x16x32_bf16(ah1, bl_, acc1, 0, 0, 0); acc1 = __builtin_amdgcn_mfma_f32_16x16x32_bf16(al1, bh_, acc1, 0, 0, 0);
;                 }
	v_pk_mul_f32 v[42:43], v[6:7], v[42:43]
	v_med3_f32 v49, v52, s53, v197
	v_med3_f32 v52, v53, s53, v197
	v_cvt_pk_fp8_f32 v54, v49, v52 op_sel:[0,0,1]
	v_med3_f32 v42, v42, s53, v197
	v_med3_f32 v43, v43, s53, v197
	v_mov_b32_e32 v52, 0
	v_cvt_pk_bf16_f32 v47, v16, v17
	v_cvt_pk_fp8_f32 v52, v42, v43
	v_lshlrev_b32_e32 v50, 16, v47
	v_and_b32_e32 v51, 0xffff0000, v47
	v_pk_add_f32 v[50:51], v[16:17], v[50:51] neg_lo:[0,1] neg_hi:[0,1]
	v_pk_mul_f32 v[42:43], v[8:9], v[44:45]
	v_cvt_pk_bf16_f32 v49, v50, v51
	ds_write_b64 v200, v[46:47]
	ds_write_b64 v200, v[48:49] offset:2304
	ds_write_b32 v201, v54 offset:5120
	v_cvt_pk_bf16_f32 v46, v2, v3
	v_cvt_pk_bf16_f32 v47, v4, v5
	v_med3_f32 v42, v42, s53, v197
	v_med3_f32 v43, v43, s53, v197
	v_lshlrev_b32_e32 v48, 16, v46
	v_and_b32_e32 v49, 0xffff0000, v46
	v_lshlrev_b32_e32 v50, 16, v47
	v_and_b32_e32 v51, 0xffff0000, v47
	v_cvt_pk_fp8_f32 v52, v42, v43 op_sel:[0,0,1]
	v_pk_add_f32 v[48:49], v[2:3], v[48:49] neg_lo:[0,1] neg_hi:[0,1]
	v_pk_add_f32 v[50:51], v[4:5], v[50:51] neg_lo:[0,1] neg_hi:[0,1]
	v_cvt_pk_bf16_f32 v42, v6, v7
	v_cvt_pk_bf16_f32 v43, v8, v9
	v_cvt_pk_bf16_f32 v48, v48, v49
	v_cvt_pk_bf16_f32 v49, v50, v51
	ds_write_b64 v202, v[46:47]
	ds_write_b64 v202, v[48:49] offset:2304
	ds_write_b32 v203, v52 offset:5120
	v_lshlrev_b32_e32 v44, 16, v42
	v_and_b32_e32 v45, 0xffff0000, v42
	v_lshlrev_b32_e32 v46, 16, v43
	v_and_b32_e32 v47, 0xffff0000, v43
	v_pk_add_f32 v[44:45], v[6:7], v[44:45] neg_lo:[0,1] neg_hi:[0,1]
	v_pk_add_f32 v[46:47], v[8:9], v[46:47] neg_lo:[0,1] neg_hi:[0,1]
	v_cvt_pk_bf16_f32 v44, v44, v45
	v_cvt_pk_bf16_f32 v45, v46, v47
	ds_write_b64 v204, v[42:43]
	ds_write_b64 v204, v[44:45] offset:2304
	ds_read_b128 v[42:45], v178 offset:57344
	ds_read_b128 v[46:49], v205
	ds_read_b128 v[50:53], v178 offset:58368
	s_waitcnt lgkmcnt(1)
	v_mfma_f32_16x16x32_bf16 v[34:37], v[42:45], v[46:49], v[34:37]
	ds_read_b128 v[54:57], v205 offset:2304
	ds_read_b128 v[74:77], v205 offset:64
	s_waitcnt lgkmcnt(2)
	v_mfma_f32_16x16x32_bf16 v[38:41], v[50:53], v[46:49], v[38:41]
	s_waitcnt lgkmcnt(1)
	v_mfma_f32_16x16x32_bf16 v[34:37], v[42:45], v[54:57], v[34:37]
	ds_read_b128 v[42:45], v179 offset:16384
	ds_read_b128 v[78:81], v179 offset:17408
	v_mfma_f32_16x16x32_bf16 v[38:41], v[50:53], v[54:57], v[38:41]
	s_waitcnt lgkmcnt(1)
	v_mfma_f32_16x16x32_bf16 v[34:37], v[42:45], v[46:49], v[34:37]
	s_waitcnt lgkmcnt(0)
	v_mfma_f32_16x16x32_bf16 v[38:41], v[78:81], v[46:49], v[38:41]
	ds_read_b128 v[42:45], v178 offset:59392
	ds_read_b128 v[46:49], v178 offset:60416
	ds_read_b128 v[50:53], v205 offset:2368
	v_lshl_add_u64 v[78:79], s[94:95], 0, v[166:167]
	s_waitcnt lgkmcnt(2)
	v_mfma_f32_16x16x32_bf16 v[34:37], v[42:45], v[74:77], v[34:37]
	v_add_co_u32_e32 v172, vcc, s54, v78
	s_waitcnt lgkmcnt(0)
	v_mfma_f32_16x16x32_bf16 v[34:37], v[42:45], v[50:53], v[34:37]
	ds_read_b128 v[42:45], v179 offset:18432
	ds_read_b128 v[54:57], v179 offset:19456
	v_addc_co_u32_e32 v173, vcc, 0, v79, vcc
	s_waitcnt lgkmcnt(1)
	v_mfma_f32_16x16x32_bf16 v[42:45], v[42:45], v[74:77], v[34:37]
	v_mfma_f32_16x16x32_bf16 v[34:37], v[46:49], v[74:77], v[38:41]
	v_mfma_f32_16x16x32_bf16 v[34:37], v[46:49], v[50:53], v[34:37]
	s_nop 1
	ds_read_b128 v[38:41], v161 offset:5120
	s_waitcnt lgkmcnt(0)
	global_store_dwordx4 v[172:173], v[38:41], off
	v_mfma_f32_16x16x32_bf16 v[46:49], v[54:57], v[74:77], v[34:37]
	global_load_dwordx4 v[54:57], v[100:101], off offset:1024 nt
	global_load_dwordx4 v[50:53], v[102:103], off offset:1024 nt
	global_load_dwordx4 v[38:41], v[104:105], off offset:1024 nt
	global_load_dwordx4 v[34:37], v[176:177], off offset:1024 nt
	ds_read_b128 v[74:77], v159 offset:256
	v_mov_b32_e32 v82, 0
	v_cvt_pk_bf16_f32 v78, v26, v27
	v_mov_b32_e32 v86, 0
	v_cvt_pk_bf16_f32 v79, v28, v29
	s_waitcnt lgkmcnt(0)
	v_pk_mul_f32 v[80:81], v[26:27], v[74:75]
	v_pk_mul_f32 v[84:85], v[30:31], v[74:75]
	v_med3_f32 v80, v80, s53, v197
	v_med3_f32 v81, v81, s53, v197
	v_cvt_pk_fp8_f32 v82, v80, v81
	v_pk_mul_f32 v[80:81], v[28:29], v[76:77]
	v_and_b32_e32 v83, 0xffff0000, v79
	v_med3_f32 v80, v80, s53, v197
	v_med3_f32 v81, v81, s53, v197
	v_cvt_pk_fp8_f32 v82, v80, v81 op_sel:[0,0,1]
	v_lshlrev_b32_e32 v80, 16, v78
	v_and_b32_e32 v81, 0xffff0000, v78
	v_pk_add_f32 v[80:81], v[26:27], v[80:81] neg_lo:[0,1] neg_hi:[0,1]
	ds_write_b32 v198, v82 offset:5120
	v_cvt_pk_bf16_f32 v80, v80, v81
	v_med3_f32 v81, v84, s53, v197
	v_med3_f32 v84, v85, s53, v197
	v_cvt_pk_fp8_f32 v86, v81, v84
	v_pk_mul_f32 v[84:85], v[32:33], v[76:77]
	v_lshlrev_b32_e32 v82, 16, v79
	v_med3_f32 v81, v84, s53, v197
	v_med3_f32 v84, v85, s53, v197
	v_cvt_pk_fp8_f32 v86, v81, v84 op_sel:[0,0,1]
	v_pk_add_f32 v[82:83], v[28:29], v[82:83] neg_lo:[0,1] neg_hi:[0,1]
	v_pk_mul_f32 v[84:85], v[18:19], v[74:75]
	v_cvt_pk_bf16_f32 v81, v82, v83
	ds_write_b64 v207, v[78:79]
	ds_write_b64 v207, v[80:81] offset:2304
	ds_write_b32 v199, v86 offset:5120
	v_cvt_pk_bf16_f32 v78, v30, v31
	v_lshlrev_b32_e32 v80, 16, v78
	v_and_b32_e32 v81, 0xffff0000, v78
	v_pk_add_f32 v[80:81], v[30:31], v[80:81] neg_lo:[0,1] neg_hi:[0,1]
	v_mov_b32_e32 v86, 0
	v_cvt_pk_bf16_f32 v80, v80, v81
	v_med3_f32 v81, v84, s53, v197
	v_med3_f32 v84, v85, s53, v197
	v_cvt_pk_fp8_f32 v86, v81, v84
	v_pk_mul_f32 v[84:85], v[20:21], v[76:77]
	s_waitcnt vmcnt(10)
; #define LAS __attribute__((address_space(3)))
; #define P7_LOADX(slot, ch_) do { xv[slot][0] = *(const f32x4*)(xp + 64 * (ch_)); xv[slot][1] = *(const f32x4*)(xp + 64 * (ch_) + 4 * DM); xv[slot][2] = *(const f32x4*)(xp + 64 * (ch_) + 8 * DM); xv[slot][3] = *(const f32x4*)(xp + 64 * (ch_) + 12 * DM); } while (0)
; DI void p7_router(Frame& F) {
;     ...
;             for (int u = 0; u < 4; ++u) {
;                 const int ch = 4 * sl + u;
;                 { const int cn = (ch + 3 < 32) ? ch + 3 : 31; P7_LOADX((u + 3) & 3, cn); }
;                 __builtin_amdgcn_sched_barrier(0);
;                 const f32x4 gv = *(const LAS f32x4*)(gl + 64 * ch + 4 * c);
;     ...
;                 P7_ROW(xv[u][0], 0, ss0); P7_ROW(xv[u][1], 1, ss1); P7_ROW(xv[u][2], 2, ss2); P7_ROW(xv[u][3], 3, ss3);
;     ...
;                 *(u32x4*)(hp + 64 * ch) = *(const LAS u32x4*)(fimg + 16 * lane);
; #pragma unroll
;                 for (int kk = 0; kk < 2; ++kk) {
;                     const bf16x8 bh_ = *(const LAS bf16x8*)(himg + c * 144 + (32 * kk + 8 * g4) * 2), bl_ = *(const LAS bf16x8*)(limg + c * 144 + (32 * kk + 8 * g4) * 2);
;                     const bf16x8 ah0 = *(const LAS bf16x8*)(wsl + u * 4096 + (kk * 2) * 1024), ah1 = *(const LAS bf16x8*)(wsl + u * 4096 + (kk * 2 + 1) * 1024);
;                     const bf16x8 al0 = *(const LAS bf16x8*)(wsl + 16384 + u * 4096 + (kk * 2) * 1024), al1 = *(const LAS bf16x8*)(wsl + 16384 + u * 4096 + (kk * 2 + 1) * 1024);
;                     acc0 = __builtin_amdgcn_mfma_f32_16x16x32_bf16(ah0, bh_, acc0, 0, 0, 0); acc0 = __builtin_amdgcn_mfma_f32_16x16x32_bf16(ah0, bl_, acc0, 0, 0, 0); acc0 = __builtin_amdgcn_mfma_f32_16x16x32_bf16(al0, bh_, acc0, 0, 0, 0);
;                     acc1 = __builtin_amdgcn_mfma_f32_16x16x32_bf16(ah1, bh_, acc1, 0, 0, 0); acc1 = __builtin_amdgcn_mfma_f32_16x16x32_bf16(ah1, bl_, acc1, 0, 0, 0); acc1 = __builtin_amdgcn_mfma_f32_16x16x32_bf16(al1, bh_, acc1, 0, 0, 0);
;                 }
	v_pk_mul_f32 v[74:75], v[22:23], v[74:75]
	v_med3_f32 v81, v84, s53, v197
	v_med3_f32 v84, v85, s53, v197
	v_cvt_pk_fp8_f32 v86, v81, v84 op_sel:[0,0,1]
	v_med3_f32 v74, v74, s53, v197
	v_med3_f32 v75, v75, s53, v197
	v_mov_b32_e32 v84, 0
	v_cvt_pk_bf16_f32 v79, v32, v33
	v_cvt_pk_fp8_f32 v84, v74, v75
	v_lshlrev_b32_e32 v82, 16, v79
	v_and_b32_e32 v83, 0xffff0000, v79
	v_pk_add_f32 v[82:83], v[32:33], v[82:83] neg_lo:[0,1] neg_hi:[0,1]
	v_pk_mul_f32 v[74:75], v[24:25], v[76:77]
	v_cvt_pk_bf16_f32 v81, v82, v83
	ds_write_b64 v200, v[78:79]
	ds_write_b64 v200, v[80:81] offset:2304
	ds_write_b32 v201, v86 offset:5120
	v_cvt_pk_bf16_f32 v78, v18, v19
	v_cvt_pk_bf16_f32 v79, v20, v21
	v_med3_f32 v74, v74, s53, v197
	v_med3_f32 v75, v75, s53, v197
	v_lshlrev_b32_e32 v80, 16, v78
	v_and_b32_e32 v81, 0xffff0000, v78
	v_lshlrev_b32_e32 v82, 16, v79
	v_and_b32_e32 v83, 0xffff0000, v79
	v_cvt_pk_fp8_f32 v84, v74, v75 op_sel:[0,0,1]
	v_pk_add_f32 v[80:81], v[18:19], v[80:81] neg_lo:[0,1] neg_hi:[0,1]
	v_pk_add_f32 v[82:83], v[20:21], v[82:83] neg_lo:[0,1] neg_hi:[0,1]
	v_cvt_pk_bf16_f32 v74, v22, v23
	v_cvt_pk_bf16_f32 v75, v24, v25
	v_cvt_pk_bf16_f32 v80, v80, v81
	v_cvt_pk_bf16_f32 v81, v82, v83
	ds_write_b64 v202, v[78:79]
	ds_write_b64 v202, v[80:81] offset:2304
	ds_write_b32 v203, v84 offset:5120
	v_lshlrev_b32_e32 v76, 16, v74
	v_and_b32_e32 v77, 0xffff0000, v74
	v_lshlrev_b32_e32 v78, 16, v75
	v_and_b32_e32 v79, 0xffff0000, v75
	v_pk_add_f32 v[76:77], v[22:23], v[76:77] neg_lo:[0,1] neg_hi:[0,1]
	v_pk_add_f32 v[78:79], v[24:25], v[78:79] neg_lo:[0,1] neg_hi:[0,1]
	v_cvt_pk_bf16_f32 v76, v76, v77
	v_cvt_pk_bf16_f32 v77, v78, v79
	ds_write_b64 v204, v[74:75]
	ds_write_b64 v204, v[76:77] offset:2304
	ds_read_b128 v[74:77], v178 offset:61440
	ds_read_b128 v[78:81], v205
	ds_read_b128 v[82:85], v178 offset:62464
	s_waitcnt lgkmcnt(1)
	v_mfma_f32_16x16x32_bf16 v[42:45], v[74:77], v[78:81], v[42:45]
	ds_read_b128 v[86:89], v205 offset:2304
	ds_read_b128 v[90:93], v205 offset:64
	s_waitcnt lgkmcnt(2)
	v_mfma_f32_16x16x32_bf16 v[46:49], v[82:85], v[78:81], v[46:49]
	s_waitcnt lgkmcnt(1)
	v_mfma_f32_16x16x32_bf16 v[42:45], v[74:77], v[86:89], v[42:45]
	ds_read_b128 v[74:77], v179 offset:20480
	ds_read_b128 v[94:97], v179 offset:21504
	v_mfma_f32_16x16x32_bf16 v[46:49], v[82:85], v[86:89], v[46:49]
	s_waitcnt lgkmcnt(1)
	v_mfma_f32_16x16x32_bf16 v[42:45], v[74:77], v[78:81], v[42:45]
	s_waitcnt lgkmcnt(0)
	v_mfma_f32_16x16x32_bf16 v[46:49], v[94:97], v[78:81], v[46:49]
	ds_read_b128 v[74:77], v178 offset:63488
	ds_read_b128 v[78:81], v178 offset:64512
	ds_read_b128 v[82:85], v205 offset:2368
	s_waitcnt lgkmcnt(2)
	v_mfma_f32_16x16x32_bf16 v[42:45], v[74:77], v[90:93], v[42:45]
	s_waitcnt lgkmcnt(0)
	v_mfma_f32_16x16x32_bf16 v[42:45], v[74:77], v[82:85], v[42:45]
	ds_read_b128 v[74:77], v179 offset:22528
	ds_read_b128 v[86:89], v179 offset:23552
	s_waitcnt lgkmcnt(1)
	v_mfma_f32_16x16x32_bf16 v[74:77], v[74:77], v[90:93], v[42:45]
	v_mfma_f32_16x16x32_bf16 v[42:45], v[78:81], v[90:93], v[46:49]
	v_mfma_f32_16x16x32_bf16 v[42:45], v[78:81], v[82:85], v[42:45]
	s_nop 1
	ds_read_b128 v[46:49], v161 offset:5120
	s_waitcnt lgkmcnt(0)
	global_store_dwordx4 v[172:173], v[46:49], off offset:64
	v_mfma_f32_16x16x32_bf16 v[78:81], v[86:89], v[90:93], v[42:45]
	global_load_dwordx4 v[86:89], v[100:101], off offset:1280 nt
	global_load_dwordx4 v[82:85], v[102:103], off offset:1280 nt
	s_nop 0
	global_load_dwordx4 v[42:45], v[104:105], off offset:1280 nt
	global_load_dwordx4 v[46:49], v[176:177], off offset:1280 nt
	ds_read_b128 v[90:93], v159 offset:512
	v_mov_b32_e32 v124, 0
	v_cvt_pk_bf16_f32 v94, v66, v67
	v_mov_b32_e32 v128, 0
	v_cvt_pk_bf16_f32 v95, v68, v69
	s_waitcnt lgkmcnt(0)
	v_pk_mul_f32 v[96:97], v[66:67], v[90:91]
	v_pk_mul_f32 v[126:127], v[70:71], v[90:91]
	v_med3_f32 v96, v96, s53, v197
	v_med3_f32 v97, v97, s53, v197
	v_cvt_pk_fp8_f32 v124, v96, v97
	v_pk_mul_f32 v[96:97], v[68:69], v[92:93]
	v_and_b32_e32 v125, 0xffff0000, v95
	v_med3_f32 v96, v96, s53, v197
	v_med3_f32 v97, v97, s53, v197
	v_cvt_pk_fp8_f32 v124, v96, v97 op_sel:[0,0,1]
	v_lshlrev_b32_e32 v96, 16, v94
	v_and_b32_e32 v97, 0xffff0000, v94
	v_pk_add_f32 v[96:97], v[66:67], v[96:97] neg_lo:[0,1] neg_hi:[0,1]
	ds_write_b32 v198, v124 offset:5120
	v_cvt_pk_bf16_f32 v96, v96, v97
	v_med3_f32 v97, v126, s53, v197
	v_med3_f32 v126, v127, s53, v197
	v_cvt_pk_fp8_f32 v128, v97, v126
	v_pk_mul_f32 v[126:127], v[72:73], v[92:93]
	v_lshlrev_b32_e32 v124, 16, v95
	v_med3_f32 v97, v126, s53, v197
	v_med3_f32 v126, v127, s53, v197
	v_cvt_pk_fp8_f32 v128, v97, v126 op_sel:[0,0,1]
	v_pk_add_f32 v[124:125], v[68:69], v[124:125] neg_lo:[0,1] neg_hi:[0,1]
	v_pk_mul_f32 v[126:127], v[58:59], v[90:91]
	v_cvt_pk_bf16_f32 v97, v124, v125
	ds_write_b64 v207, v[94:95]
	ds_write_b64 v207, v[96:97] offset:2304
	ds_write_b32 v199, v128 offset:5120
	v_cvt_pk_bf16_f32 v94, v70, v71
	v_lshlrev_b32_e32 v96, 16, v94
	v_and_b32_e32 v97, 0xffff0000, v94
	v_pk_add_f32 v[96:97], v[70:71], v[96:97] neg_lo:[0,1] neg_hi:[0,1]
	v_mov_b32_e32 v128, 0
	v_cvt_pk_bf16_f32 v96, v96, v97
	v_med3_f32 v97, v126, s53, v197
	v_med3_f32 v126, v127, s53, v197
	v_cvt_pk_fp8_f32 v128, v97, v126
	v_pk_mul_f32 v[126:127], v[60:61], v[92:93]
	s_waitcnt vmcnt(14)
; #define LAS __attribute__((address_space(3)))
; #define P7_LOADX(slot, ch_) do { xv[slot][0] = *(const f32x4*)(xp + 64 * (ch_)); xv[slot][1] = *(const f32x4*)(xp + 64 * (ch_) + 4 * DM); xv[slot][2] = *(const f32x4*)(xp + 64 * (ch_) + 8 * DM); xv[slot][3] = *(const f32x4*)(xp + 64 * (ch_) + 12 * DM); } while (0)
; DI void p7_router(Frame& F) {
;     ...
;             for (int u = 0; u < 4; ++u) {
;                 const int ch = 4 * sl + u;
;                 { const int cn = (ch + 3 < 32) ? ch + 3 : 31; P7_LOADX((u + 3) & 3, cn); }
;                 __builtin_amdgcn_sched_barrier(0);
;                 const f32x4 gv = *(const LAS f32x4*)(gl + 64 * ch + 4 * c);
;     ...
;                 P7_ROW(xv[u][0], 0, ss0); P7_ROW(xv[u][1], 1, ss1); P7_ROW(xv[u][2], 2, ss2); P7_ROW(xv[u][3], 3, ss3);
;     ...
;                 *(u32x4*)(hp + 64 * ch) = *(const LAS u32x4*)(fimg + 16 * lane);
; #pragma unroll
;                 for (int kk = 0; kk < 2; ++kk) {
;                     const bf16x8 bh_ = *(const LAS bf16x8*)(himg + c * 144 + (32 * kk + 8 * g4) * 2), bl_ = *(const LAS bf16x8*)(limg + c * 144 + (32 * kk + 8 * g4) * 2);
;                     const bf16x8 ah0 = *(const LAS bf16x8*)(wsl + u * 4096 + (kk * 2) * 1024), ah1 = *(const LAS bf16x8*)(wsl + u * 4096 + (kk * 2 + 1) * 1024);
;                     const bf16x8 al0 = *(const LAS bf16x8*)(wsl + 16384 + u * 4096 + (kk * 2) * 1024), al1 = *(const LAS bf16x8*)(wsl + 16384 + u * 4096 + (kk * 2 + 1) * 1024);
;                     acc0 = __builtin_amdgcn_mfma_f32_16x16x32_bf16(ah0, bh_, acc0, 0, 0, 0); acc0 = __builtin_amdgcn_mfma_f32_16x16x32_bf16(ah0, bl_, acc0, 0, 0, 0); acc0 = __builtin_amdgcn_mfma_f32_16x16x32_bf16(al0, bh_, acc0, 0, 0, 0);
;                     acc1 = __builtin_amdgcn_mfma_f32_16x16x32_bf16(ah1, bh_, acc1, 0, 0, 0); acc1 = __builtin_amdgcn_mfma_f32_16x16x32_bf16(ah1, bl_, acc1, 0, 0, 0); acc1 = __builtin_amdgcn_mfma_f32_16x16x32_bf16(al1, bh_, acc1, 0, 0, 0);
;                 }
	v_pk_mul_f32 v[90:91], v[62:63], v[90:91]
	v_med3_f32 v97, v126, s53, v197
	v_med3_f32 v126, v127, s53, v197
	v_cvt_pk_fp8_f32 v128, v97, v126 op_sel:[0,0,1]
	v_med3_f32 v90, v90, s53, v197
	v_med3_f32 v91, v91, s53, v197
	v_mov_b32_e32 v126, 0
	v_cvt_pk_bf16_f32 v95, v72, v73
	v_cvt_pk_fp8_f32 v126, v90, v91
	v_lshlrev_b32_e32 v124, 16, v95
	v_and_b32_e32 v125, 0xffff0000, v95
	v_pk_add_f32 v[124:125], v[72:73], v[124:125] neg_lo:[0,1] neg_hi:[0,1]
	v_pk_mul_f32 v[90:91], v[64:65], v[92:93]
	v_cvt_pk_bf16_f32 v97, v124, v125
	ds_write_b64 v200, v[94:95]
	ds_write_b64 v200, v[96:97] offset:2304
	ds_write_b32 v201, v128 offset:5120
	v_cvt_pk_bf16_f32 v94, v58, v59
	v_cvt_pk_bf16_f32 v95, v60, v61
	v_med3_f32 v90, v90, s53, v197
	v_med3_f32 v91, v91, s53, v197
	v_lshlrev_b32_e32 v96, 16, v94
	v_and_b32_e32 v97, 0xffff0000, v94
	v_lshlrev_b32_e32 v124, 16, v95
	v_and_b32_e32 v125, 0xffff0000, v95
	v_cvt_pk_fp8_f32 v126, v90, v91 op_sel:[0,0,1]
	v_pk_add_f32 v[96:97], v[58:59], v[96:97] neg_lo:[0,1] neg_hi:[0,1]
	v_pk_add_f32 v[124:125], v[60:61], v[124:125] neg_lo:[0,1] neg_hi:[0,1]
	v_cvt_pk_bf16_f32 v90, v62, v63
	v_cvt_pk_bf16_f32 v91, v64, v65
	v_cvt_pk_bf16_f32 v96, v96, v97
	v_cvt_pk_bf16_f32 v97, v124, v125
	ds_write_b64 v202, v[94:95]
	ds_write_b64 v202, v[96:97] offset:2304
	ds_write_b32 v203, v126 offset:5120
	v_lshlrev_b32_e32 v92, 16, v90
	v_and_b32_e32 v93, 0xffff0000, v90
	v_lshlrev_b32_e32 v94, 16, v91
	v_and_b32_e32 v95, 0xffff0000, v91
	v_pk_add_f32 v[92:93], v[62:63], v[92:93] neg_lo:[0,1] neg_hi:[0,1]
	v_pk_add_f32 v[94:95], v[64:65], v[94:95] neg_lo:[0,1] neg_hi:[0,1]
	v_cvt_pk_bf16_f32 v92, v92, v93
	v_cvt_pk_bf16_f32 v93, v94, v95
	ds_write_b64 v204, v[90:91]
	ds_write_b64 v204, v[92:93] offset:2304
	ds_read_b128 v[90:93], v179 offset:8192
	ds_read_b128 v[94:97], v205
	ds_read_b128 v[124:127], v179 offset:9216
	s_waitcnt lgkmcnt(1)
	v_mfma_f32_16x16x32_bf16 v[74:77], v[90:93], v[94:97], v[74:77]
	ds_read_b128 v[128:131], v205 offset:2304
	ds_read_b128 v[132:135], v205 offset:64
	s_waitcnt lgkmcnt(2)
	v_mfma_f32_16x16x32_bf16 v[78:81], v[124:127], v[94:97], v[78:81]
	s_waitcnt lgkmcnt(1)
	v_mfma_f32_16x16x32_bf16 v[74:77], v[90:93], v[128:131], v[74:77]
	ds_read_b128 v[90:93], v179 offset:24576
	ds_read_b128 v[208:211], v179 offset:25600
	v_mfma_f32_16x16x32_bf16 v[78:81], v[124:127], v[128:131], v[78:81]
	s_waitcnt lgkmcnt(1)
	v_mfma_f32_16x16x32_bf16 v[74:77], v[90:93], v[94:97], v[74:77]
	s_waitcnt lgkmcnt(0)
	v_mfma_f32_16x16x32_bf16 v[78:81], v[208:211], v[94:97], v[78:81]
	ds_read_b128 v[90:93], v179 offset:10240
	ds_read_b128 v[94:97], v179 offset:11264
	ds_read_b128 v[124:127], v205 offset:2368
	s_waitcnt lgkmcnt(2)
	v_mfma_f32_16x16x32_bf16 v[74:77], v[90:93], v[132:135], v[74:77]
	s_waitcnt lgkmcnt(0)
	v_mfma_f32_16x16x32_bf16 v[74:77], v[90:93], v[124:127], v[74:77]
	ds_read_b128 v[90:93], v179 offset:26624
	ds_read_b128 v[128:131], v179 offset:27648
	s_waitcnt lgkmcnt(1)
	v_mfma_f32_16x16x32_bf16 v[208:211], v[90:93], v[132:135], v[74:77]
	v_mfma_f32_16x16x32_bf16 v[74:77], v[94:97], v[132:135], v[78:81]
	s_nop 2
	ds_read_b128 v[78:81], v161 offset:5120
	v_mfma_f32_16x16x32_bf16 v[74:77], v[94:97], v[124:127], v[74:77]
	s_waitcnt lgkmcnt(0)
	global_store_dwordx4 v[172:173], v[78:81], off offset:128
	v_mfma_f32_16x16x32_bf16 v[124:127], v[128:131], v[132:135], v[74:77]
	global_load_dwordx4 v[94:97], v[100:101], off offset:1536 nt
	global_load_dwordx4 v[90:93], v[102:103], off offset:1536 nt
	s_nop 2
	global_load_dwordx4 v[74:77], v[104:105], off offset:1536 nt
	global_load_dwordx4 v[78:81], v[176:177], off offset:1536 nt
	ds_read_b128 v[128:131], v159 offset:768
	v_mov_b32_e32 v136, 0
	s_waitcnt vmcnt(18)
	v_cvt_pk_bf16_f32 v132, v114, v115
	v_mov_b32_e32 v214, 0
	v_cvt_pk_bf16_f32 v133, v116, v117
	s_waitcnt lgkmcnt(0)
	v_pk_mul_f32 v[134:135], v[114:115], v[128:129]
	s_waitcnt vmcnt(17)
	v_pk_mul_f32 v[212:213], v[118:119], v[128:129]
	v_med3_f32 v134, v134, s53, v197
	v_med3_f32 v135, v135, s53, v197
	v_cvt_pk_fp8_f32 v136, v134, v135
	v_pk_mul_f32 v[134:135], v[116:117], v[130:131]
	v_and_b32_e32 v137, 0xffff0000, v133
	v_med3_f32 v134, v134, s53, v197
	v_med3_f32 v135, v135, s53, v197
	v_cvt_pk_fp8_f32 v136, v134, v135 op_sel:[0,0,1]
	v_lshlrev_b32_e32 v134, 16, v132
	v_and_b32_e32 v135, 0xffff0000, v132
	v_pk_add_f32 v[134:135], v[114:115], v[134:135] neg_lo:[0,1] neg_hi:[0,1]
	ds_write_b32 v198, v136 offset:5120
	v_cvt_pk_bf16_f32 v134, v134, v135
	v_med3_f32 v135, v212, s53, v197
	v_med3_f32 v212, v213, s53, v197
	v_cvt_pk_fp8_f32 v214, v135, v212
	v_pk_mul_f32 v[212:213], v[120:121], v[130:131]
	v_lshlrev_b32_e32 v136, 16, v133
	v_med3_f32 v135, v212, s53, v197
	v_med3_f32 v212, v213, s53, v197
	v_cvt_pk_fp8_f32 v214, v135, v212 op_sel:[0,0,1]
	v_pk_add_f32 v[136:137], v[116:117], v[136:137] neg_lo:[0,1] neg_hi:[0,1]
	s_waitcnt vmcnt(16)
; #define LAS __attribute__((address_space(3)))
; #define P7_DMA(s_) do { const unsigned d_ = __builtin_amdgcn_readfirstlane((unsigned)(unsigned long long)(wbuf + ((s_) & 1) * 32768 + F.wave * 1024)); const size_t so_ = (size_t)(s_) * 16384; \
;         P7_G16(rhb + so_, d_); P7_G16(rhb + so_ + 8192, d_ + 8192u); P7_G16(rlb + so_, d_ + 16384u); P7_G16(rlb + so_ + 8192, d_ + 24576u); } while (0)
; DI void p7_router(Frame& F) {
;     ...
; #pragma unroll 2
;         for (int sl = 0; sl < 8; ++sl) {
;             asm volatile("s_waitcnt vmcnt(12) lgkmcnt(0)" ::: "memory");
;             __builtin_amdgcn_s_barrier(); asm volatile("" ::: "memory");
;             if (sl + 1 < 8) P7_DMA(sl + 1);
;             const LAS unsigned char* wsl = wbuf + (sl & 1) * 32768 + lane * 16;
; #pragma unroll
;             for (int u = 0; u < 4; ++u) {
;                 const int ch = 4 * sl + u;
;                 { const int cn = (ch + 3 < 32) ? ch + 3 : 31; P7_LOADX((u + 3) & 3, cn); }
;                 __builtin_amdgcn_sched_barrier(0);
;                 const f32x4 gv = *(const LAS f32x4*)(gl + 64 * ch + 4 * c);
;     ...
;                 P7_ROW(xv[u][0], 0, ss0); P7_ROW(xv[u][1], 1, ss1); P7_ROW(xv[u][2], 2, ss2); P7_ROW(xv[u][3], 3, ss3);
;     ...
;                 *(u32x4*)(hp + 64 * ch) = *(const LAS u32x4*)(fimg + 16 * lane);
; #pragma unroll
;                 for (int kk = 0; kk < 2; ++kk) {
;                     const bf16x8 bh_ = *(const LAS bf16x8*)(himg + c * 144 + (32 * kk + 8 * g4) * 2), bl_ = *(const LAS bf16x8*)(limg + c * 144 + (32 * kk + 8 * g4) * 2);
;                     const bf16x8 ah0 = *(const LAS bf16x8*)(wsl + u * 4096 + (kk * 2) * 1024), ah1 = *(const LAS bf16x8*)(wsl + u * 4096 + (kk * 2 + 1) * 1024);
;                     const bf16x8 al0 = *(const LAS bf16x8*)(wsl + 16384 + u * 4096 + (kk * 2) * 1024), al1 = *(const LAS bf16x8*)(wsl + 16384 + u * 4096 + (kk * 2 + 1) * 1024);
;                     acc0 = __builtin_amdgcn_mfma_f32_16x16x32_bf16(ah0, bh_, acc0, 0, 0, 0); acc0 = __builtin_amdgcn_mfma_f32_16x16x32_bf16(ah0, bl_, acc0, 0, 0, 0); acc0 = __builtin_amdgcn_mfma_f32_16x16x32_bf16(al0, bh_, acc0, 0, 0, 0);
;                     acc1 = __builtin_amdgcn_mfma_f32_16x16x32_bf16(ah1, bh_, acc1, 0, 0, 0); acc1 = __builtin_amdgcn_mfma_f32_16x16x32_bf16(ah1, bl_, acc1, 0, 0, 0); acc1 = __builtin_amdgcn_mfma_f32_16x16x32_bf16(al1, bh_, acc1, 0, 0, 0);
;                 }
	v_pk_mul_f32 v[212:213], v[106:107], v[128:129]
	v_cvt_pk_bf16_f32 v135, v136, v137
	ds_write_b64 v207, v[132:133]
	ds_write_b64 v207, v[134:135] offset:2304
	ds_write_b32 v199, v214 offset:5120
	v_cvt_pk_bf16_f32 v132, v118, v119
	v_lshlrev_b32_e32 v134, 16, v132
	v_and_b32_e32 v135, 0xffff0000, v132
	v_pk_add_f32 v[134:135], v[118:119], v[134:135] neg_lo:[0,1] neg_hi:[0,1]
	v_mov_b32_e32 v214, 0
	v_cvt_pk_bf16_f32 v134, v134, v135
	v_med3_f32 v135, v212, s53, v197
	v_med3_f32 v212, v213, s53, v197
	v_cvt_pk_fp8_f32 v214, v135, v212
	v_pk_mul_f32 v[212:213], v[108:109], v[130:131]
	s_waitcnt vmcnt(15)
	v_pk_mul_f32 v[128:129], v[110:111], v[128:129]
	v_med3_f32 v135, v212, s53, v197
	v_med3_f32 v212, v213, s53, v197
	v_cvt_pk_fp8_f32 v214, v135, v212 op_sel:[0,0,1]
	v_med3_f32 v128, v128, s53, v197
	v_med3_f32 v129, v129, s53, v197
	v_mov_b32_e32 v212, 0
	v_cvt_pk_bf16_f32 v133, v120, v121
	v_cvt_pk_fp8_f32 v212, v128, v129
	v_lshlrev_b32_e32 v136, 16, v133
	v_and_b32_e32 v137, 0xffff0000, v133
	v_pk_add_f32 v[136:137], v[120:121], v[136:137] neg_lo:[0,1] neg_hi:[0,1]
	v_pk_mul_f32 v[128:129], v[112:113], v[130:131]
	v_cvt_pk_bf16_f32 v135, v136, v137
	ds_write_b64 v200, v[132:133]
	ds_write_b64 v200, v[134:135] offset:2304
	ds_write_b32 v201, v214 offset:5120
	v_cvt_pk_bf16_f32 v132, v106, v107
	v_cvt_pk_bf16_f32 v133, v108, v109
	v_med3_f32 v128, v128, s53, v197
	v_med3_f32 v129, v129, s53, v197
	v_lshlrev_b32_e32 v134, 16, v132
	v_and_b32_e32 v135, 0xffff0000, v132
	v_lshlrev_b32_e32 v136, 16, v133
	v_and_b32_e32 v137, 0xffff0000, v133
	v_cvt_pk_fp8_f32 v212, v128, v129 op_sel:[0,0,1]
	v_pk_add_f32 v[134:135], v[106:107], v[134:135] neg_lo:[0,1] neg_hi:[0,1]
	v_pk_add_f32 v[136:137], v[108:109], v[136:137] neg_lo:[0,1] neg_hi:[0,1]
	v_cvt_pk_bf16_f32 v128, v110, v111
	v_cvt_pk_bf16_f32 v129, v112, v113
	v_cvt_pk_bf16_f32 v134, v134, v135
	v_cvt_pk_bf16_f32 v135, v136, v137
	ds_write_b64 v202, v[132:133]
	ds_write_b64 v202, v[134:135] offset:2304
	ds_write_b32 v203, v212 offset:5120
	v_lshlrev_b32_e32 v130, 16, v128
	v_and_b32_e32 v131, 0xffff0000, v128
	v_lshlrev_b32_e32 v132, 16, v129
	v_and_b32_e32 v133, 0xffff0000, v129
	v_pk_add_f32 v[130:131], v[110:111], v[130:131] neg_lo:[0,1] neg_hi:[0,1]
	v_pk_add_f32 v[132:133], v[112:113], v[132:133] neg_lo:[0,1] neg_hi:[0,1]
	v_cvt_pk_bf16_f32 v130, v130, v131
	v_cvt_pk_bf16_f32 v131, v132, v133
	ds_write_b64 v204, v[128:129]
	ds_write_b64 v204, v[130:131] offset:2304
	ds_read_b128 v[128:131], v179 offset:12288
	ds_read_b128 v[132:135], v205
	ds_read_b128 v[212:215], v179 offset:13312
	s_waitcnt lgkmcnt(1)
	v_mfma_f32_16x16x32_bf16 v[208:211], v[128:131], v[132:135], v[208:211]
	ds_read_b128 v[216:219], v205 offset:2304
	ds_read_b128 v[220:223], v205 offset:64
	s_waitcnt lgkmcnt(2)
	v_mfma_f32_16x16x32_bf16 v[124:127], v[212:215], v[132:135], v[124:127]
	s_waitcnt lgkmcnt(1)
	v_mfma_f32_16x16x32_bf16 v[128:131], v[128:131], v[216:219], v[208:211]
	s_nop 2
	ds_read_b128 v[208:211], v179 offset:28672
	ds_read_b128 v[226:229], v179 offset:29696
	v_mfma_f32_16x16x32_bf16 v[124:127], v[212:215], v[216:219], v[124:127]
	s_waitcnt lgkmcnt(1)
	v_mfma_f32_16x16x32_bf16 v[128:131], v[208:211], v[132:135], v[128:131]
	s_waitcnt lgkmcnt(0)
	v_mfma_f32_16x16x32_bf16 v[124:127], v[226:229], v[132:135], v[124:127]
	ds_read_b128 v[132:135], v179 offset:14336
	ds_read_b128 v[208:211], v179 offset:15360
	ds_read_b128 v[212:215], v205 offset:2368
	s_waitcnt lgkmcnt(2)
	v_mfma_f32_16x16x32_bf16 v[128:131], v[132:135], v[220:223], v[128:131]
	s_waitcnt lgkmcnt(0)
	v_mfma_f32_16x16x32_bf16 v[128:131], v[132:135], v[212:215], v[128:131]
	ds_read_b128 v[132:135], v179 offset:30720
	ds_read_b128 v[216:219], v179 offset:31744
	v_mfma_f32_16x16x32_bf16 v[124:127], v[208:211], v[220:223], v[124:127]
	s_waitcnt lgkmcnt(1)
	v_mfma_f32_16x16x32_bf16 v[134:137], v[132:135], v[220:223], v[128:131]
	s_nop 2
	ds_read_b128 v[128:131], v161 offset:5120
	v_mfma_f32_16x16x32_bf16 v[124:127], v[208:211], v[212:215], v[124:127]
	s_waitcnt lgkmcnt(0)
	global_store_dwordx4 v[172:173], v[128:131], off offset:192
	s_nop 1
	v_mfma_f32_16x16x32_bf16 v[130:133], v[216:219], v[220:223], v[124:127]
	s_waitcnt vmcnt(12) lgkmcnt(0)
	s_barrier
	s_cmpk_eq_i32 s8, 0x1800
	s_cbranch_scc1 .LBB0_859
	v_lshl_add_u64 v[124:125], v[122:123], 0, s[28:29]
	s_mov_b32 m0, s46
	global_load_lds_dwordx4 v[124:125], off
	v_lshl_add_u64 v[124:125], v[122:123], 0, s[30:31]
	s_mov_b32 m0, s0
	global_load_lds_dwordx4 v[124:125], off
	v_lshl_add_u64 v[124:125], v[122:123], 0, s[34:35]
	s_mov_b32 m0, s1
	global_load_lds_dwordx4 v[124:125], off
	v_lshl_add_u64 v[122:123], v[122:123], 0, s[36:37]
	s_mov_b32 m0, s42
	global_load_lds_dwordx4 v[122:123], off
	s_branch .LBB0_859

; DI void p7_router(Frame& F) {
;     ...
;         const float rs = lr[c];
;         float v[8];
; #pragma unroll
;         for (int j = 0; j < 4; ++j) { v[j] = acc0[j] * rs + F.router_b[4 * g4 + j]; v[4 + j] = acc1[j] * rs + F.router_b[16 + 4 * g4 + j]; }
;         float sv[4]; int si[4];
; #pragma unroll
;         for (int k = 0; k < 4; ++k) {
;             float bv = v[0]; int bi = 4 * g4;
; #pragma unroll
;             for (int j = 1; j < 8; ++j) { const int ce = (j < 4) ? (4 * g4 + j) : (16 + 4 * g4 + j - 4); if (v[j] > bv) { bv = v[j]; bi = ce; } }
;             { const float ov = __shfl_xor(bv, 16); const int oi = __shfl_xor(bi, 16); if (ov > bv || (ov == bv && oi < bi)) { bv = ov; bi = oi; } }
;             { const float ov = __shfl_xor(bv, 32); const int oi = __shfl_xor(bi, 32); if (ov > bv || (ov == bv && oi < bi)) { bv = ov; bi = oi; } }
.LBB0_864:
	s_or_b64 exec, exec, s[0:1]
	s_waitcnt lgkmcnt(2)
	global_load_dwordx4 v[2:5], v[156:157], off offset:64 nt
	s_waitcnt lgkmcnt(0)
	global_load_dwordx4 v[6:9], v[156:157], off nt
	ds_read_b32 v14, v196 offset:4608
	v_xor_b32_e32 v10, 16, v193
	v_cmp_lt_i32_e32 vcc, v10, v11
	s_waitcnt vmcnt(1) lgkmcnt(0)
	v_fma_f32 v12, v38, v14, v2
	s_waitcnt vmcnt(0)
	v_pk_fma_f32 v[6:7], v[34:35], v[14:15], v[6:7] op_sel_hi:[1,0,1]
	v_cndmask_b32_e32 v10, v193, v10, vcc
	v_cmp_gt_f32_e32 vcc, v7, v6
	v_fma_f32 v13, v36, v14, v8
	v_fmac_f32_e32 v9, v37, v14
	v_cndmask_b32_e32 v2, v6, v7, vcc
	v_cndmask_b32_e32 v8, v152, v1, vcc
	v_cmp_gt_f32_e32 vcc, v13, v2
	v_fma_f32 v3, v39, v14, v3
	v_fma_f32 v4, v40, v14, v4
	v_cndmask_b32_e32 v2, v2, v13, vcc
	v_cndmask_b32_e32 v8, v8, v187, vcc
	v_cmp_gt_f32_e32 vcc, v9, v2
	v_fmac_f32_e32 v5, v41, v14
	v_lshlrev_b32_e32 v10, 2, v10
	v_cndmask_b32_e32 v2, v2, v9, vcc
	v_cndmask_b32_e32 v8, v8, v188, vcc
	v_cmp_gt_f32_e32 vcc, v12, v2
	s_nop 1
	v_cndmask_b32_e32 v2, v2, v12, vcc
	v_cndmask_b32_e32 v8, v8, v186, vcc
	v_cmp_gt_f32_e32 vcc, v3, v2
	s_nop 1
	v_cndmask_b32_e32 v2, v2, v3, vcc
	v_cndmask_b32_e32 v8, v8, v189, vcc
	v_cmp_gt_f32_e32 vcc, v4, v2
	s_nop 1
	v_cndmask_b32_e32 v2, v2, v4, vcc
	v_cndmask_b32_e32 v15, v8, v190, vcc
	v_cmp_gt_f32_e32 vcc, v5, v2
	s_nop 1
	v_cndmask_b32_e32 v8, v2, v5, vcc
	ds_bpermute_b32 v14, v10, v8
	v_cndmask_b32_e32 v2, v15, v191, vcc
	ds_bpermute_b32 v15, v10, v2
	s_waitcnt lgkmcnt(1)
	v_cmp_lt_f32_e64 s[0:1], v8, v14
	v_cmp_nlt_f32_e32 vcc, v8, v14
	s_and_saveexec_b64 s[42:43], vcc
	s_cbranch_execz .LBB0_866
	v_cmp_eq_f32_e32 vcc, v8, v14
	s_waitcnt lgkmcnt(0)
	v_cmp_lt_i32_e64 s[8:9], v15, v2
	s_and_b64 s[8:9], vcc, s[8:9]
	s_andn2_b64 s[0:1], s[0:1], exec
	s_and_b64 s[8:9], s[8:9], exec
	s_or_b64 s[0:1], s[0:1], s[8:9]

; DI void p11_combine(Frame& F) {
;     ...
;     int4 ps = *(const int4*)(POS + (size_t)(gw < NTOK ? gw : 0) * 4);
; #pragma unroll 1
;     for (int tok = gw; tok < NTOK; tok += NGW) {
;         const int tn = tok + NGW < NTOK ? tok + NGW : tok;
;         const int4 psn = *(const int4*)(POS + (size_t)tn * 4);
;         f32x4* orow = (f32x4*)(F.out + (size_t)tok * DM) + F.lane;
;         const unsigned* y0 = (const unsigned*)(YB + (size_t)ps.x * DM) + F.lane; const unsigned* y1 = (const unsigned*)(YB + (size_t)ps.y * DM) + F.lane;
;         const unsigned* y2 = (const unsigned*)(YB + (size_t)ps.z * DM) + F.lane; const unsigned* y3 = (const unsigned*)(YB + (size_t)ps.w * DM) + F.lane;
;         f32x4 v[8]; unsigned qa[8], qb[8], qc[8], qd[8];
; #pragma unroll
;         for (int j = 0; j < 8; ++j) { v[j] = orow[64 * j]; qa[j] = y0[64 * j]; qb[j] = y1[64 * j]; qc[j] = y2[64 * j]; qd[j] = y3[64 * j]; }
.LBB0_1225:
	s_add_i32 s5, s10, s4
	s_cmp_lt_i32 s5, 0x8000
	s_cselect_b64 s[14:15], -1, 0
	s_and_b64 vcc, s[14:15], exec
	s_cselect_b32 s10, s5, s10
	s_ashr_i32 s11, s10, 31
	s_lshl_b64 s[10:11], s[10:11], 4
	s_add_u32 s10, s9, s10
	s_addc_u32 s11, s12, s11
	global_load_dwordx4 v[38:41], v33, s[10:11]
	s_ashr_i32 s11, s0, 31
	s_mov_b32 s10, s0
	s_lshl_b64 s[10:11], s[10:11], 11
	v_lshl_add_u64 v[42:43], v[34:35], 0, s[10:11]
	s_ashr_i32 s11, s1, 31
	s_mov_b32 s10, s1
	s_lshl_b64 s[0:1], s[10:11], 11
	v_lshl_add_u64 v[44:45], v[34:35], 0, s[0:1]
	s_ashr_i32 s1, s2, 31
	s_mov_b32 s0, s2
	s_lshl_b64 s[0:1], s[0:1], 11
	v_lshl_add_u64 v[46:47], v[34:35], 0, s[0:1]
	s_ashr_i32 s1, s3, 31
	s_mov_b32 s0, s3
	s_lshl_b64 s[0:1], s[0:1], 11
	v_lshl_add_u64 v[48:49], v[34:35], 0, s[0:1]
	global_load_dwordx4 v[0:3], v[36:37], off offset:-4096 nt
	global_load_dwordx4 v[4:7], v[36:37], off offset:-3072 nt
	s_waitcnt lgkmcnt(0)
	global_load_dwordx4 v[8:11], v[36:37], off offset:-2048 nt
	global_load_dwordx4 v[12:15], v[36:37], off offset:-1024 nt
	global_load_dwordx4 v[16:19], v[36:37], off nt
	global_load_dwordx4 v[20:23], v[36:37], off offset:1024 nt
	global_load_dwordx4 v[24:27], v[36:37], off offset:2048 nt
	global_load_dwordx4 v[28:31], v[36:37], off offset:3072 nt
	global_load_dword v32, v[42:43], off nt
	global_load_dword v56, v[42:43], off offset:256 nt
	global_load_dword v72, v[42:43], off offset:512 nt
	global_load_dword v88, v[42:43], off offset:768 nt
	global_load_dword v104, v[42:43], off offset:1024 nt
	global_load_dword v120, v[42:43], off offset:1280 nt
	global_load_dword v136, v[42:43], off offset:1536 nt
	global_load_dword v152, v[42:43], off offset:1792 nt
	global_load_dword v50, v[44:45], off nt
	global_load_dword v60, v[44:45], off offset:256 nt
	global_load_dword v76, v[44:45], off offset:512 nt
	global_load_dword v92, v[44:45], off offset:768 nt
	global_load_dword v108, v[44:45], off offset:1024 nt
	global_load_dword v124, v[44:45], off offset:1280 nt
	global_load_dword v140, v[44:45], off offset:1536 nt
	global_load_dword v156, v[44:45], off offset:1792 nt
	global_load_dword v51, v[46:47], off nt
	global_load_dword v64, v[46:47], off offset:256 nt
	global_load_dword v80, v[46:47], off offset:512 nt
	global_load_dword v96, v[46:47], off offset:768 nt
	global_load_dword v112, v[46:47], off offset:1024 nt
	global_load_dword v128, v[46:47], off offset:1280 nt
	global_load_dword v144, v[46:47], off offset:1536 nt
	global_load_dword v160, v[46:47], off offset:1792 nt
	global_load_dword v52, v[48:49], off nt
	global_load_dword v68, v[48:49], off offset:256 nt
	global_load_dword v84, v[48:49], off offset:512 nt
	global_load_dword v100, v[48:49], off offset:768 nt
	global_load_dword v116, v[48:49], off offset:1024 nt
	global_load_dword v132, v[48:49], off offset:1280 nt
	global_load_dword v148, v[48:49], off offset:1536 nt
	global_load_dword v164, v[48:49], off offset:1792 nt
	s_waitcnt vmcnt(40)
	v_readfirstlane_b32 s0, v38
	v_readfirstlane_b32 s1, v39
	v_readfirstlane_b32 s2, v40
	v_readfirstlane_b32 s3, v41
	s_waitcnt vmcnt(31)
	v_cvt_pk_f32_fp8_e32 v[38:39], v32
	v_cvt_pk_f32_fp8_sdwa v[40:41], v32 src0_sel:WORD_1
	s_waitcnt vmcnt(23)
	v_cvt_pk_f32_fp8_e32 v[42:43], v50
	v_cvt_pk_f32_fp8_sdwa v[44:45], v50 src0_sel:WORD_1
	s_waitcnt vmcnt(15)
	v_cvt_pk_f32_fp8_e32 v[46:47], v51
	v_cvt_pk_f32_fp8_sdwa v[48:49], v51 src0_sel:WORD_1
	v_cvt_pk_f32_fp8_e32 v[54:55], v56
	v_cvt_pk_f32_fp8_sdwa v[56:57], v56 src0_sel:WORD_1
	v_cvt_pk_f32_fp8_e32 v[58:59], v60
	v_cvt_pk_f32_fp8_sdwa v[60:61], v60 src0_sel:WORD_1
	v_cvt_pk_f32_fp8_e32 v[70:71], v72
	v_cvt_pk_f32_fp8_sdwa v[72:73], v72 src0_sel:WORD_1
	v_cvt_pk_f32_fp8_e32 v[74:75], v76
	v_cvt_pk_f32_fp8_sdwa v[76:77], v76 src0_sel:WORD_1
	v_cvt_pk_f32_fp8_e32 v[86:87], v88
	v_cvt_pk_f32_fp8_sdwa v[88:89], v88 src0_sel:WORD_1
	v_cvt_pk_f32_fp8_e32 v[90:91], v92
	v_cvt_pk_f32_fp8_sdwa v[92:93], v92 src0_sel:WORD_1
	v_cvt_pk_f32_fp8_e32 v[102:103], v104
	v_cvt_pk_f32_fp8_sdwa v[104:105], v104 src0_sel:WORD_1
	v_cvt_pk_f32_fp8_e32 v[106:107], v108
	v_cvt_pk_f32_fp8_sdwa v[108:109], v108 src0_sel:WORD_1
	v_cvt_pk_f32_fp8_e32 v[118:119], v120
	v_cvt_pk_f32_fp8_sdwa v[120:121], v120 src0_sel:WORD_1
	v_cvt_pk_f32_fp8_e32 v[122:123], v124
	v_cvt_pk_f32_fp8_sdwa v[124:125], v124 src0_sel:WORD_1
	v_cvt_pk_f32_fp8_e32 v[134:135], v136
	v_cvt_pk_f32_fp8_sdwa v[136:137], v136 src0_sel:WORD_1
	v_cvt_pk_f32_fp8_e32 v[138:139], v140
	v_cvt_pk_f32_fp8_sdwa v[140:141], v140 src0_sel:WORD_1
	v_cvt_pk_f32_fp8_e32 v[150:151], v152
	v_cvt_pk_f32_fp8_sdwa v[152:153], v152 src0_sel:WORD_1
	v_cvt_pk_f32_fp8_e32 v[154:155], v156
	v_cvt_pk_f32_fp8_sdwa v[156:157], v156 src0_sel:WORD_1
	s_waitcnt vmcnt(7)
; DI void p11_combine(Frame& F) {
;     ...
;         __builtin_amdgcn_sched_barrier(0);
; #pragma unroll
;         for (int j = 0; j < 8; ++j) { const unsigned a = qa[j], bq = qb[j], cq = qc[j], dq = qd[j];
;             const f32x2 a0 = __builtin_amdgcn_cvt_pk_f32_fp8((int)a, false), a1 = __builtin_amdgcn_cvt_pk_f32_fp8((int)a, true), b0 = __builtin_amdgcn_cvt_pk_f32_fp8((int)bq, false), b1 = __builtin_amdgcn_cvt_pk_f32_fp8((int)bq, true);
;             const f32x2 c0 = __builtin_amdgcn_cvt_pk_f32_fp8((int)cq, false), c1 = __builtin_amdgcn_cvt_pk_f32_fp8((int)cq, true), d0 = __builtin_amdgcn_cvt_pk_f32_fp8((int)dq, false), d1 = __builtin_amdgcn_cvt_pk_f32_fp8((int)dq, true);
;             f32x4 vv = v[j];
;             vv[0] += (((a0[0] + b0[0]) + c0[0]) + d0[0]) * 0.0625f; vv[1] += (((a0[1] + b0[1]) + c0[1]) + d0[1]) * 0.0625f;
;             vv[2] += (((a1[0] + b1[0]) + c1[0]) + d1[0]) * 0.0625f; vv[3] += (((a1[1] + b1[1]) + c1[1]) + d1[1]) * 0.0625f; orow[64 * j] = vv; }
;         ps = psn;
;     }
	v_cvt_pk_f32_fp8_e32 v[50:51], v52
	v_cvt_pk_f32_fp8_sdwa v[52:53], v52 src0_sel:WORD_1
	v_cvt_pk_f32_fp8_e32 v[62:63], v64
	v_cvt_pk_f32_fp8_sdwa v[64:65], v64 src0_sel:WORD_1
	v_cvt_pk_f32_fp8_e32 v[78:79], v80
	v_cvt_pk_f32_fp8_sdwa v[80:81], v80 src0_sel:WORD_1
	v_cvt_pk_f32_fp8_e32 v[94:95], v96
	v_cvt_pk_f32_fp8_sdwa v[96:97], v96 src0_sel:WORD_1
	v_cvt_pk_f32_fp8_e32 v[110:111], v112
	v_cvt_pk_f32_fp8_sdwa v[112:113], v112 src0_sel:WORD_1
	v_cvt_pk_f32_fp8_e32 v[126:127], v128
	v_cvt_pk_f32_fp8_sdwa v[128:129], v128 src0_sel:WORD_1
	v_cvt_pk_f32_fp8_e32 v[142:143], v144
	v_cvt_pk_f32_fp8_sdwa v[144:145], v144 src0_sel:WORD_1
	v_cvt_pk_f32_fp8_e32 v[158:159], v160
	v_cvt_pk_f32_fp8_sdwa v[160:161], v160 src0_sel:WORD_1
	s_waitcnt vmcnt(6)
	v_cvt_pk_f32_fp8_e32 v[66:67], v68
	v_cvt_pk_f32_fp8_sdwa v[68:69], v68 src0_sel:WORD_1
	s_waitcnt vmcnt(5)
	v_cvt_pk_f32_fp8_e32 v[82:83], v84
	v_cvt_pk_f32_fp8_sdwa v[84:85], v84 src0_sel:WORD_1
	s_waitcnt vmcnt(4)
	v_cvt_pk_f32_fp8_e32 v[98:99], v100
	v_cvt_pk_f32_fp8_sdwa v[100:101], v100 src0_sel:WORD_1
	s_waitcnt vmcnt(3)
	v_cvt_pk_f32_fp8_e32 v[114:115], v116
	v_cvt_pk_f32_fp8_sdwa v[116:117], v116 src0_sel:WORD_1
	s_waitcnt vmcnt(2)
	v_cvt_pk_f32_fp8_e32 v[130:131], v132
	v_cvt_pk_f32_fp8_sdwa v[132:133], v132 src0_sel:WORD_1
	s_waitcnt vmcnt(1)
	v_cvt_pk_f32_fp8_e32 v[146:147], v148
	v_cvt_pk_f32_fp8_sdwa v[148:149], v148 src0_sel:WORD_1
	s_waitcnt vmcnt(0)
	v_cvt_pk_f32_fp8_e32 v[162:163], v164
	v_cvt_pk_f32_fp8_sdwa v[164:165], v164 src0_sel:WORD_1
	v_pk_add_f32 v[38:39], v[38:39], v[42:43]
	v_pk_add_f32 v[40:41], v[40:41], v[44:45]
	v_pk_add_f32 v[42:43], v[54:55], v[58:59]
	v_pk_add_f32 v[44:45], v[56:57], v[60:61]
	v_pk_add_f32 v[54:55], v[70:71], v[74:75]
	v_pk_add_f32 v[56:57], v[72:73], v[76:77]
	v_pk_add_f32 v[58:59], v[86:87], v[90:91]
	v_pk_add_f32 v[60:61], v[88:89], v[92:93]
	v_pk_add_f32 v[70:71], v[102:103], v[106:107]
	v_pk_add_f32 v[72:73], v[104:105], v[108:109]
	v_pk_add_f32 v[74:75], v[118:119], v[122:123]
	v_pk_add_f32 v[76:77], v[120:121], v[124:125]
	v_pk_add_f32 v[86:87], v[134:135], v[138:139]
	v_pk_add_f32 v[88:89], v[136:137], v[140:141]
	v_pk_add_f32 v[90:91], v[150:151], v[154:155]
	v_pk_add_f32 v[92:93], v[152:153], v[156:157]
	v_pk_add_f32 v[38:39], v[38:39], v[46:47]
	v_pk_add_f32 v[40:41], v[40:41], v[48:49]
	v_pk_add_f32 v[42:43], v[42:43], v[62:63]
	v_pk_add_f32 v[44:45], v[44:45], v[64:65]
	v_pk_add_f32 v[46:47], v[54:55], v[78:79]
	v_pk_add_f32 v[48:49], v[56:57], v[80:81]
	v_pk_add_f32 v[54:55], v[58:59], v[94:95]
	v_pk_add_f32 v[56:57], v[60:61], v[96:97]
	v_pk_add_f32 v[58:59], v[70:71], v[110:111]
	v_pk_add_f32 v[60:61], v[72:73], v[112:113]
	v_pk_add_f32 v[62:63], v[74:75], v[126:127]
	v_pk_add_f32 v[64:65], v[76:77], v[128:129]
	v_pk_add_f32 v[70:71], v[86:87], v[142:143]
	v_pk_add_f32 v[72:73], v[88:89], v[144:145]
	v_pk_add_f32 v[74:75], v[90:91], v[158:159]
	v_pk_add_f32 v[76:77], v[92:93], v[160:161]
	v_pk_add_f32 v[38:39], v[38:39], v[50:51]
	v_pk_add_f32 v[40:41], v[40:41], v[52:53]
	v_pk_add_f32 v[42:43], v[42:43], v[66:67]
	v_pk_add_f32 v[44:45], v[44:45], v[68:69]
	v_pk_add_f32 v[46:47], v[46:47], v[82:83]
	v_pk_add_f32 v[48:49], v[48:49], v[84:85]
	v_pk_add_f32 v[50:51], v[54:55], v[98:99]
	v_pk_add_f32 v[52:53], v[56:57], v[100:101]
	v_pk_add_f32 v[54:55], v[58:59], v[114:115]
	v_pk_add_f32 v[56:57], v[60:61], v[116:117]
	v_pk_add_f32 v[58:59], v[62:63], v[130:131]
	v_pk_add_f32 v[60:61], v[64:65], v[132:133]
	v_pk_add_f32 v[62:63], v[70:71], v[146:147]
	v_pk_add_f32 v[64:65], v[72:73], v[148:149]
	v_pk_add_f32 v[66:67], v[74:75], v[162:163]
	v_pk_add_f32 v[68:69], v[76:77], v[164:165]
	v_pk_fma_f32 v[2:3], v[40:41], s[8:9], v[2:3] op_sel_hi:[1,0,1]
	v_pk_fma_f32 v[0:1], v[38:39], s[8:9], v[0:1] op_sel_hi:[1,0,1]
	s_mov_b32 s10, s5
	v_pk_fma_f32 v[6:7], v[44:45], s[8:9], v[6:7] op_sel_hi:[1,0,1]
	v_pk_fma_f32 v[4:5], v[42:43], s[8:9], v[4:5] op_sel_hi:[1,0,1]
	v_pk_fma_f32 v[10:11], v[48:49], s[8:9], v[10:11] op_sel_hi:[1,0,1]
	v_pk_fma_f32 v[8:9], v[46:47], s[8:9], v[8:9] op_sel_hi:[1,0,1]
	v_pk_fma_f32 v[14:15], v[52:53], s[8:9], v[14:15] op_sel_hi:[1,0,1]
	v_pk_fma_f32 v[12:13], v[50:51], s[8:9], v[12:13] op_sel_hi:[1,0,1]
	v_pk_fma_f32 v[18:19], v[56:57], s[8:9], v[18:19] op_sel_hi:[1,0,1]
	v_pk_fma_f32 v[16:17], v[54:55], s[8:9], v[16:17] op_sel_hi:[1,0,1]
	v_pk_fma_f32 v[22:23], v[60:61], s[8:9], v[22:23] op_sel_hi:[1,0,1]
	v_pk_fma_f32 v[20:21], v[58:59], s[8:9], v[20:21] op_sel_hi:[1,0,1]
	v_pk_fma_f32 v[26:27], v[64:65], s[8:9], v[26:27] op_sel_hi:[1,0,1]
	v_pk_fma_f32 v[24:25], v[62:63], s[8:9], v[24:25] op_sel_hi:[1,0,1]
	v_pk_fma_f32 v[30:31], v[68:69], s[8:9], v[30:31] op_sel_hi:[1,0,1]
	v_pk_fma_f32 v[28:29], v[66:67], s[8:9], v[28:29] op_sel_hi:[1,0,1]
	global_store_dwordx4 v[36:37], v[0:3], off offset:-4096 nt
	global_store_dwordx4 v[36:37], v[4:7], off offset:-3072 nt
	global_store_dwordx4 v[36:37], v[8:11], off offset:-2048 nt
	global_store_dwordx4 v[36:37], v[12:15], off offset:-1024 nt
	global_store_dwordx4 v[36:37], v[16:19], off nt
	global_store_dwordx4 v[36:37], v[20:23], off offset:1024 nt
	global_store_dwordx4 v[36:37], v[24:27], off offset:2048 nt
	global_store_dwordx4 v[36:37], v[28:31], off offset:3072 nt
	v_lshl_add_u64 v[36:37], v[36:37], 0, s[6:7]
	s_cbranch_vccnz .LBB0_1225
